# defer 8192 layer-1 weight-conversion items from prologue to 32 helper WGs running during layer-0 MoE GEMM phases (224 workers)
# speedup vs baseline: 1.0132x; 1.0132x over previous
;     ...
;             const int l = it / C_L; int r = it % C_L;
;             const float* W; unsigned char* WT; int ldw, K, k0, n0, scol, esz = 2;
;             if (r < C_IN) { const int kb = r / 188, nb = r % 188; n0 = 64 * nb; k0 = 64 * kb; ldw = NIN; K = D; W = a.w_in + (size_t)l * D * NIN;
;                 if (n0 < 3072) { d.rope = 1; scol = (n0 >> 7) * 128 + 32 * ((n0 >> 6) & 1) + 64 * (q4 >> 3) + 4 * (q4 & 7); }
;                 else if (n0 < 7680) scol = n0 + 4 * q4;
;                 else if (n0 < 11776) scol = n0 + 16 + 4 * q4;
;                 else if (n0 == 11776) { scol = (q4 < 4) ? 7680 + 4 * q4 : 0; d.zero = (q4 < 4) ? 0 : 1; }
;                 else { scol = 0; d.zero = 1; }
;     ...
;                 d.f8 = 1; esz = 1; WT = ws + WS_WIN + (size_t)l * NP * D;
;     ...
;                 WT = ws + WS_WIN + (size_t)l * NP * D * 2;
;     ...
;             } else if ((r -= C_IN) < C_OA) { const int kb = r / 32, nb = r % 32; n0 = 64 * nb; k0 = 64 * kb; ldw = D; K = 512; scol = n0 + 4 * q4; W = a.w_out_a + (size_t)l * 512 * D; WT = ws + WS_WOA + (size_t)l * D * 512 * (MIX_F8 ? 1 : 2); if (MIX_F8) { d.f8 = 1; esz = 1; }
;                 if (BR_FUSE) { K = 1536; WT = ws + WS_WOA + (size_t)l * D * 1536 + 1024; }
;             } else if ((r -= C_OA) < C_OB) { const int kb = r / 32, nb = r % 32; n0 = 64 * nb; k0 = 64 * kb; ldw = D; K = 1024; scol = n0 + 4 * q4; W = a.w_out_b + (size_t)l * 1024 * D; WT = ws + WS_WOB + (size_t)l * D * 1024 * (MIX_F8 ? 1 : 2); if (MIX_F8) { d.f8 = 1; esz = 1; }
;                 if (BR_FUSE) { K = 1536; WT = ws + WS_WOA + (size_t)l * D * 1536; }
;             } else if ((r -= C_OB) < C_O) { const int kb = r / 32, nb = r % 32; n0 = 64 * nb; k0 = 64 * kb; ldw = D; K = D; scol = n0 + 4 * q4; W = a.w_out + (size_t)l * D * D; WT = ws + WS_WO + (size_t)l * D * D * (MIX_F8 ? 1 : 2); if (MIX_F8) { d.f8 = 1; esz = 1; }
;     ...
;         while (it < NIT) {
;             const int itB = it + NGW;
;             if (itB < NIT) { dB = decode(NIT - 1 - itB); tr_load(dB, vB); }
;             tr_finish(dA, vA, scr, lane);
;             if (itB >= NIT) break;
;             const int itA = itB + NGW;
;             if (itA < NIT) { dA = decode(NIT - 1 - itA); tr_load(dA, vA); }
;             tr_finish(dB, vB, scr, lane);
;             it = itA;
.LBB0_72:
	s_cmp_gt_i32 s42, 0xfcff
	s_cbranch_scc1 .LBB0_70
	s_add_i32 s44, s42, s48
	s_cmpk_lt_i32 s44, 0x2800
	s_cbranch_scc0 .Lps_1
	s_add_i32 s44, s44, 0x2000
.Lps_1:
	s_cmp_lt_i32 s44, 0xfd00
	s_cselect_b64 s[20:21], -1, 0
	s_cmp_gt_i32 s44, 0xfcff
	s_cselect_b64 s[12:13], -1, 0
	s_and_b64 vcc, exec, s[12:13]
	s_cbranch_vccnz .LBB0_106
	s_sub_i32 s3, 0xfcff, s44
	s_mul_hi_u32 s0, s3, 0x81848da9
	s_lshr_b32 s0, s0, 14
	s_mul_i32 s14, s0, 0x7e80
	s_sub_i32 s45, s3, s14
	s_cmpk_gt_u32 s45, 0x177f
	s_cbranch_scc0 .LBB0_81
	s_cmpk_gt_u32 s45, 0x187f
	s_cbranch_scc0 .LBB0_83
	s_cmpk_gt_u32 s45, 0x1a7f
	s_cbranch_scc0 .LBB0_84
	s_cmpk_gt_u32 s45, 0x1e7f
	s_cbranch_scc0 .LBB0_85
	s_lshl_b32 s24, s45, 6
	s_cmpk_gt_u32 s45, 0x5e7f
	s_cbranch_scc0 .LBB0_121
	s_add_i32 s14, s45, 0xffffa180
	s_lshr_b32 s18, s14, 9
	s_lshl_b32 s14, s14, 1
	s_and_b32 s49, s14, 0x3c0
	s_load_dwordx2 s[14:15], s[8:9], 0x88
	s_lshl_b32 s19, s0, 4
	s_add_i32 s22, s18, s19
	s_mov_b32 s23, s1
	s_and_b32 s3, s24, 0x7c0
	s_lshl_b64 s[18:19], s[22:23], 23
	s_waitcnt lgkmcnt(0)
	s_add_u32 s18, s14, s18
	s_addc_u32 s19, s15, s19
	s_lshl_b64 s[14:15], s[22:23], 21
	s_add_u32 s22, s28, s14
	v_or_b32_e32 v0, s3, v136
	s_addc_u32 s23, s29, s15
	s_cbranch_execz .LBB0_122
	s_movk_i32 s14, 0x400
	s_mov_b64 s[24:25], 0x800
	s_cbranch_execz .LBB0_86
	s_branch .LBB0_87

; #define LAS __attribute__((address_space(3)))
; #define GAS __attribute__((address_space(1)))
; #define LDS_WAIT() asm volatile("s_waitcnt lgkmcnt(0)" ::: "memory")
; __device__ __forceinline__ unsigned pk_fp8x4(float a, float b, float c, float d) { int p = __builtin_amdgcn_cvt_pk_fp8_f32(sat8(a), sat8(b), 0, false); p = __builtin_amdgcn_cvt_pk_fp8_f32(sat8(c), sat8(d), p, true); return (unsigned)p; }
; __device__ __forceinline__ void tr_finish(const TrDesc& d, f32x4 (&v)[16], LAS float* scr, int lane) {
;     ...
;     { LAS float* rp = scr + kk * 65 + d0;
; #pragma unroll
;         for (int i = 0; i < 16; ++i) { rp[4 * i * 65] = v[i][0]; rp[4 * i * 65 + ds] = v[i][1]; rp[4 * i * 65 + 2 * ds] = v[i][2]; rp[4 * i * 65 + 3 * ds] = v[i][3]; } }
;     LDS_WAIT(); asm volatile("" ::: "memory");
;     if (d.f8) {
;         const int c = lane & 3, nl = lane >> 2; const LAS float* sp = scr + (16 * c) * 65 + nl; unsigned char* dp = d.dst + (size_t)nl * d.K + 16 * c;
; #pragma unroll
;         for (int j = 0; j < 4; ++j) { u32x4 o;
;             o.x = pk_fp8x4(sp[0 * 65 + 16 * j] * 32.0f, sp[1 * 65 + 16 * j] * 32.0f, sp[2 * 65 + 16 * j] * 32.0f, sp[3 * 65 + 16 * j] * 32.0f);
;             o.y = pk_fp8x4(sp[4 * 65 + 16 * j] * 32.0f, sp[5 * 65 + 16 * j] * 32.0f, sp[6 * 65 + 16 * j] * 32.0f, sp[7 * 65 + 16 * j] * 32.0f);
;             o.z = pk_fp8x4(sp[8 * 65 + 16 * j] * 32.0f, sp[9 * 65 + 16 * j] * 32.0f, sp[10 * 65 + 16 * j] * 32.0f, sp[11 * 65 + 16 * j] * 32.0f);
;             o.w = pk_fp8x4(sp[12 * 65 + 16 * j] * 32.0f, sp[13 * 65 + 16 * j] * 32.0f, sp[14 * 65 + 16 * j] * 32.0f, sp[15 * 65 + 16 * j] * 32.0f);
;             *(GAS u32x4*)(dp + (size_t)(16 * j) * d.K) = o; }
.LBB0_108:
	s_or_b64 exec, exec, s[22:23]
	s_cmp_eq_u32 s43, 0
	s_cselect_b64 vcc, -1, 0
	s_cmp_lg_u32 s43, 0
	s_cselect_b64 s[22:23], -1, 0
	v_cndmask_b32_e64 v2, 0, 1, s[22:23]
	s_and_b64 s[22:23], s[22:23], exec
	v_cndmask_b32_e32 v0, v140, v136, vcc
	s_cselect_b32 s0, 2, 1
	v_lshl_add_u32 v0, v0, 2, v141
	s_lshl_b32 s3, s0, 2
	v_add_u32_e32 v3, s3, v0
	v_lshlrev_b32_e64 v2, v2, 3
	s_waitcnt vmcnt(15)
	ds_write_b32 v3, v5
	v_lshl_add_u32 v3, s0, 3, v0
	v_lshl_add_u32 v2, v2, 2, v0
	v_subrev_u32_e32 v146, s3, v3
	ds_write_b32 v0, v4
	ds_write_b32 v3, v6
	ds_write_b32 v2, v7
	s_waitcnt vmcnt(14)
	ds_write_b32 v0, v8 offset:1040
	ds_write_b32 v146, v9 offset:1040
	ds_write_b32 v3, v10 offset:1040
	ds_write_b32 v2, v11 offset:1040
	s_waitcnt vmcnt(13)
	ds_write_b32 v0, v12 offset:2080
	ds_write_b32 v146, v13 offset:2080
	ds_write_b32 v3, v14 offset:2080
	ds_write_b32 v2, v15 offset:2080
	s_waitcnt vmcnt(12)
	ds_write_b32 v0, v16 offset:3120
	ds_write_b32 v146, v17 offset:3120
	ds_write_b32 v3, v18 offset:3120
	ds_write_b32 v2, v19 offset:3120
	s_waitcnt vmcnt(11)
	ds_write_b32 v0, v20 offset:4160
	ds_write_b32 v146, v21 offset:4160
	ds_write_b32 v3, v22 offset:4160
	ds_write_b32 v2, v23 offset:4160
	s_waitcnt vmcnt(10)
	ds_write_b32 v0, v24 offset:5200
	ds_write_b32 v146, v25 offset:5200
	ds_write_b32 v3, v26 offset:5200
	ds_write_b32 v2, v27 offset:5200
	s_waitcnt vmcnt(9)
	ds_write_b32 v0, v28 offset:6240
	ds_write_b32 v146, v29 offset:6240
	ds_write_b32 v3, v30 offset:6240
	ds_write_b32 v2, v31 offset:6240
	s_waitcnt vmcnt(8)
	ds_write_b32 v0, v32 offset:7280
	ds_write_b32 v146, v33 offset:7280
	ds_write_b32 v3, v34 offset:7280
	ds_write_b32 v2, v35 offset:7280
	s_waitcnt vmcnt(7)
	ds_write_b32 v0, v36 offset:8320
	ds_write_b32 v146, v37 offset:8320
	ds_write_b32 v3, v38 offset:8320
	ds_write_b32 v2, v39 offset:8320
	s_waitcnt vmcnt(6)
	ds_write_b32 v0, v40 offset:9360
	ds_write_b32 v146, v41 offset:9360
	ds_write_b32 v3, v42 offset:9360
	ds_write_b32 v2, v43 offset:9360
	s_waitcnt vmcnt(5)
	ds_write_b32 v0, v44 offset:10400
	ds_write_b32 v146, v45 offset:10400
	ds_write_b32 v3, v46 offset:10400
	ds_write_b32 v2, v47 offset:10400
	s_waitcnt vmcnt(4)
	ds_write_b32 v0, v48 offset:11440
	ds_write_b32 v146, v49 offset:11440
	ds_write_b32 v3, v50 offset:11440
	ds_write_b32 v2, v51 offset:11440
	s_waitcnt vmcnt(3)
	ds_write_b32 v0, v52 offset:12480
	ds_write_b32 v146, v53 offset:12480
	ds_write_b32 v3, v54 offset:12480
	ds_write_b32 v2, v55 offset:12480
	s_waitcnt vmcnt(2)
	ds_write_b32 v0, v56 offset:13520
	ds_write_b32 v146, v57 offset:13520
	ds_write_b32 v3, v58 offset:13520
	ds_write_b32 v2, v59 offset:13520
	s_waitcnt vmcnt(1)
	ds_write_b32 v0, v60 offset:14560
	ds_write_b32 v146, v61 offset:14560
	ds_write_b32 v3, v62 offset:14560
	ds_write_b32 v2, v63 offset:14560
	s_waitcnt vmcnt(0)
	ds_write_b32 v0, v64 offset:15600
	ds_write_b32 v146, v65 offset:15600
	ds_write_b32 v3, v66 offset:15600
	ds_write_b32 v2, v67 offset:15600
	s_waitcnt lgkmcnt(0)
	ds_read2_b32 v[2:3], v142 offset1:16
	ds_read2_b32 v[148:149], v142 offset0:65 offset1:81
	ds_read2_b32 v[154:155], v142 offset0:130 offset1:146
	ds_read2_b32 v[156:157], v142 offset0:195 offset1:211
	v_mov_b32_e32 v150, 0
	s_waitcnt lgkmcnt(3)
	v_mul_f32_e32 v0, 0x42000000, v2
	s_waitcnt lgkmcnt(2)
	v_mul_f32_e32 v2, 0x42000000, v148
	v_med3_f32 v0, v0, s41, v143
	s_waitcnt lgkmcnt(0)
	v_mul_f32_e32 v147, 0x42000000, v156
	v_med3_f32 v2, v2, s41, v143
	v_cvt_pk_fp8_f32 v150, v0, v2
	v_med3_f32 v2, v147, s41, v143
	v_add_u32_e32 v147, 0x400, v142
	ds_read2_b32 v[160:161], v147 offset0:4 offset1:20
	ds_read2_b32 v[162:163], v147 offset0:69 offset1:85
	ds_read2_b32 v[164:165], v147 offset0:134 offset1:150
	ds_read2_b32 v[166:167], v147 offset0:199 offset1:215
	v_mul_f32_e32 v146, 0x42000000, v154
	v_med3_f32 v0, v146, s41, v143
	v_cvt_pk_fp8_f32 v150, v0, v2 op_sel:[0,0,1]
	s_waitcnt lgkmcnt(3)
	v_mul_f32_e32 v0, 0x42000000, v160
	s_waitcnt lgkmcnt(2)
	v_mul_f32_e32 v2, 0x42000000, v162
	s_waitcnt lgkmcnt(0)
	v_mul_f32_e32 v148, 0x42000000, v166
	v_med3_f32 v0, v0, s41, v143
	v_med3_f32 v2, v2, s41, v143
	v_mov_b32_e32 v151, 0
	v_cvt_pk_fp8_f32 v151, v0, v2
	v_med3_f32 v2, v148, s41, v143
	v_add_u32_e32 v148, 0x800, v142
	ds_read2_b32 v[168:169], v148 offset0:8 offset1:24
	ds_read2_b32 v[170:171], v148 offset0:73 offset1:89
	ds_read2_b32 v[172:173], v148 offset0:138 offset1:154
	ds_read2_b32 v[174:175], v148 offset0:203 offset1:219
	v_mul_f32_e32 v146, 0x42000000, v164
	v_med3_f32 v0, v146, s41, v143
	v_cvt_pk_fp8_f32 v151, v0, v2 op_sel:[0,0,1]
	s_waitcnt lgkmcnt(3)
	v_mul_f32_e32 v0, 0x42000000, v168
	s_waitcnt lgkmcnt(2)
	v_mul_f32_e32 v2, 0x42000000, v170
	s_waitcnt lgkmcnt(1)
	v_mul_f32_e32 v146, 0x42000000, v172
	v_med3_f32 v0, v0, s41, v143
	v_med3_f32 v2, v2, s41, v143
	v_mov_b32_e32 v152, 0
	v_cvt_pk_fp8_f32 v152, v0, v2
	v_med3_f32 v0, v146, s41, v143
	v_add_u32_e32 v146, 0xc00, v142
	ds_read2_b32 v[176:177], v146 offset0:12 offset1:28
	ds_read2_b32 v[178:179], v146 offset0:77 offset1:93
	ds_read2_b32 v[180:181], v146 offset0:142 offset1:158
	s_waitcnt lgkmcnt(3)
	v_mul_f32_e32 v153, 0x42000000, v174
	v_med3_f32 v2, v153, s41, v143
	ds_read2_b32 v[182:183], v146 offset0:207 offset1:223
	v_cvt_pk_fp8_f32 v152, v0, v2 op_sel:[0,0,1]
	s_waitcnt lgkmcnt(3)
	v_mul_f32_e32 v0, 0x42000000, v176
	s_waitcnt lgkmcnt(2)
	v_mul_f32_e32 v2, 0x42000000, v178
	v_med3_f32 v0, v0, s41, v143
	v_med3_f32 v2, v2, s41, v143
	v_mov_b32_e32 v153, 0
	v_cvt_pk_fp8_f32 v153, v0, v2
	s_waitcnt lgkmcnt(1)
	v_mul_f32_e32 v154, 0x42000000, v180
	s_waitcnt lgkmcnt(0)
; #define GAS __attribute__((address_space(1)))
; __device__ __forceinline__ unsigned pk_fp8x4(float a, float b, float c, float d) { int p = __builtin_amdgcn_cvt_pk_fp8_f32(sat8(a), sat8(b), 0, false); p = __builtin_amdgcn_cvt_pk_fp8_f32(sat8(c), sat8(d), p, true); return (unsigned)p; }
; __device__ __forceinline__ void tr_finish(const TrDesc& d, f32x4 (&v)[16], LAS float* scr, int lane) {
;     ...
;         for (int j = 0; j < 4; ++j) { u32x4 o;
;             o.x = pk_fp8x4(sp[0 * 65 + 16 * j] * 32.0f, sp[1 * 65 + 16 * j] * 32.0f, sp[2 * 65 + 16 * j] * 32.0f, sp[3 * 65 + 16 * j] * 32.0f);
;             o.y = pk_fp8x4(sp[4 * 65 + 16 * j] * 32.0f, sp[5 * 65 + 16 * j] * 32.0f, sp[6 * 65 + 16 * j] * 32.0f, sp[7 * 65 + 16 * j] * 32.0f);
;             o.z = pk_fp8x4(sp[8 * 65 + 16 * j] * 32.0f, sp[9 * 65 + 16 * j] * 32.0f, sp[10 * 65 + 16 * j] * 32.0f, sp[11 * 65 + 16 * j] * 32.0f);
;             o.w = pk_fp8x4(sp[12 * 65 + 16 * j] * 32.0f, sp[13 * 65 + 16 * j] * 32.0f, sp[14 * 65 + 16 * j] * 32.0f, sp[15 * 65 + 16 * j] * 32.0f);
;             *(GAS u32x4*)(dp + (size_t)(16 * j) * d.K) = o; }
;     ...
;             if (itB >= NIT) break;
;             const int itA = itB + NGW;
;             if (itA < NIT) { dA = decode(NIT - 1 - itA); tr_load(dA, vA); }
	v_mul_f32_e32 v0, 0x42000000, v182
	v_med3_f32 v2, v154, s41, v143
	v_med3_f32 v0, v0, s41, v143
	v_cvt_pk_fp8_f32 v153, v2, v0 op_sel:[0,0,1]
	v_mov_b64_e32 v[158:159], s[16:17]
	v_mad_i64_i32 v[158:159], s[22:23], s2, v132, v[158:159]
	v_lshl_add_u64 v[158:159], v[158:159], 0, v[134:135]
	v_mul_f32_e32 v0, 0x42000000, v3
	v_mul_f32_e32 v2, 0x42000000, v149
	global_store_dwordx4 v[158:159], v[150:153], off
	v_med3_f32 v0, v0, s41, v143
	v_med3_f32 v2, v2, s41, v143
	v_mov_b32_e32 v150, 0
	v_cvt_pk_fp8_f32 v150, v0, v2
	v_mul_f32_e32 v3, 0x42000000, v155
	v_mul_f32_e32 v0, 0x42000000, v157
	v_med3_f32 v2, v3, s41, v143
	v_med3_f32 v0, v0, s41, v143
	v_cvt_pk_fp8_f32 v150, v2, v0 op_sel:[0,0,1]
	v_mul_f32_e32 v0, 0x42000000, v161
	v_mul_f32_e32 v2, 0x42000000, v163
	v_med3_f32 v0, v0, s41, v143
	v_med3_f32 v2, v2, s41, v143
	v_mov_b32_e32 v151, 0
	v_cvt_pk_fp8_f32 v151, v0, v2
	v_mul_f32_e32 v3, 0x42000000, v165
	v_mul_f32_e32 v0, 0x42000000, v167
	v_med3_f32 v2, v3, s41, v143
	v_med3_f32 v0, v0, s41, v143
	v_cvt_pk_fp8_f32 v151, v2, v0 op_sel:[0,0,1]
	v_mul_f32_e32 v0, 0x42000000, v169
	v_mul_f32_e32 v2, 0x42000000, v171
	v_med3_f32 v0, v0, s41, v143
	v_med3_f32 v2, v2, s41, v143
	v_mov_b32_e32 v152, 0
	v_cvt_pk_fp8_f32 v152, v0, v2
	v_mul_f32_e32 v3, 0x42000000, v173
	v_mul_f32_e32 v0, 0x42000000, v175
	v_med3_f32 v2, v3, s41, v143
	v_med3_f32 v0, v0, s41, v143
	v_cvt_pk_fp8_f32 v152, v2, v0 op_sel:[0,0,1]
	v_mul_f32_e32 v0, 0x42000000, v177
	v_mul_f32_e32 v2, 0x42000000, v179
	v_med3_f32 v0, v0, s41, v143
	v_med3_f32 v2, v2, s41, v143
	v_mov_b32_e32 v153, 0
	v_cvt_pk_fp8_f32 v153, v0, v2
	s_ashr_i32 s3, s2, 31
	v_mul_f32_e32 v3, 0x42000000, v181
	v_mul_f32_e32 v0, 0x42000000, v183
	v_med3_f32 v2, v3, s41, v143
	v_med3_f32 v0, v0, s41, v143
	s_lshl_b64 s[22:23], s[2:3], 4
	v_cvt_pk_fp8_f32 v153, v2, v0 op_sel:[0,0,1]
	v_lshl_add_u64 v[2:3], v[158:159], 0, s[22:23]
	ds_read2_b32 v[154:155], v142 offset0:32 offset1:48
	ds_read2_b32 v[156:157], v142 offset0:97 offset1:113
	ds_read2_b32 v[158:159], v142 offset0:162 offset1:178
	ds_read2_b32 v[160:161], v142 offset0:227 offset1:243
	s_andn2_b64 vcc, exec, s[20:21]
	s_waitcnt lgkmcnt(3)
	v_mul_f32_e32 v0, 0x42000000, v154
	s_waitcnt lgkmcnt(2)
	v_mul_f32_e32 v149, 0x42000000, v156
	global_store_dwordx4 v[2:3], v[150:153], off
	v_med3_f32 v0, v0, s41, v143
	v_med3_f32 v149, v149, s41, v143
	v_mov_b32_e32 v150, 0
	v_cvt_pk_fp8_f32 v150, v0, v149
	ds_read2_b32 v[162:163], v147 offset0:36 offset1:52
	ds_read2_b32 v[164:165], v147 offset0:101 offset1:117
	ds_read2_b32 v[166:167], v147 offset0:166 offset1:182
	ds_read2_b32 v[168:169], v147 offset0:231 offset1:247
	s_waitcnt lgkmcnt(5)
	v_mul_f32_e32 v151, 0x42000000, v158
	s_waitcnt lgkmcnt(4)
	v_mul_f32_e32 v152, 0x42000000, v160
	v_med3_f32 v0, v151, s41, v143
	v_med3_f32 v149, v152, s41, v143
	v_cvt_pk_fp8_f32 v150, v0, v149 op_sel:[0,0,1]
	s_waitcnt lgkmcnt(3)
	v_mul_f32_e32 v0, 0x42000000, v162
	s_waitcnt lgkmcnt(2)
	v_mul_f32_e32 v149, 0x42000000, v164
	v_med3_f32 v0, v0, s41, v143
	v_med3_f32 v149, v149, s41, v143
	v_mov_b32_e32 v151, 0
	v_cvt_pk_fp8_f32 v151, v0, v149
	ds_read2_b32 v[170:171], v148 offset0:40 offset1:56
	ds_read2_b32 v[172:173], v148 offset0:105 offset1:121
	ds_read2_b32 v[174:175], v148 offset0:170 offset1:186
	ds_read2_b32 v[176:177], v148 offset0:235 offset1:251
	s_waitcnt lgkmcnt(5)
	v_mul_f32_e32 v152, 0x42000000, v166
	s_waitcnt lgkmcnt(4)
	v_mul_f32_e32 v153, 0x42000000, v168
	v_med3_f32 v0, v152, s41, v143
	v_med3_f32 v149, v153, s41, v143
	v_cvt_pk_fp8_f32 v151, v0, v149 op_sel:[0,0,1]
	s_waitcnt lgkmcnt(3)
	v_mul_f32_e32 v0, 0x42000000, v170
	s_waitcnt lgkmcnt(2)
	v_mul_f32_e32 v149, 0x42000000, v172
	v_med3_f32 v0, v0, s41, v143
	v_med3_f32 v149, v149, s41, v143
	v_mov_b32_e32 v152, 0
	v_cvt_pk_fp8_f32 v152, v0, v149
	ds_read2_b32 v[178:179], v146 offset0:44 offset1:60
	ds_read2_b32 v[180:181], v146 offset0:109 offset1:125
	ds_read2_b32 v[182:183], v146 offset0:174 offset1:190
	s_waitcnt lgkmcnt(4)
	v_mul_f32_e32 v153, 0x42000000, v174
	s_waitcnt lgkmcnt(3)
	v_mul_f32_e32 v154, 0x42000000, v176
	v_med3_f32 v0, v153, s41, v143
	v_med3_f32 v149, v154, s41, v143
	ds_read2_b32 v[184:185], v146 offset0:239 offset1:255
	v_cvt_pk_fp8_f32 v152, v0, v149 op_sel:[0,0,1]
	s_waitcnt lgkmcnt(3)
	v_mul_f32_e32 v0, 0x42000000, v178
	s_waitcnt lgkmcnt(2)
	v_mul_f32_e32 v149, 0x42000000, v180
	v_med3_f32 v0, v0, s41, v143
	v_med3_f32 v149, v149, s41, v143
	v_mov_b32_e32 v153, 0
	v_cvt_pk_fp8_f32 v153, v0, v149
	s_waitcnt lgkmcnt(1)
	v_mul_f32_e32 v154, 0x42000000, v182
	s_waitcnt lgkmcnt(0)
	v_mul_f32_e32 v0, 0x42000000, v184
	v_med3_f32 v149, v154, s41, v143
	v_med3_f32 v0, v0, s41, v143
	v_cvt_pk_fp8_f32 v153, v149, v0 op_sel:[0,0,1]
	v_mul_f32_e32 v0, 0x42000000, v155
	v_mul_f32_e32 v149, 0x42000000, v157
	v_med3_f32 v0, v0, s41, v143
	v_med3_f32 v149, v149, s41, v143
	v_mov_b32_e32 v154, 0
	v_cvt_pk_fp8_f32 v154, v0, v149
	v_mul_f32_e32 v155, 0x42000000, v159
	v_mul_f32_e32 v0, 0x42000000, v161
	v_med3_f32 v149, v155, s41, v143
	v_med3_f32 v0, v0, s41, v143
	v_cvt_pk_fp8_f32 v154, v149, v0 op_sel:[0,0,1]
	v_mul_f32_e32 v0, 0x42000000, v163
	v_mul_f32_e32 v149, 0x42000000, v165
	v_med3_f32 v0, v0, s41, v143
	v_med3_f32 v149, v149, s41, v143
	v_mov_b32_e32 v155, 0
	v_cvt_pk_fp8_f32 v155, v0, v149
	v_mul_f32_e32 v156, 0x42000000, v167
	v_mul_f32_e32 v0, 0x42000000, v169
	v_med3_f32 v149, v156, s41, v143
	v_med3_f32 v0, v0, s41, v143
	v_cvt_pk_fp8_f32 v155, v149, v0 op_sel:[0,0,1]
	v_mul_f32_e32 v0, 0x42000000, v171
	v_mul_f32_e32 v149, 0x42000000, v173
	v_med3_f32 v0, v0, s41, v143
	v_med3_f32 v149, v149, s41, v143
	v_mov_b32_e32 v156, 0
	v_cvt_pk_fp8_f32 v156, v0, v149
	v_mul_f32_e32 v157, 0x42000000, v175
	v_mul_f32_e32 v0, 0x42000000, v177
	v_med3_f32 v149, v157, s41, v143
	v_med3_f32 v0, v0, s41, v143
	v_cvt_pk_fp8_f32 v156, v149, v0 op_sel:[0,0,1]
	v_mul_f32_e32 v0, 0x42000000, v179
	v_mul_f32_e32 v149, 0x42000000, v181
	v_med3_f32 v0, v0, s41, v143
	v_med3_f32 v149, v149, s41, v143
	v_mov_b32_e32 v157, 0
	v_cvt_pk_fp8_f32 v157, v0, v149
	v_mul_f32_e32 v158, 0x42000000, v183
	v_mul_f32_e32 v0, 0x42000000, v185
	v_med3_f32 v149, v158, s41, v143
	v_med3_f32 v0, v0, s41, v143
	v_cvt_pk_fp8_f32 v157, v149, v0 op_sel:[0,0,1]
	v_lshl_add_u64 v[2:3], v[2:3], 0, s[22:23]
	global_store_dwordx4 v[2:3], v[150:153], off
	v_lshl_add_u64 v[2:3], v[2:3], 0, s[22:23]
	global_store_dwordx4 v[2:3], v[154:157], off
	s_waitcnt lgkmcnt(0)
	s_cbranch_vccnz .LBB0_71
	s_add_i32 s42, s44, s48
	s_cmpk_lt_i32 s42, 0x2800
	s_cbranch_scc0 .Lps_2
	s_add_i32 s42, s42, 0x2000
;     ...
;             const int l = it / C_L; int r = it % C_L;
;             const float* W; unsigned char* WT; int ldw, K, k0, n0, scol, esz = 2;
;             if (r < C_IN) { const int kb = r / 188, nb = r % 188; n0 = 64 * nb; k0 = 64 * kb; ldw = NIN; K = D; W = a.w_in + (size_t)l * D * NIN;
;                 if (n0 < 3072) { d.rope = 1; scol = (n0 >> 7) * 128 + 32 * ((n0 >> 6) & 1) + 64 * (q4 >> 3) + 4 * (q4 & 7); }
;                 else if (n0 < 7680) scol = n0 + 4 * q4;
;                 else if (n0 < 11776) scol = n0 + 16 + 4 * q4;
;                 else if (n0 == 11776) { scol = (q4 < 4) ? 7680 + 4 * q4 : 0; d.zero = (q4 < 4) ? 0 : 1; }
;                 else { scol = 0; d.zero = 1; }
;     ...
;                 d.f8 = 1; esz = 1; WT = ws + WS_WIN + (size_t)l * NP * D;
;     ...
;                 WT = ws + WS_WIN + (size_t)l * NP * D * 2;
;     ...
;             } else if ((r -= C_IN) < C_OA) { const int kb = r / 32, nb = r % 32; n0 = 64 * nb; k0 = 64 * kb; ldw = D; K = 512; scol = n0 + 4 * q4; W = a.w_out_a + (size_t)l * 512 * D; WT = ws + WS_WOA + (size_t)l * D * 512 * (MIX_F8 ? 1 : 2); if (MIX_F8) { d.f8 = 1; esz = 1; }
;                 if (BR_FUSE) { K = 1536; WT = ws + WS_WOA + (size_t)l * D * 1536 + 1024; }
;             } else if ((r -= C_OA) < C_OB) { const int kb = r / 32, nb = r % 32; n0 = 64 * nb; k0 = 64 * kb; ldw = D; K = 1024; scol = n0 + 4 * q4; W = a.w_out_b + (size_t)l * 1024 * D; WT = ws + WS_WOB + (size_t)l * D * 1024 * (MIX_F8 ? 1 : 2); if (MIX_F8) { d.f8 = 1; esz = 1; }
;                 if (BR_FUSE) { K = 1536; WT = ws + WS_WOA + (size_t)l * D * 1536; }
;             } else if ((r -= C_OB) < C_O) { const int kb = r / 32, nb = r % 32; n0 = 64 * nb; k0 = 64 * kb; ldw = D; K = D; scol = n0 + 4 * q4; W = a.w_out + (size_t)l * D * D; WT = ws + WS_WO + (size_t)l * D * D * (MIX_F8 ? 1 : 2); if (MIX_F8) { d.f8 = 1; esz = 1; }
;             } else if ((r -= C_O) < C_GU) { const int e = r / 1024, r2 = r % 1024, kb = r2 / 32, nb = r2 % 32, pn = nb >> 2, sgu = (nb >> 1) & 1, c0 = 64 * (nb & 1);
;                 n0 = 64 * nb; k0 = 64 * kb; ldw = FF; K = D; scol = 128 * pn + c0 + 4 * q4; W = (sgu ? a.w_up_e : a.w_gate_e) + (size_t)(l * NE + e) * D * FF; WT = ws + WS_WGU + (size_t)(l * NE + e) * 2048 * D; d.f8 = 1; esz = 1;
;             } else { r -= C_GU; const int e = r / 512, r2 = r % 512, kb = r2 / 32, nb = r2 % 32;
.Lps_2:
	s_cmp_gt_i32 s42, 0xfcff
	s_cbranch_scc1 .LBB0_144
	s_sub_i32 s2, 0xfcff, s42
	s_mul_hi_u32 s0, s2, 0x81848da9
	s_lshr_b32 s0, s0, 14
	s_mul_i32 s3, s0, 0x7e80
	s_sub_i32 s27, s2, s3
	s_cmpk_gt_u32 s27, 0x177f
	s_cbranch_scc0 .LBB0_117
	s_cmpk_gt_u32 s27, 0x187f
	s_cbranch_scc0 .LBB0_119
	s_cmpk_gt_u32 s27, 0x1a7f
	s_cbranch_scc0 .LBB0_120
	s_cmpk_gt_u32 s27, 0x1e7f
	s_cbranch_scc0 .LBB0_123
	s_lshl_b32 s22, s27, 6
	s_cmpk_gt_u32 s27, 0x5e7f
	s_cbranch_scc0 .LBB0_147
	s_add_i32 s2, s27, 0xffffa180
	s_lshr_b32 s16, s2, 9
	s_lshl_b32 s2, s2, 1
	s_and_b32 s44, s2, 0x3c0
	s_load_dwordx2 s[2:3], s[8:9], 0x88
	s_lshl_b32 s17, s0, 4
	s_add_i32 s20, s16, s17
	s_mov_b32 s21, s1
	s_and_b32 s15, s22, 0x7c0
	s_lshl_b64 s[16:17], s[20:21], 23
	s_waitcnt lgkmcnt(0)
	s_add_u32 s16, s2, s16
	s_addc_u32 s17, s3, s17
	s_lshl_b64 s[2:3], s[20:21], 21
	s_add_u32 s20, s28, s2
	v_or_b32_e32 v0, s15, v136
	s_addc_u32 s21, s29, s3
	s_cbranch_execz .LBB0_148
	s_movk_i32 s2, 0x400
	s_mov_b64 s[22:23], 0x800
	s_cbranch_execz .LBB0_124
	s_branch .LBB0_125

; #define LAS __attribute__((address_space(3)))
; __device__ __forceinline__ void gla_local_unit(LAS unsigned char* lds, GlaPre& R, const bf16_t* proj, const float* alow, const float (&w2)[16], const float bias, ...
;     const int n = u & 31, h = (u >> 5) & 3, b = u >> 7;
;     const int d = tid & 127, ig = tid >> 7;
;     const int fr = lane & 15, fq = lane >> 4;
;     LAS unsigned char* QD = lds; LAS unsigned char* KI = lds + 17408; LAS unsigned char* KET = lds + 34816; LAS unsigned char* VL = lds + 53248;
;     LAS unsigned char* AT = lds + 86016;
;     LAS float* CS = (LAS float*)(lds + 95232); LAS float* ALs = (LAS float*)(lds + 97280);
;     const size_t t0 = (size_t)b * SEQ + 64 * n;
; #pragma unroll
;     for (int it = 0; it < 2; ++it) { const int id = tid + NTHREADS * it, row = id >> 4, ch = id & 15; *(LAS u32x4*)(QD + row * 272 + ch * 16) = R.q[it]; *(LAS u32x4*)(KI + row * 272 + ch * 16) = R.k[it]; }
;     ALs[tid] = R.al0; ALs[512 + tid] = R.al1;
; #pragma unroll
;     for (int it = 0; it < 4; ++it) { const int id = tid + NTHREADS * it, row = id >> 5, ch = id & 31; *(LAS u32x4*)(VL + swz512(row, ch)) = R.v[it]; }
; template <unsigned MASK, bool ONE>
; __global__ void __launch_bounds__(NTHREADS, 2) fwd_kernel(Args a_unused) {
;     ...
;                 const int hw = (vcu >> 5) & 3, dw = tid & 127; float w2[16];
; #pragma unroll
;                 for (int r = 0; r < 16; ++r) w2[r] = (a.w_alpha2 + (size_t)l * 16 * 512)[r * 512 + hw * 128 + dw];
;                 const float bias = (a.b_alpha2 + (size_t)l * 512)[hw * 128 + dw];
;                 for (int u = vcu; u < NB * 4 * 32; u += G) { GlaPre R; gla_local_issue(R, proj, alow, u, tid);
.LBB0_347:
	s_or_b64 exec, exec, s[0:1]
	v_readlane_b32 s0, v255, 17
	v_readlane_b32 s1, v255, 18
	s_mov_b32 s1, s97
	v_writelane_b32 v255, s0, 17
	s_mov_b32 s2, s38
	s_waitcnt lgkmcnt(0)
	v_writelane_b32 v255, s1, 18
	v_readlane_b32 s0, v253, 0
	v_readlane_b32 s1, v253, 1
	s_barrier
	s_nop 0
	v_mbcnt_lo_u32_b32 v0, s2, 0
	v_mbcnt_hi_u32_b32 v2, s2, v0
	v_readlane_b32 s2, v253, 10
	v_readlane_b32 s3, v253, 11
	s_andn2_b64 vcc, exec, s[2:3]
	s_cbranch_vccnz .LBB0_356
	s_load_dwordx4 s[4:7], s[0:1], 0x38
	s_load_dwordx2 s[2:3], s[0:1], 0xa0
	v_readlane_b32 s8, v255, 17
	v_readlane_b32 s9, v255, 18
	v_add_u32_e32 v0, s78, v2
	s_lshl_b64 s[0:1], s[8:9], 15
	v_and_b32_e32 v3, 0x7f, v0
	s_waitcnt lgkmcnt(0)
	s_add_u32 s0, s4, s0
	v_readlane_b32 s4, v253, 9
	s_addc_u32 s1, s5, s1
	v_ashrrev_i32_e32 v22, 5, v0
	v_or_b32_e32 v1, s4, v3
	v_lshlrev_b32_e32 v32, 2, v1
	v_lshl_add_u64 v[4:5], s[0:1], 0, v[32:33]
	v_add_co_u32_e32 v6, vcc, s82, v4
	s_movk_i32 s4, 0x2000
	s_nop 0
	v_addc_co_u32_e32 v7, vcc, 0, v5, vcc
	v_add_co_u32_e32 v8, vcc, s4, v4
	s_movk_i32 s4, 0x3000
	s_nop 0
	v_addc_co_u32_e32 v9, vcc, 0, v5, vcc
	v_add_co_u32_e32 v10, vcc, s4, v4
	s_movk_i32 s4, 0x4000
	s_nop 0
	v_addc_co_u32_e32 v11, vcc, 0, v5, vcc
	v_add_co_u32_e32 v12, vcc, s4, v4
	s_movk_i32 s4, 0x5000
	s_nop 0
	v_addc_co_u32_e32 v13, vcc, 0, v5, vcc
	v_add_co_u32_e32 v14, vcc, s4, v4
	s_movk_i32 s4, 0x6000
	s_nop 0
	v_addc_co_u32_e32 v15, vcc, 0, v5, vcc
	v_add_co_u32_e32 v16, vcc, s4, v4
	s_movk_i32 s4, 0x7000
	s_nop 0
	v_addc_co_u32_e32 v17, vcc, 0, v5, vcc
	v_add_co_u32_e32 v4, vcc, s4, v4
	s_lshl_b64 s[4:5], s[8:9], 11
	global_load_dword v46, v[8:9], off offset:-4096
	global_load_dword v47, v[8:9], off
	global_load_dword v48, v[8:9], off offset:2048
	global_load_dword v49, v[12:13], off offset:-4096
	global_load_dword v50, v[12:13], off
	global_load_dword v51, v[12:13], off offset:2048
	global_load_dword v52, v[16:17], off offset:-4096
	global_load_dword v53, v[16:17], off
	global_load_dword v54, v[16:17], off offset:2048
	s_add_u32 s4, s6, s4
	v_addc_co_u32_e32 v5, vcc, 0, v5, vcc
	s_addc_u32 s5, s7, s5
	global_load_dword v55, v32, s[0:1]
	global_load_dword v56, v32, s[0:1] offset:2048
	global_load_dword v57, v[6:7], off offset:2048
	global_load_dword v58, v[10:11], off offset:2048
	global_load_dword v59, v[14:15], off offset:2048
	global_load_dword v60, v[4:5], off
	global_load_dword v61, v32, s[4:5]
	global_load_dword v62, v[4:5], off offset:2048
	v_add_u32_e32 v6, 0x200, v0
	v_lshlrev_b32_e32 v15, 2, v22
	v_ashrrev_i32_e32 v24, 5, v6
	v_and_b32_e32 v13, 31, v2
	v_and_b32_e32 v15, 12, v15
	v_bfe_u32 v30, v22, 2, 2
	v_bitop3_b32 v15, v15, v13, v30 bitop3:0x36
	v_lshlrev_b32_e32 v30, 2, v24
	v_add_u32_e32 v7, 0x400, v0
	v_and_b32_e32 v30, 12, v30
	v_bfe_u32 v31, v24, 2, 2
	v_ashrrev_i32_e32 v26, 5, v7
	v_bitop3_b32 v30, v30, v13, v31 bitop3:0x36
	v_lshl_add_u32 v45, v30, 4, 0
	v_lshlrev_b32_e32 v30, 2, v26
	v_add_u32_e32 v7, 0x600, v0
	v_and_b32_e32 v30, 12, v30
	v_bfe_u32 v31, v26, 2, 2
	v_ashrrev_i32_e32 v28, 5, v7
	v_bitop3_b32 v30, v30, v13, v31 bitop3:0x36
	v_ashrrev_i32_e32 v11, 7, v0
	v_lshlrev_b32_e32 v12, 2, v0
	v_readlane_b32 s4, v254, 49
	v_lshl_add_u32 v76, v30, 4, 0
	v_lshlrev_b32_e32 v30, 2, v28
	v_ashrrev_i32_e32 v18, 4, v0
	v_add_u32_e32 v63, s4, v12
	v_and_b32_e32 v30, 12, v30
	v_bfe_u32 v31, v28, 2, 2
	v_lshl_add_u32 v64, v11, 10, s4
	v_readlane_b32 s4, v254, 50
	s_movk_i32 s16, 0x90
	v_lshlrev_b32_e32 v5, 4, v0
	v_bitop3_b32 v13, v30, v13, v31 bitop3:0x36
	v_add_u32_e32 v65, s4, v12
	v_lshl_add_u32 v66, v3, 2, s4
	v_lshl_add_u32 v12, v3, 1, 0
	v_mad_u32_u24 v79, v3, s16, 0
	v_and_b32_e32 v3, 3, v2
	s_movk_i32 s14, 0xc0
	v_lshlrev_b32_e32 v30, 2, v18
	v_and_b32_e32 v32, 0xf0, v5
	v_and_or_b32 v3, v5, s14, v3
	v_and_b32_e32 v5, 0x1fffff00, v0
	v_and_b32_e32 v30, 60, v30
	v_ashrrev_i32_e32 v20, 4, v6
	v_or3_b32 v5, v5, v30, v3
	v_lshlrev_b32_e32 v30, 3, v5
	v_and_b32_e32 v5, 0x1fffff00, v6
	v_lshlrev_b32_e32 v6, 2, v20
	v_and_b32_e32 v6, 60, v6
	v_ashrrev_i32_e32 v36, 4, v2
	v_or3_b32 v3, v5, v6, v3
	v_and_b32_e32 v7, 15, v2
	v_lshlrev_b32_e32 v34, 3, v3
	v_lshlrev_b32_e32 v3, 2, v36
	v_readlane_b32 s14, v253, 12
	s_movk_i32 s15, 0x110
; __device__ __forceinline__ void gla_local_unit(LAS unsigned char* lds, GlaPre& R, const bf16_t* proj, const float* alow, const float (&w2)[16], const float bias, ...
;     const int n = u & 31, h = (u >> 5) & 3, b = u >> 7;
;     const int d = tid & 127, ig = tid >> 7;
;     const int fr = lane & 15, fq = lane >> 4;
;     LAS unsigned char* QD = lds; LAS unsigned char* KI = lds + 17408; LAS unsigned char* KET = lds + 34816; LAS unsigned char* VL = lds + 53248;
;     LAS unsigned char* AT = lds + 86016;
;     LAS float* CS = (LAS float*)(lds + 95232); LAS float* ALs = (LAS float*)(lds + 97280);
;     const size_t t0 = (size_t)b * SEQ + 64 * n;
; #pragma unroll
;     for (int it = 0; it < 2; ++it) { const int id = tid + NTHREADS * it, row = id >> 4, ch = id & 15; *(LAS u32x4*)(QD + row * 272 + ch * 16) = R.q[it]; *(LAS u32x4*)(KI + row * 272 + ch * 16) = R.k[it]; }
;     ALs[tid] = R.al0; ALs[512 + tid] = R.al1;
; #pragma unroll
;     for (int it = 0; it < 4; ++it) { const int id = tid + NTHREADS * it, row = id >> 5, ch = id & 31; *(LAS u32x4*)(VL + swz512(row, ch)) = R.v[it]; }
;     __syncthreads();
;     if (u_next >= 0) gla_local_issue(R, proj, alow, u_next, tid);
;     float bl[16]; float run = 0.f;
; #pragma unroll
;     for (int ii = 0; ii < 16; ++ii) { float z = bias; const LAS f32x4* ap = (const LAS f32x4*)(ALs + (16 * ig + ii) * 16);
; #pragma unroll
;         for (int r4 = 0; r4 < 4; ++r4) { const f32x4 av = ap[r4]; z = fmaf(av[0], w2[4 * r4], z); z = fmaf(av[1], w2[4 * r4 + 1], z); z = fmaf(av[2], w2[4 * r4 + 2], z); z = fmaf(av[3], w2[4 * r4 + 3], z); }
;         const float la = (fminf(z, 0.f) - __logf(1.0f + __expf(-fabsf(z)))) * 0.0625f; run += la; bl[ii] = run; }
;     CS[ig * 128 + d] = run;
;     __syncthreads();
;     float pre = 0.f, tot = 0.f;
; #pragma unroll
;     for (int g2 = 0; g2 < 4; ++g2) { const float cv = CS[g2 * 128 + d]; tot += cv; pre += (g2 < ig) ? cv : 0.f; }
;     const float qscale = 0.08838834764831845f; const float etot = __expf(tot);
;     unsigned ke[8];
; #pragma unroll
;     for (int ii = 0; ii < 16; ++ii) { const float bb = pre + bl[ii];
;         LAS bf16_t* qp = (LAS bf16_t*)(QD + (16 * ig + ii) * 272 + 2 * d); LAS bf16_t* kp = (LAS bf16_t*)(KI + (16 * ig + ii) * 272 + 2 * d);
;         const float qf_ = bf2f(*qp), kf_ = bf2f(*kp);
;         const float eb = __expf(bb), einv = __builtin_amdgcn_rcpf(eb);
	v_readlane_b32 s31, v254, 51
	v_add_u32_e32 v5, s14, v3
	v_or_b32_e32 v6, s14, v7
	v_readlane_b32 s14, v253, 15
	v_or_b32_e32 v38, 1, v5
	v_or_b32_e32 v39, 2, v5
	v_or_b32_e32 v37, s14, v7
	v_or_b32_e32 v40, 3, v5
	v_mul_lo_u32 v9, v18, s15
	v_mul_lo_u32 v10, v20, s15
	v_mul_lo_u32 v6, v6, s15
	v_mad_u32_u24 v68, v37, s15, 0
	v_lshl_add_u32 v80, v37, 1, s31
	v_cmp_lt_i32_e64 s[14:15], v5, v37
	v_mul_lo_u32 v81, v5, s16
	v_cmp_lt_i32_e64 s[16:17], v38, v37
	v_cmp_lt_i32_e64 s[18:19], v39, v37
	v_cmp_lt_i32_e64 s[20:21], v40, v37
	v_or_b32_e32 v37, 16, v37
	v_cmp_lt_i32_e64 s[22:23], v5, v37
	v_bfe_u32 v5, v2, 2, 2
	v_and_b32_e32 v67, -16, v2
	v_lshl_add_u32 v83, v37, 1, s31
	v_cmp_lt_i32_e64 s[24:25], v38, v37
	v_cmp_lt_i32_e64 s[26:27], v39, v37
	v_cmp_lt_i32_e64 s[28:29], v40, v37
	v_lshl_or_b32 v5, v36, 3, v5
	v_lshrrev_b32_e32 v37, 1, v2
	v_readlane_b32 s30, v253, 18
	v_and_b32_e32 v38, 12, v2
	v_lshlrev_b32_e32 v36, 1, v36
	v_lshlrev_b32_e32 v2, 3, v2
	v_and_or_b32 v37, v37, 1, s30
	v_and_b32_e32 v36, 2, v36
	v_and_b32_e32 v85, 8, v2
	v_add_u32_e32 v2, 0, v85
	v_or_b32_e32 v39, 4, v5
	v_bitop3_b32 v40, v36, v37, v38 bitop3:0x36
	v_lshl_add_u32 v70, v40, 4, v2
	v_lshlrev_b32_e32 v40, 9, v39
	v_bfe_u32 v39, v39, 2, 2
	v_bitop3_b32 v41, v39, v37, v38 bitop3:0x36
	v_lshlrev_b32_e32 v69, 9, v5
	v_lshlrev_b32_e32 v41, 4, v41
	v_add_u32_e32 v5, 36, v5
	v_add3_u32 v84, 0, v41, v40
	v_lshlrev_b32_e32 v41, 9, v5
	v_bfe_u32 v5, v5, 2, 2
	v_bitop3_b32 v42, v5, v37, v38 bitop3:0x36
	v_or_b32_e32 v37, 2, v37
	v_bitop3_b32 v36, v36, v37, v38 bitop3:0x36
	v_lshl_add_u32 v72, v36, 4, v2
	v_bitop3_b32 v2, v39, v37, v38 bitop3:0x36
	v_lshlrev_b32_e32 v2, 4, v2
	v_add3_u32 v87, 0, v2, v40
	v_bitop3_b32 v2, v5, v37, v38 bitop3:0x36
	s_add_u32 s0, s2, 0x30600000
	s_movk_i32 s12, 0x1100
	v_lshlrev_b32_e32 v2, 4, v2
	s_addc_u32 s1, s3, 0
	v_ashrrev_i32_e32 v1, 31, v0
	v_mul_lo_u32 v78, v11, s12
	s_movk_i32 s12, 0x80
	v_add3_u32 v5, 0, v2, v41
	v_lshl_add_u32 v2, v7, 4, v3
	v_lshlrev_b32_e32 v4, 3, v0
	v_lshl_add_u64 v[16:17], s[0:1], 0, v[32:33]
	v_add_u32_e32 v8, 0, v32
	v_cmp_gt_u32_e64 s[12:13], s12, v0
	v_mov_b32_e32 v32, v0
	v_mul_u32_u24_e32 v89, 0x90, v7
	v_ashrrev_i32_e32 v3, 31, v2
	v_add_u32_e32 v7, s31, v67
	v_lshl_add_u64 v[0:1], v[0:1], 2, s[2:3]
	s_mov_b64 s[30:31], 0x300000
	v_lshl_add_u64 v[36:37], v[0:1], 0, s[30:31]
	v_lshl_add_u64 v[0:1], v[2:3], 1, s[2:3]
	s_mov_b64 s[30:31], 0x4ae00000
	s_add_u32 s36, s2, 0x47e00000
	v_lshlrev_b32_e32 v42, 4, v42
	v_lshl_add_u64 v[38:39], v[0:1], 0, s[30:31]
	s_mov_b64 s[30:31], 0x48e00000
	s_addc_u32 s37, s3, 0
	v_add3_u32 v86, 0, v42, v41
	v_lshl_add_u64 v[40:41], v[0:1], 0, s[30:31]
	v_readlane_b32 s30, v254, 27
	s_add_u32 s2, s2, s30
	v_readlane_b32 s30, v254, 28
	v_and_b32_e32 v4, 0xf8, v4
	v_lshlrev_b32_e32 v14, 9, v22
	v_lshl_add_u32 v15, v15, 4, 0
	v_lshlrev_b32_e32 v44, 9, v24
	v_lshlrev_b32_e32 v75, 9, v26
	v_lshlrev_b32_e32 v77, 9, v28
	v_lshl_add_u32 v13, v13, 4, 0
	v_cmp_lt_i32_e64 s[4:5], 0, v11
	v_cmp_lt_i32_e64 s[6:7], 1, v11
	v_cmp_lt_i32_e64 s[8:9], 2, v11
	v_cmp_lt_i32_e64 s[10:11], 3, v11
	v_lshlrev_b32_e32 v11, 5, v11
	v_add_u32_e32 v6, 0, v6
	v_add_u32_e32 v82, 0x1100, v68
	v_add_u32_e32 v88, 0, v67
	s_addc_u32 s3, s3, s30
	v_ashrrev_i32_e32 v19, 31, v18
	v_ashrrev_i32_e32 v21, 31, v20
	v_ashrrev_i32_e32 v23, 31, v22
	v_ashrrev_i32_e32 v25, 31, v24
	v_ashrrev_i32_e32 v27, 31, v26
	v_ashrrev_i32_e32 v29, 31, v28
	v_ashrrev_i32_e32 v31, 31, v30
	v_ashrrev_i32_e32 v35, 31, v34
	v_add_u32_e32 v71, 0x4000, v69
	v_lshl_add_u64 v[42:43], v[32:33], 2, s[2:3]
	v_lshlrev_b32_e32 v32, 1, v4
	v_add_u32_e32 v73, v15, v14
	v_add_u32_e32 v74, v45, v44
	v_add_u32_e32 v75, v76, v75
	v_add_u32_e32 v76, v13, v77
	v_add_u32_e32 v77, v12, v78
	v_add_u32_e32 v78, v79, v11
	v_add_u32_e32 v79, v80, v81
	v_add_u32_e32 v80, v82, v67
	v_add_u32_e32 v81, v83, v81
	v_add_u32_e32 v82, v84, v85
	v_add_u32_e32 v83, v86, v85
	v_add_u32_e32 v84, v87, v85
	v_add_u32_e32 v85, v5, v85
	v_add_u32_e32 v86, v88, v89
	v_add_u32_e32 v87, v7, v89
	v_add_u32_e32 v88, v8, v9
	v_add_u32_e32 v89, v8, v10
	v_add_u32_e32 v90, v6, v67
	v_readlane_b32 s40, v254, 21
	s_mov_b32 s41, s76
	s_branch .LBB0_350

; #define LAS __attribute__((address_space(3)))
; __device__ __forceinline__ void gla_local_issue(GlaPre& R, const bf16_t* proj, const float* alow, int u, int tid) {
;     const int n = u & 31, h = (u >> 5) & 3, b = u >> 7;
;     const size_t t0 = (size_t)b * SEQ + 64 * n;
;     R.al0 = alow[t0 * 16 + tid]; R.al1 = alow[t0 * 16 + 512 + tid];
; #pragma unroll
;     for (int it = 0; it < 2; ++it) { const int id = tid + NTHREADS * it, row = id >> 4, ch = id & 15; const bf16_t* src = proj + (t0 + row) * NP + h * 128 + ch * 8; R.q[it] = *(const u32x4*)(src + QB); R.k[it] = *(const u32x4*)(src + KB); }
; #pragma unroll
;     for (int it = 0; it < 4; ++it) { const int id = tid + NTHREADS * it, row = id >> 5, ch = id & 31; R.v[it] = *(const u32x4*)(proj + (t0 + row) * NP + VB + h * 256 + ch * 8); }
; }
; __device__ __forceinline__ void gla_local_unit(LAS unsigned char* lds, GlaPre& R, const bf16_t* proj, const float* alow, const float (&w2)[16], const float bias, ...
;     const int n = u & 31, h = (u >> 5) & 3, b = u >> 7;
;     const int d = tid & 127, ig = tid >> 7;
;     const int fr = lane & 15, fq = lane >> 4;
;     LAS unsigned char* QD = lds; LAS unsigned char* KI = lds + 17408; LAS unsigned char* KET = lds + 34816; LAS unsigned char* VL = lds + 53248;
;     LAS unsigned char* AT = lds + 86016;
;     LAS float* CS = (LAS float*)(lds + 95232); LAS float* ALs = (LAS float*)(lds + 97280);
;     const size_t t0 = (size_t)b * SEQ + 64 * n;
; #pragma unroll
;     for (int it = 0; it < 2; ++it) { const int id = tid + NTHREADS * it, row = id >> 4, ch = id & 15; *(LAS u32x4*)(QD + row * 272 + ch * 16) = R.q[it]; *(LAS u32x4*)(KI + row * 272 + ch * 16) = R.k[it]; }
;     ALs[tid] = R.al0; ALs[512 + tid] = R.al1;
; #pragma unroll
;     for (int it = 0; it < 4; ++it) { const int id = tid + NTHREADS * it, row = id >> 5, ch = id & 31; *(LAS u32x4*)(VL + swz512(row, ch)) = R.v[it]; }
;     __syncthreads();
;     if (u_next >= 0) gla_local_issue(R, proj, alow, u_next, tid);
;     float bl[16]; float run = 0.f;
; #pragma unroll
;     for (int ii = 0; ii < 16; ++ii) { float z = bias; const LAS f32x4* ap = (const LAS f32x4*)(ALs + (16 * ig + ii) * 16);
; #pragma unroll
;         for (int r4 = 0; r4 < 4; ++r4) { const f32x4 av = ap[r4]; z = fmaf(av[0], w2[4 * r4], z); z = fmaf(av[1], w2[4 * r4 + 1], z); z = fmaf(av[2], w2[4 * r4 + 2], z); z = fmaf(av[3], w2[4 * r4 + 3], z); }
.LBB0_350:
	s_ashr_i32 s2, s41, 7
	s_ashr_i32 s3, s2, 31
	s_bfe_u32 s30, s41, 0x20005
	s_lshl_b64 s[2:3], s[2:3], 11
	s_and_b32 s31, s40, 0x7c0
	s_or_b32 s2, s2, s31
	s_lshl_b32 s96, s30, 8
	s_lshl_b64 s[34:35], s[2:3], 6
	v_lshl_add_u64 v[4:5], v[16:17], 0, s[96:97]
	v_lshl_add_u64 v[2:3], s[2:3], 0, v[18:19]
	v_lshl_add_u64 v[0:1], v[36:37], 0, s[34:35]
	v_mad_u64_u32 v[6:7], s[34:35], v2, s49, v[4:5]
	s_movk_i32 s31, 0x2000
	v_lshl_add_u64 v[14:15], s[2:3], 0, v[22:23]
	v_mov_b64_e32 v[44:45], s[0:1]
	v_mad_i32_i24 v2, v3, s49, v7
	v_add_co_u32_e32 v6, vcc, s31, v6
	v_lshl_add_u64 v[8:9], s[2:3], 0, v[20:21]
	v_mad_u64_u32 v[92:93], s[34:35], v14, s49, v[44:45]
	v_lshl_add_u64 v[96:97], s[2:3], 0, v[24:25]
	v_addc_co_u32_e32 v7, vcc, 0, v2, vcc
	v_mad_u64_u32 v[4:5], s[34:35], v8, s49, v[4:5]
	v_mad_i32_i24 v93, v15, s49, v93
	s_lshl_b32 s96, s30, 9
	v_mad_u64_u32 v[98:99], s[34:35], v96, s49, v[44:45]
	v_mad_i32_i24 v5, v9, s49, v5
	v_add_co_u32_e32 v12, vcc, s31, v4
	v_lshl_add_u64 v[14:15], v[92:93], 0, s[96:97]
	v_mad_i32_i24 v99, v97, s49, v99
	v_addc_co_u32_e32 v13, vcc, 0, v5, vcc
	v_lshl_add_u64 v[14:15], v[14:15], 0, v[32:33]
	v_lshl_add_u64 v[96:97], v[98:99], 0, s[96:97]
	v_lshl_add_u64 v[98:99], s[2:3], 0, v[26:27]
	v_add_co_u32_e32 v92, vcc, s31, v14
	v_mad_u64_u32 v[100:101], s[34:35], v98, s49, v[44:45]
	s_nop 0
	v_addc_co_u32_e32 v93, vcc, 0, v15, vcc
	v_lshl_add_u64 v[96:97], v[96:97], 0, v[32:33]
	v_mad_i32_i24 v101, v99, s49, v101
	v_add_co_u32_e32 v96, vcc, s31, v96
	v_lshl_add_u64 v[98:99], v[100:101], 0, s[96:97]
	s_nop 0
	v_addc_co_u32_e32 v97, vcc, 0, v97, vcc
	v_lshl_add_u64 v[98:99], v[98:99], 0, v[32:33]
	v_add_co_u32_e32 v100, vcc, s31, v98
	global_load_dword v91, v[0:1], off
	global_load_dword v108, v[0:1], off offset:2048
	s_nop 0
	global_load_dwordx4 v[0:3], v[6:7], off offset:1024
	v_addc_co_u32_e32 v101, vcc, 0, v99, vcc
	global_load_dwordx4 v[4:7], v[6:7], off offset:2048
	s_nop 0
	global_load_dwordx4 v[8:11], v[12:13], off offset:1024
	s_nop 0
	global_load_dwordx4 v[12:15], v[12:13], off offset:2048
	s_nop 0
	global_load_dwordx4 v[92:95], v[92:93], off offset:3072
	s_nop 0
	global_load_dwordx4 v[96:99], v[96:97], off offset:3072
	s_nop 0
	global_load_dwordx4 v[100:103], v[100:101], off offset:3072
	v_lshl_add_u64 v[104:105], s[2:3], 0, v[28:29]
	v_mad_u64_u32 v[44:45], s[2:3], v104, s49, v[44:45]
	v_mad_i32_i24 v45, v105, s49, v45
	v_lshl_add_u64 v[44:45], v[44:45], 0, s[96:97]
	v_lshl_add_u64 v[44:45], v[44:45], 0, v[32:33]
	v_add_co_u32_e32 v44, vcc, s31, v44
	s_mov_b32 s3, 0xbfb8aa3b
	s_nop 0
	v_addc_co_u32_e32 v45, vcc, 0, v45, vcc
	global_load_dwordx4 v[104:107], v[44:45], off offset:3072
	s_mov_b32 s31, 0x800000
	s_mov_b32 s42, 0x3f317217
	s_mov_b32 s43, 0x7f800000
	s_mov_b32 s2, 0x3d800000
	s_waitcnt vmcnt(7)
	ds_write_b128 v88, v[0:3]
	s_waitcnt vmcnt(6)
	ds_write_b128 v88, v[4:7] offset:17408
	s_waitcnt vmcnt(5)
	ds_write_b128 v89, v[8:11]
	s_waitcnt vmcnt(4)
	ds_write_b128 v89, v[12:15] offset:17408
	ds_write2st64_b32 v63, v91, v108 offset1:8
	s_waitcnt vmcnt(3)
	ds_write_b128 v73, v[92:95] offset:53248
	s_waitcnt vmcnt(2)
	ds_write_b128 v74, v[96:99] offset:53248
	s_waitcnt vmcnt(1)
	ds_write_b128 v75, v[100:103] offset:53248
	s_waitcnt vmcnt(0)
	ds_write_b128 v76, v[104:107] offset:53248
	s_waitcnt lgkmcnt(0)
	s_barrier
	ds_read_b128 v[0:3], v64
	ds_read_b128 v[4:7], v64 offset:16
	ds_read_b128 v[8:11], v64 offset:32
	ds_read_b128 v[12:15], v64 offset:48
	ds_read_b128 v[92:95], v64 offset:64
	s_waitcnt lgkmcnt(4)
	v_fma_f32 v44, v0, v55, v61
	v_fmac_f32_e32 v44, v1, v56
	v_fmac_f32_e32 v44, v2, v46
	v_fmac_f32_e32 v44, v3, v57
	s_waitcnt lgkmcnt(3)
	v_fmac_f32_e32 v44, v4, v47
	v_fmac_f32_e32 v44, v5, v48
	v_fmac_f32_e32 v44, v6, v49
	v_fmac_f32_e32 v44, v7, v58
	s_waitcnt lgkmcnt(2)
	v_fmac_f32_e32 v44, v8, v50
	v_fmac_f32_e32 v44, v9, v51
	v_fmac_f32_e32 v44, v10, v52
	v_fmac_f32_e32 v44, v11, v59
	s_waitcnt lgkmcnt(1)
	v_fmac_f32_e32 v44, v12, v53
	v_fmac_f32_e32 v44, v13, v54
	v_fmac_f32_e32 v44, v14, v60
	v_fmac_f32_e32 v44, v15, v62
	v_mul_f32_e64 v0, |v44|, s3
	v_exp_f32_e32 v4, v0
	ds_read_b128 v[0:3], v64 offset:80
	s_waitcnt lgkmcnt(1)
	v_fma_f32 v8, v92, v55, v61
	v_fmac_f32_e32 v8, v93, v56
	v_add_f32_e32 v4, 1.0, v4
	v_cmp_gt_f32_e32 vcc, s31, v4
	v_fmac_f32_e32 v8, v94, v46
	v_fmac_f32_e32 v8, v95, v57
	v_cndmask_b32_e64 v5, 0, 32, vcc
	v_ldexp_f32 v4, v4, v5
	v_log_f32_e32 v9, v4
	v_min_f32_e32 v10, 0, v44
	ds_read_b128 v[92:95], v64 offset:592
	ds_read_b128 v[96:99], v64 offset:848
	v_mul_f32_e32 v4, 0x3f317217, v9
	v_fma_f32 v11, v9, s42, -v4
	ds_read_b128 v[4:7], v64 offset:96
	s_waitcnt lgkmcnt(3)
	v_fmac_f32_e32 v8, v0, v47
	v_fmac_f32_e32 v8, v1, v48
	v_fmac_f32_e32 v8, v2, v49
	v_fmac_f32_e32 v8, v3, v58
	ds_read_b128 v[0:3], v64 offset:112
	s_waitcnt lgkmcnt(1)
	v_fmac_f32_e32 v8, v4, v50
	v_fmac_f32_e32 v8, v5, v51
	v_fmac_f32_e32 v8, v6, v52
	v_fmac_f32_e32 v8, v7, v59
	ds_read_b128 v[4:7], v64 offset:128
	s_waitcnt lgkmcnt(1)
	v_fmac_f32_e32 v8, v0, v53
	v_fmac_f32_e32 v8, v1, v54
	v_fmac_f32_e32 v8, v2, v60
	v_fmac_f32_e32 v8, v3, v62
	v_mul_f32_e64 v0, |v8|, s3
	v_exp_f32_e32 v0, v0
	v_fmac_f32_e32 v11, 0x3377d1cf, v9
	v_fmac_f32_e32 v11, 0x3f317217, v9
	v_cmp_lt_f32_e64 s[34:35], |v9|, s43
	v_cndmask_b32_e32 v2, 0, v191, vcc
	v_add_f32_e32 v0, 1.0, v0
	v_cndmask_b32_e64 v1, v9, v11, s[34:35]
	v_sub_f32_e32 v1, v1, v2
	v_cmp_gt_f32_e32 vcc, s31, v0
	v_sub_f32_e32 v1, v10, v1
	s_waitcnt lgkmcnt(0)
	v_fma_f32 v12, v4, v55, v61
	v_cndmask_b32_e64 v2, 0, 32, vcc
	v_ldexp_f32 v0, v0, v2
	v_fma_f32 v2, v1, s2, 0
	v_min_f32_e32 v1, 0, v8
	ds_read_b128 v[8:11], v64 offset:144
	v_fmac_f32_e32 v12, v5, v56
	v_fmac_f32_e32 v12, v6, v46
	v_fmac_f32_e32 v12, v7, v57
	ds_read_b128 v[4:7], v64 offset:160
	s_waitcnt lgkmcnt(1)
; #define LAS __attribute__((address_space(3)))
; __device__ __forceinline__ void gla_local_unit(LAS unsigned char* lds, GlaPre& R, const bf16_t* proj, const float* alow, const float (&w2)[16], const float bias, ...
;     ...
;     float bl[16]; float run = 0.f;
; #pragma unroll
;     for (int ii = 0; ii < 16; ++ii) { float z = bias; const LAS f32x4* ap = (const LAS f32x4*)(ALs + (16 * ig + ii) * 16);
; #pragma unroll
;         for (int r4 = 0; r4 < 4; ++r4) { const f32x4 av = ap[r4]; z = fmaf(av[0], w2[4 * r4], z); z = fmaf(av[1], w2[4 * r4 + 1], z); z = fmaf(av[2], w2[4 * r4 + 2], z); z = fmaf(av[3], w2[4 * r4 + 3], z); }
;         const float la = (fminf(z, 0.f) - __logf(1.0f + __expf(-fabsf(z)))) * 0.0625f; run += la; bl[ii] = run; }
	v_fmac_f32_e32 v12, v8, v47
	v_fmac_f32_e32 v12, v9, v48
	v_fmac_f32_e32 v12, v10, v49
	v_fmac_f32_e32 v12, v11, v58
	ds_read_b128 v[8:11], v64 offset:176
	s_waitcnt lgkmcnt(1)
	v_fmac_f32_e32 v12, v4, v50
	v_fmac_f32_e32 v12, v5, v51
	v_fmac_f32_e32 v12, v6, v52
	v_fmac_f32_e32 v12, v7, v59
	v_log_f32_e32 v0, v0
	s_waitcnt lgkmcnt(0)
	v_fmac_f32_e32 v12, v8, v53
	v_fmac_f32_e32 v12, v9, v54
	v_fmac_f32_e32 v12, v10, v60
	v_fmac_f32_e32 v12, v11, v62
	v_mul_f32_e32 v3, 0x3f317217, v0
	v_mul_f32_e64 v4, |v12|, s3
	v_fma_f32 v3, v0, s42, -v3
	v_exp_f32_e32 v4, v4
	v_fmac_f32_e32 v3, 0x3377d1cf, v0
	v_fmac_f32_e32 v3, 0x3f317217, v0
	v_cmp_lt_f32_e64 s[34:35], |v0|, s43
	s_mov_b32 s2, 0xffff0000
	s_nop 0
	v_cndmask_b32_e64 v0, v0, v3, s[34:35]
	v_cndmask_b32_e32 v3, 0, v191, vcc
	v_sub_f32_e32 v0, v0, v3
	v_add_f32_e32 v3, 1.0, v4
	v_cmp_gt_f32_e32 vcc, s31, v3
	v_sub_f32_e32 v0, v1, v0
	v_min_f32_e32 v1, 0, v12
	v_cndmask_b32_e64 v4, 0, 32, vcc
	v_ldexp_f32 v3, v3, v4
	v_log_f32_e32 v3, v3
	ds_read_b128 v[4:7], v64 offset:192
	v_fmamk_f32 v0, v0, 0x3d800000, v2
	v_mul_f32_e32 v8, 0x3f317217, v3
	v_fma_f32 v12, v3, s42, -v8
	ds_read_b128 v[8:11], v64 offset:208
	s_waitcnt lgkmcnt(1)
	v_fma_f32 v13, v4, v55, v61
	v_fmac_f32_e32 v13, v5, v56
	v_fmac_f32_e32 v13, v6, v46
	v_fmac_f32_e32 v13, v7, v57
	ds_read_b128 v[4:7], v64 offset:224
	s_waitcnt lgkmcnt(1)
	v_fmac_f32_e32 v13, v8, v47
	v_fmac_f32_e32 v13, v9, v48
	v_fmac_f32_e32 v13, v10, v49
	v_fmac_f32_e32 v13, v11, v58
	ds_read_b128 v[8:11], v64 offset:240
	s_waitcnt lgkmcnt(1)
	v_fmac_f32_e32 v13, v4, v50
	v_fmac_f32_e32 v13, v5, v51
	v_fmac_f32_e32 v13, v6, v52
	v_fmac_f32_e32 v13, v7, v59
	s_waitcnt lgkmcnt(0)
	v_fmac_f32_e32 v13, v8, v53
	v_fmac_f32_e32 v13, v9, v54
	v_fmac_f32_e32 v13, v10, v60
	v_fmac_f32_e32 v13, v11, v62
	v_mul_f32_e64 v4, |v13|, s3
	v_exp_f32_e32 v4, v4
	v_fmac_f32_e32 v12, 0x3377d1cf, v3
	v_fmac_f32_e32 v12, 0x3f317217, v3
	v_cmp_lt_f32_e64 s[34:35], |v3|, s43
	v_add_f32_e32 v4, 1.0, v4
	v_cndmask_b32_e32 v5, 0, v191, vcc
	v_cndmask_b32_e64 v3, v3, v12, s[34:35]
	v_cmp_gt_f32_e32 vcc, s31, v4
	v_sub_f32_e32 v3, v3, v5
	v_sub_f32_e32 v1, v1, v3
	v_cndmask_b32_e64 v5, 0, 32, vcc
	v_ldexp_f32 v4, v4, v5
	v_log_f32_e32 v12, v4
	ds_read_b128 v[4:7], v64 offset:256
	v_min_f32_e32 v3, 0, v13
	v_fmamk_f32 v1, v1, 0x3d800000, v0
	v_mul_f32_e32 v8, 0x3f317217, v12
	v_fma_f32 v13, v12, s42, -v8
	ds_read_b128 v[8:11], v64 offset:272
	s_waitcnt lgkmcnt(1)
	v_fma_f32 v14, v4, v55, v61
	v_fmac_f32_e32 v14, v5, v56
	v_fmac_f32_e32 v14, v6, v46
	v_fmac_f32_e32 v14, v7, v57
	ds_read_b128 v[4:7], v64 offset:288
	s_waitcnt lgkmcnt(1)
	v_fmac_f32_e32 v14, v8, v47
	v_fmac_f32_e32 v14, v9, v48
	v_fmac_f32_e32 v14, v10, v49
	v_fmac_f32_e32 v14, v11, v58
	ds_read_b128 v[8:11], v64 offset:304
	s_waitcnt lgkmcnt(1)
	v_fmac_f32_e32 v14, v4, v50
	v_fmac_f32_e32 v14, v5, v51
	v_fmac_f32_e32 v14, v6, v52
	v_fmac_f32_e32 v14, v7, v59
	s_waitcnt lgkmcnt(0)
	v_fmac_f32_e32 v14, v8, v53
	v_fmac_f32_e32 v14, v9, v54
	v_fmac_f32_e32 v14, v10, v60
	v_fmac_f32_e32 v14, v11, v62
	v_mul_f32_e64 v4, |v14|, s3
	v_exp_f32_e32 v4, v4
	v_fmac_f32_e32 v13, 0x3377d1cf, v12
	v_fmac_f32_e32 v13, 0x3f317217, v12
	v_cmp_lt_f32_e64 s[34:35], |v12|, s43
	v_add_f32_e32 v4, 1.0, v4
	v_cndmask_b32_e32 v6, 0, v191, vcc
	v_cndmask_b32_e64 v5, v12, v13, s[34:35]
	v_cmp_gt_f32_e32 vcc, s31, v4
	v_sub_f32_e32 v5, v5, v6
	v_sub_f32_e32 v3, v3, v5
	v_cndmask_b32_e64 v6, 0, 32, vcc
	v_ldexp_f32 v4, v4, v6
	v_log_f32_e32 v12, v4
	ds_read_b128 v[4:7], v64 offset:320
	v_min_f32_e32 v13, 0, v14
	v_fmamk_f32 v3, v3, 0x3d800000, v1
	v_mul_f32_e32 v8, 0x3f317217, v12
	v_fma_f32 v14, v12, s42, -v8
	ds_read_b128 v[8:11], v64 offset:336
	s_waitcnt lgkmcnt(1)
	v_fma_f32 v15, v4, v55, v61
	v_fmac_f32_e32 v15, v5, v56
	v_fmac_f32_e32 v15, v6, v46
	v_fmac_f32_e32 v15, v7, v57
	ds_read_b128 v[4:7], v64 offset:352
	s_waitcnt lgkmcnt(1)
	v_fmac_f32_e32 v15, v8, v47
	v_fmac_f32_e32 v15, v9, v48
	v_fmac_f32_e32 v15, v10, v49
	v_fmac_f32_e32 v15, v11, v58
	ds_read_b128 v[8:11], v64 offset:368
	s_waitcnt lgkmcnt(1)
	v_fmac_f32_e32 v15, v4, v50
	v_fmac_f32_e32 v15, v5, v51
	v_fmac_f32_e32 v15, v6, v52
	v_fmac_f32_e32 v15, v7, v59
	s_waitcnt lgkmcnt(0)
	v_fmac_f32_e32 v15, v8, v53
	v_fmac_f32_e32 v15, v9, v54
	v_fmac_f32_e32 v15, v10, v60
	v_fmac_f32_e32 v15, v11, v62
	v_mul_f32_e64 v4, |v15|, s3
	v_exp_f32_e32 v4, v4
	v_fmac_f32_e32 v14, 0x3377d1cf, v12
	v_fmac_f32_e32 v14, 0x3f317217, v12
	v_cmp_lt_f32_e64 s[34:35], |v12|, s43
	v_add_f32_e32 v4, 1.0, v4
	v_cndmask_b32_e32 v6, 0, v191, vcc
	v_cndmask_b32_e64 v5, v12, v14, s[34:35]
	v_cmp_gt_f32_e32 vcc, s31, v4
	v_sub_f32_e32 v5, v5, v6
	v_sub_f32_e32 v5, v13, v5
	v_cndmask_b32_e64 v6, 0, 32, vcc
	v_ldexp_f32 v4, v4, v6
	v_log_f32_e32 v4, v4
	ds_read_b128 v[6:9], v64 offset:384
	v_min_f32_e32 v14, 0, v15
	v_fmamk_f32 v5, v5, 0x3d800000, v3
	v_mul_f32_e32 v10, 0x3f317217, v4
	v_fma_f32 v15, v4, s42, -v10
	ds_read_b128 v[10:13], v64 offset:400
	s_waitcnt lgkmcnt(1)
	v_fma_f32 v44, v6, v55, v61
	v_fmac_f32_e32 v44, v7, v56
	v_fmac_f32_e32 v44, v8, v46
	v_fmac_f32_e32 v44, v9, v57
	ds_read_b128 v[6:9], v64 offset:416
	s_waitcnt lgkmcnt(1)
	v_fmac_f32_e32 v44, v10, v47
	v_fmac_f32_e32 v44, v11, v48
	v_fmac_f32_e32 v44, v12, v49
	v_fmac_f32_e32 v44, v13, v58
	ds_read_b128 v[10:13], v64 offset:432
	s_waitcnt lgkmcnt(1)
	v_fmac_f32_e32 v44, v6, v50
	v_fmac_f32_e32 v44, v7, v51
	v_fmac_f32_e32 v44, v8, v52
	v_fmac_f32_e32 v44, v9, v59
	s_waitcnt lgkmcnt(0)
; #define LAS __attribute__((address_space(3)))
; __device__ __forceinline__ void gla_local_unit(LAS unsigned char* lds, GlaPre& R, const bf16_t* proj, const float* alow, const float (&w2)[16], const float bias, ...
;     ...
;     float bl[16]; float run = 0.f;
; #pragma unroll
;     for (int ii = 0; ii < 16; ++ii) { float z = bias; const LAS f32x4* ap = (const LAS f32x4*)(ALs + (16 * ig + ii) * 16);
; #pragma unroll
;         for (int r4 = 0; r4 < 4; ++r4) { const f32x4 av = ap[r4]; z = fmaf(av[0], w2[4 * r4], z); z = fmaf(av[1], w2[4 * r4 + 1], z); z = fmaf(av[2], w2[4 * r4 + 2], z); z = fmaf(av[3], w2[4 * r4 + 3], z); }
;         const float la = (fminf(z, 0.f) - __logf(1.0f + __expf(-fabsf(z)))) * 0.0625f; run += la; bl[ii] = run; }
	v_fmac_f32_e32 v44, v10, v53
	v_fmac_f32_e32 v44, v11, v54
	v_fmac_f32_e32 v44, v12, v60
	v_fmac_f32_e32 v44, v13, v62
	v_mul_f32_e64 v6, |v44|, s3
	v_exp_f32_e32 v6, v6
	v_fmac_f32_e32 v15, 0x3377d1cf, v4
	v_fmac_f32_e32 v15, 0x3f317217, v4
	v_cmp_lt_f32_e64 s[34:35], |v4|, s43
	v_add_f32_e32 v6, 1.0, v6
	v_cndmask_b32_e32 v7, 0, v191, vcc
	v_cndmask_b32_e64 v4, v4, v15, s[34:35]
	v_cmp_gt_f32_e32 vcc, s31, v6
	v_sub_f32_e32 v4, v4, v7
	ds_read_b128 v[8:11], v64 offset:448
	v_cndmask_b32_e64 v7, 0, 32, vcc
	v_ldexp_f32 v6, v6, v7
	v_log_f32_e32 v7, v6
	v_sub_f32_e32 v4, v14, v4
	v_fmamk_f32 v6, v4, 0x3d800000, v5
	v_min_f32_e32 v4, 0, v44
	v_mul_f32_e32 v12, 0x3f317217, v7
	v_fma_f32 v44, v7, s42, -v12
	ds_read_b128 v[12:15], v64 offset:464
	s_waitcnt lgkmcnt(1)
	v_fma_f32 v45, v8, v55, v61
	v_fmac_f32_e32 v45, v9, v56
	v_fmac_f32_e32 v45, v10, v46
	v_fmac_f32_e32 v45, v11, v57
	ds_read_b128 v[8:11], v64 offset:480
	s_waitcnt lgkmcnt(1)
	v_fmac_f32_e32 v45, v12, v47
	v_fmac_f32_e32 v45, v13, v48
	v_fmac_f32_e32 v45, v14, v49
	v_fmac_f32_e32 v45, v15, v58
	ds_read_b128 v[12:15], v64 offset:496
	s_waitcnt lgkmcnt(1)
	v_fmac_f32_e32 v45, v8, v50
	v_fmac_f32_e32 v45, v9, v51
	v_fmac_f32_e32 v45, v10, v52
	v_fmac_f32_e32 v45, v11, v59
	s_waitcnt lgkmcnt(0)
	v_fmac_f32_e32 v45, v12, v53
	v_fmac_f32_e32 v45, v13, v54
	v_fmac_f32_e32 v45, v14, v60
	v_fmac_f32_e32 v45, v15, v62
	v_mul_f32_e64 v8, |v45|, s3
	v_exp_f32_e32 v8, v8
	v_fmac_f32_e32 v44, 0x3377d1cf, v7
	v_fmac_f32_e32 v44, 0x3f317217, v7
	v_cmp_lt_f32_e64 s[34:35], |v7|, s43
	v_add_f32_e32 v8, 1.0, v8
	v_cndmask_b32_e32 v9, 0, v191, vcc
	v_cndmask_b32_e64 v7, v7, v44, s[34:35]
	v_cmp_gt_f32_e32 vcc, s31, v8
	v_sub_f32_e32 v7, v7, v9
	v_sub_f32_e32 v4, v4, v7
	v_cndmask_b32_e64 v9, 0, 32, vcc
	v_ldexp_f32 v8, v8, v9
	v_log_f32_e32 v44, v8
	ds_read_b128 v[8:11], v64 offset:512
	v_fmamk_f32 v7, v4, 0x3d800000, v6
	v_min_f32_e32 v4, 0, v45
	v_mul_f32_e32 v12, 0x3f317217, v44
	v_fma_f32 v45, v44, s42, -v12
	ds_read_b128 v[12:15], v64 offset:528
	s_waitcnt lgkmcnt(1)
	v_fma_f32 v91, v8, v55, v61
	v_fmac_f32_e32 v91, v9, v56
	v_fmac_f32_e32 v91, v10, v46
	v_fmac_f32_e32 v91, v11, v57
	ds_read_b128 v[8:11], v64 offset:544
	s_waitcnt lgkmcnt(1)
	v_fmac_f32_e32 v91, v12, v47
	v_fmac_f32_e32 v91, v13, v48
	v_fmac_f32_e32 v91, v14, v49
	v_fmac_f32_e32 v91, v15, v58
	ds_read_b128 v[12:15], v64 offset:560
	s_waitcnt lgkmcnt(1)
	v_fmac_f32_e32 v91, v8, v50
	v_fmac_f32_e32 v91, v9, v51
	v_fmac_f32_e32 v91, v10, v52
	v_fmac_f32_e32 v91, v11, v59
	s_waitcnt lgkmcnt(0)
	v_fmac_f32_e32 v91, v12, v53
	v_fmac_f32_e32 v91, v13, v54
	v_fmac_f32_e32 v91, v14, v60
	v_fmac_f32_e32 v91, v15, v62
	ds_read_b128 v[12:15], v64 offset:576
	v_fmac_f32_e32 v45, 0x3377d1cf, v44
	v_fmac_f32_e32 v45, 0x3f317217, v44
	v_cmp_lt_f32_e64 s[34:35], |v44|, s43
	v_mul_f32_e64 v8, |v91|, s3
	v_exp_f32_e32 v8, v8
	v_cndmask_b32_e64 v9, v44, v45, s[34:35]
	s_waitcnt lgkmcnt(0)
	v_fma_f32 v44, v12, v55, v61
	v_fmac_f32_e32 v44, v13, v56
	v_fmac_f32_e32 v44, v14, v46
	v_fmac_f32_e32 v44, v15, v57
	ds_read_b128 v[12:15], v64 offset:608
	v_fmac_f32_e32 v44, v92, v47
	v_fmac_f32_e32 v44, v93, v48
	v_fmac_f32_e32 v44, v94, v49
	v_fmac_f32_e32 v44, v95, v58
	ds_read_b128 v[92:95], v64 offset:624
	v_add_f32_e32 v8, 1.0, v8
	s_waitcnt lgkmcnt(1)
	v_fmac_f32_e32 v44, v12, v50
	v_cndmask_b32_e32 v10, 0, v191, vcc
	v_cmp_gt_f32_e32 vcc, s31, v8
	v_fmac_f32_e32 v44, v13, v51
	v_sub_f32_e32 v9, v9, v10
	v_cndmask_b32_e64 v10, 0, 32, vcc
	v_fmac_f32_e32 v44, v14, v52
	v_ldexp_f32 v8, v8, v10
	v_fmac_f32_e32 v44, v15, v59
	v_log_f32_e32 v8, v8
	s_waitcnt lgkmcnt(0)
	v_fmac_f32_e32 v44, v92, v53
	v_fmac_f32_e32 v44, v93, v54
	v_fmac_f32_e32 v44, v94, v60
	v_fmac_f32_e32 v44, v95, v62
	v_sub_f32_e32 v4, v4, v9
	v_mul_f32_e32 v9, 0x3f317217, v8
	v_mul_f32_e64 v11, |v44|, s3
	v_fma_f32 v9, v8, s42, -v9
	v_exp_f32_e32 v11, v11
	v_fmac_f32_e32 v9, 0x3377d1cf, v8
	v_fmac_f32_e32 v9, 0x3f317217, v8
	v_cmp_lt_f32_e64 s[34:35], |v8|, s43
	ds_read_b128 v[12:15], v64 offset:640
	ds_read_b128 v[92:95], v64 offset:656
	v_cndmask_b32_e64 v8, v8, v9, s[34:35]
	v_cndmask_b32_e32 v9, 0, v191, vcc
	v_sub_f32_e32 v8, v8, v9
	v_add_f32_e32 v9, 1.0, v11
	v_fmamk_f32 v10, v4, 0x3d800000, v7
	v_min_f32_e32 v4, 0, v91
	v_cmp_gt_f32_e32 vcc, s31, v9
	v_sub_f32_e32 v4, v4, v8
	s_nop 0
	v_cndmask_b32_e64 v11, 0, 32, vcc
	v_ldexp_f32 v9, v9, v11
	v_fmamk_f32 v11, v4, 0x3d800000, v10
	v_min_f32_e32 v4, 0, v44
	s_waitcnt lgkmcnt(1)
	v_fma_f32 v44, v12, v55, v61
	v_fmac_f32_e32 v44, v13, v56
	v_fmac_f32_e32 v44, v14, v46
	v_fmac_f32_e32 v44, v15, v57
	ds_read_b128 v[12:15], v64 offset:672
	s_waitcnt lgkmcnt(1)
	v_fmac_f32_e32 v44, v92, v47
	v_fmac_f32_e32 v44, v93, v48
	v_fmac_f32_e32 v44, v94, v49
	v_fmac_f32_e32 v44, v95, v58
	ds_read_b128 v[92:95], v64 offset:688
	s_waitcnt lgkmcnt(1)
	v_fmac_f32_e32 v44, v12, v50
	v_fmac_f32_e32 v44, v13, v51
	v_fmac_f32_e32 v44, v14, v52
	v_fmac_f32_e32 v44, v15, v59
	v_log_f32_e32 v9, v9
	s_waitcnt lgkmcnt(0)
	v_fmac_f32_e32 v44, v92, v53
	v_fmac_f32_e32 v44, v93, v54
	v_fmac_f32_e32 v44, v94, v60
	v_fmac_f32_e32 v44, v95, v62
	v_mul_f32_e32 v8, 0x3f317217, v9
	v_mul_f32_e64 v12, |v44|, s3
	v_fma_f32 v8, v9, s42, -v8
	v_exp_f32_e32 v12, v12
	v_fmac_f32_e32 v8, 0x3377d1cf, v9
	v_fmac_f32_e32 v8, 0x3f317217, v9
	v_cmp_lt_f32_e64 s[34:35], |v9|, s43
	ds_read_b128 v[92:95], v64 offset:720
	s_nop 0
	v_cndmask_b32_e64 v8, v9, v8, s[34:35]
	v_cndmask_b32_e32 v9, 0, v191, vcc
	v_sub_f32_e32 v8, v8, v9
	v_add_f32_e32 v9, 1.0, v12
	v_cmp_gt_f32_e32 vcc, s31, v9
	v_sub_f32_e32 v4, v4, v8
	v_fmamk_f32 v8, v4, 0x3d800000, v11
	v_cndmask_b32_e64 v12, 0, 32, vcc
	v_ldexp_f32 v9, v9, v12
	ds_read_b128 v[12:15], v64 offset:704
	v_log_f32_e32 v9, v9
	v_min_f32_e32 v4, 0, v44
	s_waitcnt lgkmcnt(0)
; #define LAS __attribute__((address_space(3)))
; __device__ __forceinline__ void gla_local_unit(LAS unsigned char* lds, GlaPre& R, const bf16_t* proj, const float* alow, const float (&w2)[16], const float bias, ...
;     ...
;     float bl[16]; float run = 0.f;
; #pragma unroll
;     for (int ii = 0; ii < 16; ++ii) { float z = bias; const LAS f32x4* ap = (const LAS f32x4*)(ALs + (16 * ig + ii) * 16);
; #pragma unroll
;         for (int r4 = 0; r4 < 4; ++r4) { const f32x4 av = ap[r4]; z = fmaf(av[0], w2[4 * r4], z); z = fmaf(av[1], w2[4 * r4 + 1], z); z = fmaf(av[2], w2[4 * r4 + 2], z); z = fmaf(av[3], w2[4 * r4 + 3], z); }
;         const float la = (fminf(z, 0.f) - __logf(1.0f + __expf(-fabsf(z)))) * 0.0625f; run += la; bl[ii] = run; }
;     CS[ig * 128 + d] = run;
;     __syncthreads();
	v_fma_f32 v45, v12, v55, v61
	v_fmac_f32_e32 v45, v13, v56
	v_fmac_f32_e32 v45, v14, v46
	v_fmac_f32_e32 v45, v15, v57
	ds_read_b128 v[12:15], v64 offset:736
	v_fmac_f32_e32 v45, v92, v47
	v_fmac_f32_e32 v45, v93, v48
	v_fmac_f32_e32 v45, v94, v49
	v_fmac_f32_e32 v45, v95, v58
	ds_read_b128 v[92:95], v64 offset:752
	s_waitcnt lgkmcnt(1)
	v_fmac_f32_e32 v45, v12, v50
	v_fmac_f32_e32 v45, v13, v51
	v_fmac_f32_e32 v45, v14, v52
	v_fmac_f32_e32 v45, v15, v59
	s_waitcnt lgkmcnt(0)
	v_fmac_f32_e32 v45, v92, v53
	v_fmac_f32_e32 v45, v93, v54
	v_fmac_f32_e32 v45, v94, v60
	v_fmac_f32_e32 v45, v95, v62
	v_mul_f32_e64 v12, |v45|, s3
	v_exp_f32_e32 v12, v12
	v_mul_f32_e32 v44, 0x3f317217, v9
	v_fma_f32 v44, v9, s42, -v44
	v_fmac_f32_e32 v44, 0x3377d1cf, v9
	v_fmac_f32_e32 v44, 0x3f317217, v9
	v_cmp_lt_f32_e64 s[34:35], |v9|, s43
	v_add_f32_e32 v12, 1.0, v12
	v_cndmask_b32_e32 v13, 0, v191, vcc
	v_cndmask_b32_e64 v9, v9, v44, s[34:35]
	v_cmp_gt_f32_e32 vcc, s31, v12
	v_sub_f32_e32 v9, v9, v13
	ds_read_b128 v[92:95], v64 offset:784
	v_cndmask_b32_e64 v13, 0, 32, vcc
	v_ldexp_f32 v12, v12, v13
	v_log_f32_e32 v44, v12
	ds_read_b128 v[12:15], v64 offset:768
	v_sub_f32_e32 v4, v4, v9
	v_fmamk_f32 v9, v4, 0x3d800000, v8
	v_min_f32_e32 v4, 0, v45
	v_mul_f32_e32 v45, 0x3f317217, v44
	s_waitcnt lgkmcnt(0)
	v_fma_f32 v91, v12, v55, v61
	v_fmac_f32_e32 v91, v13, v56
	v_fmac_f32_e32 v91, v14, v46
	v_fmac_f32_e32 v91, v15, v57
	ds_read_b128 v[12:15], v64 offset:800
	v_fmac_f32_e32 v91, v92, v47
	v_fmac_f32_e32 v91, v93, v48
	v_fmac_f32_e32 v91, v94, v49
	v_fmac_f32_e32 v91, v95, v58
	ds_read_b128 v[92:95], v64 offset:816
	s_waitcnt lgkmcnt(1)
	v_fmac_f32_e32 v91, v12, v50
	v_fmac_f32_e32 v91, v13, v51
	v_fmac_f32_e32 v91, v14, v52
	v_fmac_f32_e32 v91, v15, v59
	s_waitcnt lgkmcnt(0)
	v_fmac_f32_e32 v91, v92, v53
	v_fmac_f32_e32 v91, v93, v54
	v_fmac_f32_e32 v91, v94, v60
	v_fmac_f32_e32 v91, v95, v62
	ds_read_b128 v[92:95], v64 offset:832
	v_mul_f32_e64 v12, |v91|, s3
	v_exp_f32_e32 v12, v12
	v_fma_f32 v45, v44, s42, -v45
	v_fmac_f32_e32 v45, 0x3377d1cf, v44
	s_waitcnt lgkmcnt(0)
	v_fma_f32 v15, v92, v55, v61
	v_fmac_f32_e32 v15, v93, v56
	v_fmac_f32_e32 v15, v94, v46
	v_fmac_f32_e32 v15, v95, v57
	ds_read_b128 v[92:95], v64 offset:864
	v_fmac_f32_e32 v15, v96, v47
	v_fmac_f32_e32 v15, v97, v48
	v_fmac_f32_e32 v15, v98, v49
	v_fmac_f32_e32 v15, v99, v58
	ds_read_b128 v[96:99], v64 offset:880
	v_fmac_f32_e32 v45, 0x3f317217, v44
	v_cmp_lt_f32_e64 s[34:35], |v44|, s43
	v_add_f32_e32 v12, 1.0, v12
	s_waitcnt lgkmcnt(1)
	v_fmac_f32_e32 v15, v92, v50
	v_cndmask_b32_e64 v13, v44, v45, s[34:35]
	v_cndmask_b32_e32 v14, 0, v191, vcc
	v_cmp_gt_f32_e32 vcc, s31, v12
	v_fmac_f32_e32 v15, v93, v51
	v_sub_f32_e32 v13, v13, v14
	v_cndmask_b32_e64 v14, 0, 32, vcc
	v_fmac_f32_e32 v15, v94, v52
	v_ldexp_f32 v12, v12, v14
	v_fmac_f32_e32 v15, v95, v59
	v_log_f32_e32 v14, v12
	s_waitcnt lgkmcnt(0)
	v_fmac_f32_e32 v15, v96, v53
	v_fmac_f32_e32 v15, v97, v54
	v_fmac_f32_e32 v15, v98, v60
	v_fmac_f32_e32 v15, v99, v62
	v_sub_f32_e32 v4, v4, v13
	v_mul_f32_e32 v13, 0x3f317217, v14
	v_mul_f32_e64 v44, |v15|, s3
	v_fma_f32 v13, v14, s42, -v13
	v_exp_f32_e32 v44, v44
	v_fmac_f32_e32 v13, 0x3377d1cf, v14
	v_fmac_f32_e32 v13, 0x3f317217, v14
	v_cmp_lt_f32_e64 s[34:35], |v14|, s43
	ds_read_b128 v[92:95], v64 offset:896
	ds_read_b128 v[96:99], v64 offset:912
	v_cndmask_b32_e64 v13, v14, v13, s[34:35]
	v_cndmask_b32_e32 v14, 0, v191, vcc
	v_sub_f32_e32 v13, v13, v14
	v_add_f32_e32 v14, 1.0, v44
	v_cmp_gt_f32_e32 vcc, s31, v14
	v_fmamk_f32 v12, v4, 0x3d800000, v9
	v_min_f32_e32 v4, 0, v91
	v_cndmask_b32_e64 v44, 0, 32, vcc
	v_ldexp_f32 v14, v14, v44
	s_waitcnt lgkmcnt(1)
	v_fma_f32 v44, v92, v55, v61
	v_fmac_f32_e32 v44, v93, v56
	v_fmac_f32_e32 v44, v94, v46
	v_fmac_f32_e32 v44, v95, v57
	ds_read_b128 v[92:95], v64 offset:928
	s_waitcnt lgkmcnt(1)
	v_fmac_f32_e32 v44, v96, v47
	v_fmac_f32_e32 v44, v97, v48
	v_fmac_f32_e32 v44, v98, v49
	v_fmac_f32_e32 v44, v99, v58
	ds_read_b128 v[96:99], v64 offset:944
	s_waitcnt lgkmcnt(1)
	v_fmac_f32_e32 v44, v92, v50
	v_fmac_f32_e32 v44, v93, v51
	v_fmac_f32_e32 v44, v94, v52
	v_fmac_f32_e32 v44, v95, v59
	v_log_f32_e32 v14, v14
	s_waitcnt lgkmcnt(0)
	v_fmac_f32_e32 v44, v96, v53
	v_fmac_f32_e32 v44, v97, v54
	v_fmac_f32_e32 v44, v98, v60
	v_sub_f32_e32 v4, v4, v13
	v_fmac_f32_e32 v44, v99, v62
	v_fmamk_f32 v13, v4, 0x3d800000, v12
	v_min_f32_e32 v4, 0, v15
	v_mul_f32_e32 v15, 0x3f317217, v14
	v_mul_f32_e64 v45, |v44|, s3
	v_fma_f32 v15, v14, s42, -v15
	v_exp_f32_e32 v45, v45
	v_fmac_f32_e32 v15, 0x3377d1cf, v14
	v_fmac_f32_e32 v15, 0x3f317217, v14
	v_cmp_lt_f32_e64 s[34:35], |v14|, s43
	ds_read_b128 v[92:95], v64 offset:960
	ds_read_b128 v[96:99], v64 offset:976
	v_cndmask_b32_e64 v14, v14, v15, s[34:35]
	v_cndmask_b32_e32 v15, 0, v191, vcc
	v_sub_f32_e32 v14, v14, v15
	v_add_f32_e32 v15, 1.0, v45
	v_cmp_gt_f32_e32 vcc, s31, v15
	v_sub_f32_e32 v4, v4, v14
	v_fmamk_f32 v14, v4, 0x3d800000, v13
	v_cndmask_b32_e64 v45, 0, 32, vcc
	v_ldexp_f32 v15, v15, v45
	s_waitcnt lgkmcnt(1)
	v_fma_f32 v45, v92, v55, v61
	v_fmac_f32_e32 v45, v93, v56
	v_fmac_f32_e32 v45, v94, v46
	v_fmac_f32_e32 v45, v95, v57
	ds_read_b128 v[92:95], v64 offset:992
	s_waitcnt lgkmcnt(1)
	v_fmac_f32_e32 v45, v96, v47
	v_fmac_f32_e32 v45, v97, v48
	v_fmac_f32_e32 v45, v98, v49
	v_fmac_f32_e32 v45, v99, v58
	ds_read_b128 v[96:99], v64 offset:1008
	s_waitcnt lgkmcnt(1)
	v_fmac_f32_e32 v45, v92, v50
	v_fmac_f32_e32 v45, v93, v51
	v_fmac_f32_e32 v45, v94, v52
	v_fmac_f32_e32 v45, v95, v59
	v_log_f32_e32 v15, v15
	s_waitcnt lgkmcnt(0)
	v_fmac_f32_e32 v45, v96, v53
	v_fmac_f32_e32 v45, v97, v54
	v_fmac_f32_e32 v45, v98, v60
	v_fmac_f32_e32 v45, v99, v62
	v_min_f32_e32 v4, 0, v44
	v_mul_f32_e32 v44, 0x3f317217, v15
	v_mul_f32_e64 v91, |v45|, s3
	v_fma_f32 v44, v15, s42, -v44
	v_exp_f32_e32 v91, v91
	v_fmac_f32_e32 v44, 0x3377d1cf, v15
	v_fmac_f32_e32 v44, 0x3f317217, v15
	v_cmp_lt_f32_e64 s[34:35], |v15|, s43
	s_nop 1
	v_cndmask_b32_e64 v15, v15, v44, s[34:35]
	v_cndmask_b32_e32 v44, 0, v191, vcc
	v_sub_f32_e32 v15, v15, v44
	v_add_f32_e32 v44, 1.0, v91
	v_cmp_gt_f32_e32 vcc, s31, v44
	v_sub_f32_e32 v4, v4, v15
	v_fmamk_f32 v15, v4, 0x3d800000, v14
	v_cndmask_b32_e64 v91, 0, 32, vcc
	v_ldexp_f32 v44, v44, v91
	v_log_f32_e32 v44, v44
	v_min_f32_e32 v4, 0, v45
	v_mul_f32_e32 v45, 0x3f317217, v44
	v_fma_f32 v45, v44, s42, -v45
	v_fmac_f32_e32 v45, 0x3377d1cf, v44
	v_fmac_f32_e32 v45, 0x3f317217, v44
	v_cmp_lt_f32_e64 s[34:35], |v44|, s43
	s_nop 1
	v_cndmask_b32_e64 v44, v44, v45, s[34:35]
	v_cndmask_b32_e32 v45, 0, v191, vcc
	v_sub_f32_e32 v44, v44, v45
	v_sub_f32_e32 v4, v4, v44
	v_fmamk_f32 v44, v4, 0x3d800000, v15
	ds_write_b32 v65, v44
	s_waitcnt lgkmcnt(0)
	s_barrier
; #define LAS __attribute__((address_space(3)))
; __device__ __forceinline__ unsigned f2bf(float f) { unsigned u = __builtin_bit_cast(unsigned, f); return (u + 0x7fffu + ((u >> 16) & 1u)) >> 16; }
; __device__ __forceinline__ void gla_local_unit(LAS unsigned char* lds, GlaPre& R, const bf16_t* proj, const float* alow, const float (&w2)[16], const float bias, ...
;     ...
;     float pre = 0.f, tot = 0.f;
; #pragma unroll
;     for (int g2 = 0; g2 < 4; ++g2) { const float cv = CS[g2 * 128 + d]; tot += cv; pre += (g2 < ig) ? cv : 0.f; }
;     const float qscale = 0.08838834764831845f; const float etot = __expf(tot);
;     unsigned ke[8];
; #pragma unroll
;     for (int ii = 0; ii < 16; ++ii) { const float bb = pre + bl[ii];
;         LAS bf16_t* qp = (LAS bf16_t*)(QD + (16 * ig + ii) * 272 + 2 * d); LAS bf16_t* kp = (LAS bf16_t*)(KI + (16 * ig + ii) * 272 + 2 * d);
;         const float qf_ = bf2f(*qp), kf_ = bf2f(*kp);
;         const float eb = __expf(bb), einv = __builtin_amdgcn_rcpf(eb);
;         const float qd = qf_ * qscale * eb, ki = kf_ * einv, kend = kf_ * (etot * einv);
;         *qp = (bf16_t)f2bf(qd); *kp = (bf16_t)f2bf(ki);
;         if (ii & 1) ke[ii >> 1] |= f2bf(kend) << 16; else ke[ii >> 1] = f2bf(kend); }
;     *(LAS u32x4*)(KET + d * 144 + 32 * ig) = (u32x4){ke[0], ke[1], ke[2], ke[3]}; *(LAS u32x4*)(KET + d * 144 + 32 * ig + 16) = (u32x4){ke[4], ke[5], ke[6], ke[7]};
	ds_read2st64_b32 v[92:93], v66 offset1:2
	ds_read2st64_b32 v[94:95], v66 offset0:4 offset1:6
	s_waitcnt lgkmcnt(1)
	v_add_f32_e32 v4, 0, v92
	v_cndmask_b32_e64 v45, 0, v4, s[4:5]
	v_cndmask_b32_e64 v91, 0, v93, s[6:7]
	v_add_f32_e32 v45, v45, v91
	s_waitcnt lgkmcnt(0)
	v_cndmask_b32_e64 v91, 0, v94, s[8:9]
	v_add_f32_e32 v45, v45, v91
	v_cndmask_b32_e64 v91, 0, v95, s[10:11]
	v_add_f32_e32 v45, v45, v91
	v_add_f32_e32 v2, v2, v45
	v_mul_f32_e32 v2, 0x3fb8aa3b, v2
	v_exp_f32_e32 v2, v2
	ds_read_u16 v91, v77
	ds_read_u16 v92, v77 offset:272
	ds_read_u16 v96, v77 offset:544
	ds_read_u16 v97, v77 offset:816
	ds_read_u16 v98, v77 offset:1088
	ds_read_u16 v99, v77 offset:1360
	ds_read_u16 v100, v77 offset:1632
	ds_read_u16 v101, v77 offset:1904
	s_waitcnt lgkmcnt(7)
	v_lshlrev_b32_e32 v91, 16, v91
	v_mul_f32_e32 v91, 0x3db504f3, v91
	v_add_f32_e32 v4, v4, v93
	v_rcp_f32_e32 v93, v2
	v_mul_f32_e32 v2, v2, v91
	v_bfe_u32 v91, v2, 16, 1
	v_add_f32_e32 v0, v0, v45
	v_mul_f32_e32 v0, 0x3fb8aa3b, v0
	v_add3_u32 v2, v2, v91, s33
	v_exp_f32_e32 v0, v0
	ds_write_b16_d16_hi v77, v2
	v_add_f32_e32 v4, v4, v94
	ds_read_u16 v91, v77 offset:17680
	ds_read_u16 v102, v77 offset:18224
	ds_read_u16 v103, v77 offset:18496
	ds_read_u16 v104, v77 offset:18768
	ds_read_u16 v105, v77 offset:19040
	ds_read_u16 v106, v77 offset:19312
	ds_read_u16 v107, v77 offset:17952
	ds_read_u16 v94, v77 offset:17408
	s_waitcnt lgkmcnt(14)
	v_lshlrev_b32_e32 v2, 16, v92
	v_mul_f32_e32 v2, 0x3db504f3, v2
	v_rcp_f32_e32 v92, v0
	v_mul_f32_e32 v0, v0, v2
	v_add_f32_e32 v4, v4, v95
	v_bfe_u32 v2, v0, 16, 1
	v_mul_f32_e32 v4, 0x3fb8aa3b, v4
	v_add3_u32 v0, v0, v2, s33
	s_waitcnt lgkmcnt(0)
	v_lshlrev_b32_e32 v95, 16, v94
	v_exp_f32_e32 v4, v4
	ds_write_b16_d16_hi v77, v0 offset:272
	v_mul_f32_e32 v0, v93, v95
	v_bfe_u32 v2, v0, 16, 1
	v_lshlrev_b32_e32 v94, 16, v91
	v_add3_u32 v0, v0, v2, s33
	ds_write_b16_d16_hi v77, v0 offset:17408
	v_mul_f32_e32 v0, v92, v94
	v_bfe_u32 v2, v0, 16, 1
	v_pk_mul_f32 v[92:93], v[4:5], v[92:93] op_sel_hi:[0,1]
	v_add3_u32 v0, v0, v2, s33
	v_pk_mul_f32 v[92:93], v[92:93], v[94:95]
	v_add_f32_e32 v1, v1, v45
	ds_write_b16_d16_hi v77, v0 offset:17680
	v_and_b32_sdwa v0, v93, v188 dst_sel:DWORD dst_unused:UNUSED_PAD src0_sel:WORD_1 src1_sel:DWORD
	v_mul_f32_e32 v1, 0x3fb8aa3b, v1
	v_and_b32_sdwa v2, v92, v188 dst_sel:DWORD dst_unused:UNUSED_PAD src0_sel:WORD_1 src1_sel:DWORD
	v_add3_u32 v0, v93, v0, s33
	v_exp_f32_e32 v1, v1
	v_add3_u32 v2, v92, v2, s33
	v_lshrrev_b32_e32 v0, 16, v0
	v_and_or_b32 v0, v2, s2, v0
	v_lshlrev_b32_e32 v2, 16, v96
	v_mul_f32_e32 v2, 0x3db504f3, v2
	v_add_f32_e32 v3, v3, v45
	v_rcp_f32_e32 v93, v1
	v_mul_f32_e32 v1, v1, v2
	v_mul_f32_e32 v3, 0x3fb8aa3b, v3
	v_bfe_u32 v2, v1, 16, 1
	v_exp_f32_e32 v3, v3
	v_add3_u32 v1, v1, v2, s33
	ds_write_b16_d16_hi v77, v1 offset:544
	v_lshlrev_b32_e32 v1, 16, v97
	v_mul_f32_e32 v1, 0x3db504f3, v1
	v_mul_f32_e32 v1, v3, v1
	v_bfe_u32 v2, v1, 16, 1
	v_rcp_f32_e32 v92, v3
	v_add3_u32 v1, v1, v2, s33
	v_lshlrev_b32_e32 v3, 16, v107
	ds_write_b16_d16_hi v77, v1 offset:816
	v_mul_f32_e32 v1, v93, v3
	v_bfe_u32 v91, v1, 16, 1
	v_lshlrev_b32_e32 v2, 16, v102
	v_add3_u32 v1, v1, v91, s33
	ds_write_b16_d16_hi v77, v1 offset:17952
	v_mul_f32_e32 v1, v92, v2
	v_bfe_u32 v91, v1, 16, 1
	v_pk_mul_f32 v[92:93], v[4:5], v[92:93] op_sel_hi:[0,1]
	v_add3_u32 v1, v1, v91, s33
	v_pk_mul_f32 v[2:3], v[92:93], v[2:3]
	ds_write_b16_d16_hi v77, v1 offset:18224
	v_and_b32_sdwa v1, v3, v188 dst_sel:DWORD dst_unused:UNUSED_PAD src0_sel:WORD_1 src1_sel:DWORD
	v_add3_u32 v1, v3, v1, s33
	v_add_f32_e32 v3, v5, v45
	v_mul_f32_e32 v3, 0x3fb8aa3b, v3
	v_and_b32_sdwa v91, v2, v188 dst_sel:DWORD dst_unused:UNUSED_PAD src0_sel:WORD_1 src1_sel:DWORD
	v_exp_f32_e32 v5, v3
	v_add3_u32 v2, v2, v91, s33
	v_lshrrev_b32_e32 v1, 16, v1
	v_and_or_b32 v1, v2, s2, v1
	v_lshlrev_b32_e32 v2, 16, v98
	v_add_f32_e32 v6, v6, v45
	v_mul_f32_e32 v2, 0x3db504f3, v2
	v_mul_f32_e32 v6, 0x3fb8aa3b, v6
	v_mul_f32_e32 v2, v5, v2
	v_exp_f32_e32 v6, v6
	v_rcp_f32_e32 v3, v5
	v_bfe_u32 v5, v2, 16, 1
	v_add3_u32 v2, v2, v5, s33
	v_lshlrev_b32_e32 v5, 16, v99
	v_mul_f32_e32 v5, 0x3db504f3, v5
	v_mul_f32_e32 v5, v6, v5
	ds_write_b16_d16_hi v77, v2 offset:1088
	v_rcp_f32_e32 v2, v6
	v_bfe_u32 v6, v5, 16, 1
	v_add3_u32 v5, v5, v6, s33
	v_lshlrev_b32_e32 v93, 16, v103
	ds_write_b16_d16_hi v77, v5 offset:1360
	v_mul_f32_e32 v5, v3, v93
	v_bfe_u32 v6, v5, 16, 1
	v_lshlrev_b32_e32 v92, 16, v104
	v_add3_u32 v5, v5, v6, s33
	ds_write_b16_d16_hi v77, v5 offset:18496
	v_mul_f32_e32 v5, v2, v92
	v_bfe_u32 v6, v5, 16, 1
	v_add3_u32 v5, v5, v6, s33
	v_pk_mul_f32 v[2:3], v[4:5], v[2:3] op_sel_hi:[0,1]
	v_pk_mul_f32 v[2:3], v[2:3], v[92:93]
	ds_write_b16_d16_hi v77, v5 offset:18768
	v_and_b32_sdwa v5, v3, v188 dst_sel:DWORD dst_unused:UNUSED_PAD src0_sel:WORD_1 src1_sel:DWORD
	v_add3_u32 v3, v3, v5, s33
	v_add_f32_e32 v5, v7, v45
	v_mul_f32_e32 v5, 0x3fb8aa3b, v5
	v_and_b32_sdwa v6, v2, v188 dst_sel:DWORD dst_unused:UNUSED_PAD src0_sel:WORD_1 src1_sel:DWORD
	v_exp_f32_e32 v5, v5
	v_add3_u32 v2, v2, v6, s33
	v_lshrrev_b32_e32 v3, 16, v3
	v_and_or_b32 v2, v2, s2, v3
	v_lshlrev_b32_e32 v3, 16, v100
	v_mul_f32_e32 v3, 0x3db504f3, v3
	v_add_f32_e32 v6, v10, v45
	v_mul_f32_e32 v3, v5, v3
	v_mul_f32_e32 v6, 0x3fb8aa3b, v6
	v_rcp_f32_e32 v7, v5
	v_bfe_u32 v5, v3, 16, 1
	v_exp_f32_e32 v10, v6
	v_add3_u32 v3, v3, v5, s33
	ds_write_b16_d16_hi v77, v3 offset:1632
	v_lshlrev_b32_e32 v3, 16, v101
	v_mul_f32_e32 v3, 0x3db504f3, v3
	v_mul_f32_e32 v3, v10, v3
	v_bfe_u32 v5, v3, 16, 1
	v_rcp_f32_e32 v6, v10
	v_add3_u32 v3, v3, v5, s33
	v_lshlrev_b32_e32 v93, 16, v105
	ds_write_b16_d16_hi v77, v3 offset:1904
	v_mul_f32_e32 v3, v7, v93
	v_bfe_u32 v5, v3, 16, 1
	v_lshlrev_b32_e32 v92, 16, v106
	v_add3_u32 v3, v3, v5, s33
	ds_write_b16_d16_hi v77, v3 offset:19040
	v_mul_f32_e32 v3, v6, v92
	v_bfe_u32 v5, v3, 16, 1
	v_pk_mul_f32 v[6:7], v[4:5], v[6:7] op_sel_hi:[0,1]
	v_add3_u32 v3, v3, v5, s33
	v_pk_mul_f32 v[6:7], v[6:7], v[92:93]
	ds_write_b16_d16_hi v77, v3 offset:19312
	v_and_b32_sdwa v3, v7, v188 dst_sel:DWORD dst_unused:UNUSED_PAD src0_sel:WORD_1 src1_sel:DWORD
	v_and_b32_sdwa v5, v6, v188 dst_sel:DWORD dst_unused:UNUSED_PAD src0_sel:WORD_1 src1_sel:DWORD
	v_add3_u32 v3, v7, v3, s33
	v_add3_u32 v5, v6, v5, s33
	v_lshrrev_b32_e32 v3, 16, v3
	v_and_or_b32 v3, v5, s2, v3
	v_add_f32_e32 v5, v11, v45
	v_mul_f32_e32 v5, 0x3fb8aa3b, v5
	v_exp_f32_e32 v5, v5
	ds_read_u16 v6, v77 offset:2176
	ds_read_u16 v10, v77 offset:2448
	ds_read_u16 v91, v77 offset:2720
	ds_read_u16 v92, v77 offset:2992
	ds_read_u16 v93, v77 offset:3264
	ds_read_u16 v94, v77 offset:3536
	ds_read_u16 v95, v77 offset:3808
	ds_read_u16 v96, v77 offset:4080
	s_waitcnt lgkmcnt(7)
; #define LAS __attribute__((address_space(3)))
; __device__ __forceinline__ unsigned f2bf(float f) { unsigned u = __builtin_bit_cast(unsigned, f); return (u + 0x7fffu + ((u >> 16) & 1u)) >> 16; }
; __device__ __forceinline__ void gla_local_unit(LAS unsigned char* lds, GlaPre& R, const bf16_t* proj, const float* alow, const float (&w2)[16], const float bias, ...
;     ...
;     for (int ii = 0; ii < 16; ++ii) { const float bb = pre + bl[ii];
;         LAS bf16_t* qp = (LAS bf16_t*)(QD + (16 * ig + ii) * 272 + 2 * d); LAS bf16_t* kp = (LAS bf16_t*)(KI + (16 * ig + ii) * 272 + 2 * d);
;         const float qf_ = bf2f(*qp), kf_ = bf2f(*kp);
;         const float eb = __expf(bb), einv = __builtin_amdgcn_rcpf(eb);
;         const float qd = qf_ * qscale * eb, ki = kf_ * einv, kend = kf_ * (etot * einv);
;         *qp = (bf16_t)f2bf(qd); *kp = (bf16_t)f2bf(ki);
;         if (ii & 1) ke[ii >> 1] |= f2bf(kend) << 16; else ke[ii >> 1] = f2bf(kend); }
;     *(LAS u32x4*)(KET + d * 144 + 32 * ig) = (u32x4){ke[0], ke[1], ke[2], ke[3]}; *(LAS u32x4*)(KET + d * 144 + 32 * ig + 16) = (u32x4){ke[4], ke[5], ke[6], ke[7]};
;     if (ig == 0) decg[(size_t)u * 128 + d] = etot;
	v_lshlrev_b32_e32 v6, 16, v6
	v_mul_f32_e32 v6, 0x3db504f3, v6
	v_add_f32_e32 v8, v8, v45
	v_rcp_f32_e32 v7, v5
	v_mul_f32_e32 v5, v5, v6
	v_mul_f32_e32 v8, 0x3fb8aa3b, v8
	v_bfe_u32 v6, v5, 16, 1
	v_exp_f32_e32 v8, v8
	v_add3_u32 v5, v5, v6, s33
	ds_write_b16_d16_hi v77, v5 offset:2176
	s_waitcnt lgkmcnt(7)
	v_lshlrev_b32_e32 v5, 16, v10
	v_mul_f32_e32 v5, 0x3db504f3, v5
	v_mul_f32_e32 v5, v8, v5
	v_rcp_f32_e32 v6, v8
	v_bfe_u32 v8, v5, 16, 1
	v_add3_u32 v5, v5, v8, s33
	ds_write_b16_d16_hi v77, v5 offset:2448
	ds_read_u16 v5, v77 offset:19584
	ds_read_u16 v8, v77 offset:19856
	ds_read_u16 v97, v77 offset:20128
	ds_read_u16 v98, v77 offset:20400
	ds_read_u16 v99, v77 offset:20672
	ds_read_u16 v100, v77 offset:20944
	ds_read_u16 v101, v77 offset:21216
	ds_read_u16 v102, v77 offset:21488
	s_waitcnt lgkmcnt(7)
	v_lshlrev_b32_e32 v11, 16, v5
	v_mul_f32_e32 v5, v7, v11
	s_waitcnt lgkmcnt(6)
	v_lshlrev_b32_e32 v10, 16, v8
	v_bfe_u32 v8, v5, 16, 1
	v_add3_u32 v5, v5, v8, s33
	ds_write_b16_d16_hi v77, v5 offset:19584
	v_mul_f32_e32 v5, v6, v10
	v_bfe_u32 v8, v5, 16, 1
	v_add3_u32 v5, v5, v8, s33
	v_pk_mul_f32 v[6:7], v[4:5], v[6:7] op_sel_hi:[0,1]
	v_pk_mul_f32 v[6:7], v[6:7], v[10:11]
	ds_write_b16_d16_hi v77, v5 offset:19856
	v_and_b32_sdwa v5, v7, v188 dst_sel:DWORD dst_unused:UNUSED_PAD src0_sel:WORD_1 src1_sel:DWORD
	v_add3_u32 v5, v7, v5, s33
	v_add_f32_e32 v7, v9, v45
	v_mul_f32_e32 v7, 0x3fb8aa3b, v7
	v_and_b32_sdwa v8, v6, v188 dst_sel:DWORD dst_unused:UNUSED_PAD src0_sel:WORD_1 src1_sel:DWORD
	v_exp_f32_e32 v7, v7
	v_add3_u32 v6, v6, v8, s33
	v_lshrrev_b32_e32 v5, 16, v5
	v_and_or_b32 v6, v6, s2, v5
	v_lshlrev_b32_e32 v5, 16, v91
	v_mul_f32_e32 v5, 0x3db504f3, v5
	v_add_f32_e32 v8, v12, v45
	v_mul_f32_e32 v5, v7, v5
	v_mul_f32_e32 v8, 0x3fb8aa3b, v8
	v_rcp_f32_e32 v9, v7
	v_bfe_u32 v7, v5, 16, 1
	v_exp_f32_e32 v10, v8
	v_add3_u32 v5, v5, v7, s33
	ds_write_b16_d16_hi v77, v5 offset:2720
	v_lshlrev_b32_e32 v5, 16, v92
	v_mul_f32_e32 v5, 0x3db504f3, v5
	v_mul_f32_e32 v5, v10, v5
	v_bfe_u32 v7, v5, 16, 1
	v_rcp_f32_e32 v8, v10
	v_add3_u32 v5, v5, v7, s33
	s_waitcnt lgkmcnt(8)
	v_lshlrev_b32_e32 v11, 16, v97
	ds_write_b16_d16_hi v77, v5 offset:2992
	v_mul_f32_e32 v5, v9, v11
	v_bfe_u32 v7, v5, 16, 1
	s_waitcnt lgkmcnt(8)
	v_lshlrev_b32_e32 v10, 16, v98
	v_add3_u32 v5, v5, v7, s33
	ds_write_b16_d16_hi v77, v5 offset:20128
	v_mul_f32_e32 v5, v8, v10
	v_bfe_u32 v7, v5, 16, 1
	v_add3_u32 v5, v5, v7, s33
	v_pk_mul_f32 v[8:9], v[4:5], v[8:9] op_sel_hi:[0,1]
	v_pk_mul_f32 v[8:9], v[8:9], v[10:11]
	ds_write_b16_d16_hi v77, v5 offset:20400
	v_and_b32_sdwa v7, v8, v188 dst_sel:DWORD dst_unused:UNUSED_PAD src0_sel:WORD_1 src1_sel:DWORD
	v_add3_u32 v7, v8, v7, s33
	v_add_f32_e32 v8, v45, v13
	v_and_b32_sdwa v5, v9, v188 dst_sel:DWORD dst_unused:UNUSED_PAD src0_sel:WORD_1 src1_sel:DWORD
	v_mul_f32_e32 v8, 0x3fb8aa3b, v8
	v_add3_u32 v5, v9, v5, s33
	v_exp_f32_e32 v8, v8
	v_lshrrev_b32_e32 v5, 16, v5
	v_and_or_b32 v7, v7, s2, v5
	v_lshlrev_b32_e32 v5, 16, v93
	v_mul_f32_e32 v5, 0x3db504f3, v5
	v_add_f32_e32 v10, v45, v14
	v_mul_f32_e32 v5, v8, v5
	v_mul_f32_e32 v10, 0x3fb8aa3b, v10
	v_rcp_f32_e32 v9, v8
	v_bfe_u32 v8, v5, 16, 1
	v_exp_f32_e32 v10, v10
	v_add3_u32 v5, v5, v8, s33
	ds_write_b16_d16_hi v77, v5 offset:3264
	v_lshlrev_b32_e32 v5, 16, v94
	v_mul_f32_e32 v5, 0x3db504f3, v5
	v_mul_f32_e32 v5, v10, v5
	v_rcp_f32_e32 v8, v10
	v_bfe_u32 v10, v5, 16, 1
	v_add3_u32 v5, v5, v10, s33
	s_waitcnt lgkmcnt(10)
	v_lshlrev_b32_e32 v11, 16, v99
	ds_write_b16_d16_hi v77, v5 offset:3536
	v_mul_f32_e32 v5, v9, v11
	v_bfe_u32 v12, v5, 16, 1
	s_waitcnt lgkmcnt(10)
	v_lshlrev_b32_e32 v10, 16, v100
	v_add3_u32 v5, v5, v12, s33
	ds_write_b16_d16_hi v77, v5 offset:20672
	v_mul_f32_e32 v5, v8, v10
	v_bfe_u32 v12, v5, 16, 1
	v_add3_u32 v5, v5, v12, s33
	v_pk_mul_f32 v[8:9], v[4:5], v[8:9] op_sel_hi:[0,1]
	v_pk_mul_f32 v[8:9], v[8:9], v[10:11]
	ds_write_b16_d16_hi v77, v5 offset:20944
	v_and_b32_sdwa v5, v9, v188 dst_sel:DWORD dst_unused:UNUSED_PAD src0_sel:WORD_1 src1_sel:DWORD
	v_add3_u32 v5, v9, v5, s33
	v_add_f32_e32 v9, v45, v15
	v_mul_f32_e32 v9, 0x3fb8aa3b, v9
	v_and_b32_sdwa v10, v8, v188 dst_sel:DWORD dst_unused:UNUSED_PAD src0_sel:WORD_1 src1_sel:DWORD
	v_exp_f32_e32 v9, v9
	v_add3_u32 v8, v8, v10, s33
	v_lshrrev_b32_e32 v5, 16, v5
	v_and_or_b32 v8, v8, s2, v5
	v_lshlrev_b32_e32 v5, 16, v95
	v_mul_f32_e32 v5, 0x3db504f3, v5
	v_add_f32_e32 v10, v45, v44
	v_mul_f32_e32 v5, v9, v5
	v_mul_f32_e32 v10, 0x3fb8aa3b, v10
	v_rcp_f32_e32 v11, v9
	v_bfe_u32 v9, v5, 16, 1
	v_exp_f32_e32 v12, v10
	v_add3_u32 v5, v5, v9, s33
	ds_write_b16_d16_hi v77, v5 offset:3808
	v_lshlrev_b32_e32 v5, 16, v96
	v_mul_f32_e32 v5, 0x3db504f3, v5
	v_mul_f32_e32 v5, v12, v5
	v_bfe_u32 v9, v5, 16, 1
	v_rcp_f32_e32 v10, v12
	v_add3_u32 v5, v5, v9, s33
	s_waitcnt lgkmcnt(12)
	v_lshlrev_b32_e32 v13, 16, v101
	ds_write_b16_d16_hi v77, v5 offset:4080
	v_mul_f32_e32 v5, v11, v13
	v_bfe_u32 v9, v5, 16, 1
	s_waitcnt lgkmcnt(12)
	v_lshlrev_b32_e32 v12, 16, v102
	v_add3_u32 v5, v5, v9, s33
	ds_write_b16_d16_hi v77, v5 offset:21216
	v_mul_f32_e32 v5, v10, v12
	v_bfe_u32 v9, v5, 16, 1
	v_add3_u32 v5, v5, v9, s33
	v_pk_mul_f32 v[10:11], v[4:5], v[10:11] op_sel_hi:[0,1]
	v_pk_mul_f32 v[10:11], v[10:11], v[12:13]
	ds_write_b16_d16_hi v77, v5 offset:21488
	v_and_b32_sdwa v5, v11, v188 dst_sel:DWORD dst_unused:UNUSED_PAD src0_sel:WORD_1 src1_sel:DWORD
	v_and_b32_sdwa v9, v10, v188 dst_sel:DWORD dst_unused:UNUSED_PAD src0_sel:WORD_1 src1_sel:DWORD
	v_add3_u32 v5, v11, v5, s33
	v_add3_u32 v9, v10, v9, s33
	v_lshrrev_b32_e32 v5, 16, v5
	v_and_or_b32 v9, v9, s2, v5
	ds_write_b128 v78, v[0:3] offset:34816
	ds_write_b128 v78, v[6:9] offset:34832
	s_and_saveexec_b64 s[2:3], s[12:13]
	s_cbranch_execz .LBB0_352
	global_store_dword v[42:43], v4, off

; #define LAS __attribute__((address_space(3)))
; #define FRESH_TID() do { ap = fresh_args(); ws = ap->ws; unsigned m1_ = ~0u; asm volatile("" : "+s"(m1_)); lane = (int)__builtin_amdgcn_mbcnt_hi(m1_, __builtin_amdgcn_mbcnt_lo(m1_, 0u)); asm volatile("" : "+v"(lane)); wave = wave0; tid = wave0 * 64 + lane; } while (0)
; __device__ __forceinline__ void moe_table_build(LAS unsigned char* lds, const unsigned* cnt, int tid) {
;     if (tid < NE) { const int n = (int)__hip_atomic_load(cnt + 64 * tid, RLX_AGENT); ((LAS int*)(lds + MOE_TAB_OFF))[16 + tid] = n; }
; template <unsigned MASK, bool ONE>
; __global__ void __launch_bounds__(NTHREADS, 2) fwd_kernel(Args a_unused) {
;     ...
;         if (IN(P + 8, 9)) { FRESH_TID();
;             pg8::moe_table_build(lds, cntl, tid);
;             pg8::MoeOrder S; S.init(lds, 8, G, bx); pg8::RowsGather AM{rlist, lds}; pg8::EpiSwiGLU8 E{(unsigned char*)act};
.LBB0_925:
	s_or_b64 exec, exec, s[0:1]
	v_readlane_b32 s101, v255, 17
	s_movk_i32 s100, 0x100
	s_cmp_eq_u32 s101, 0
	s_cselect_b32 s100, 0xe0, s100
	s_cselect_b32 s101, 32, 0
	v_readlane_b32 s0, v253, 0
	v_readlane_b32 s1, v253, 1
	s_waitcnt lgkmcnt(0)
	s_barrier
	s_load_dwordx2 s[6:7], s[0:1], 0xa0
	s_mov_b32 s0, s38
	s_nop 0
	v_mbcnt_lo_u32_b32 v0, s0, 0
	v_mbcnt_hi_u32_b32 v0, s0, v0
	s_nop 0
	v_add_u32_e32 v1, s78, v0
	v_cmp_gt_i32_e32 vcc, 16, v1
	s_and_saveexec_b64 s[0:1], vcc
	s_cbranch_execz .LBB0_927
	s_lshl_b64 s[2:3], s[96:97], 2
	s_waitcnt lgkmcnt(0)
	s_add_u32 s2, s6, s2
	v_lshlrev_b32_e32 v2, 6, v1
	s_addc_u32 s3, s7, s3
	v_ashrrev_i32_e32 v3, 31, v2
	v_lshl_add_u64 v[2:3], v[2:3], 2, s[2:3]
	v_add_co_u32_e32 v2, vcc, 0x10000, v2
	v_readlane_b32 s2, v255, 23
	s_nop 0
	v_addc_co_u32_e32 v3, vcc, 0, v3, vcc
	global_load_dword v2, v[2:3], off sc1
	v_lshl_add_u32 v3, v1, 2, s2
	s_waitcnt vmcnt(0)
	ds_write_b32 v3, v2 offset:64

; #define LAS __attribute__((address_space(3)))
;     __device__ __forceinline__ bool next(int i, Unit& u) const { u.e = 0; u.ti = 0; return grid_order<WGM, ROT>(nM, nN, G, c, i, u.pm, u.pn); }
;     __device__ __forceinline__ bool next(int i, Unit& u) const { u.e = i & 1; u.ti = 0; return grid_order<WGM_MIX, ROT_MIX>(nM, nN, G, c, i >> 1, u.pm, u.pn); }
; #define PG8_OFFS(dst, u) do { _Pragma("unroll") for (int _h = 0; _h < 2; ++_h) _Pragma("unroll") for (int _i = 0; _i < 2; ++_i) { int _R, _C; stage_rc(tid * 16 + _i * 8192, _R, _C); \
;         dst[_h][_i] = (AM.row(u, _h * HALF + _R) * (unsigned)K + (unsigned)_C) * 2u; } } while (0)
; #define PG8_RAW(dst, u) do { _Pragma("unroll") for (int _h = 0; _h < 2; ++_h) _Pragma("unroll") for (int _i = 0; _i < 2; ++_i) { int _R, _C; stage_rc(tid * 16 + _i * 8192, _R, _C); dst[_h][_i] = AM.row(u, _h * HALF + _R); } } while (0)
;     __device__ __forceinline__ void init(LAS unsigned char* lds_, int nN_, int G_, int c_) {
;         lds = lds_; NT = __builtin_amdgcn_readfirstlane(((LAS int*)(lds + MOE_TAB_OFF))[15]); nN = nN_; G = G_; c = c_; }
;     __device__ __forceinline__ bool next(int i, Unit& u) const {
;         if (!grid_order<WGM_MOE>(NT, nN, G, c, i, u.pm, u.pn)) return false;
;         int e = 0, ts = 0;
; #pragma unroll
;         for (int q = 0; q < 4; ++q) { const i32x4 t = ((const LAS i32x4*)(lds + MOE_TAB_OFF))[q];
; #pragma unroll
;             for (int j = 0; j < 4; ++j) { const bool ge = u.pm >= t[j]; e += ge ? 1 : 0; ts = ge ? t[j] : ts; } }
;         u.e = __builtin_amdgcn_readfirstlane(e); u.ti = u.pm - __builtin_amdgcn_readfirstlane(ts); return true;
; template <class Epi, class Sched, class AMap, bool ALIGN_EPI, bool F8 = false, bool SEG2 = false>
; __device__ __forceinline__ void gemm_phase(LAS unsigned char* lds, const int tid, const bf16_t* A, const bf16_t* Bt, size_t bstride, int K, const Sched& S, const AMap& AM, const Epi& E) {
;     ...
;     if constexpr (AMap::GATHER) { PG8_OFFS(offC, cur); has_next = S.next(1, nxt);
;         if (has_next) { PG8_RAW(rawN, nxt); } else {
.LBB0_929:
	s_or_b64 exec, exec, s[0:1]
	v_readlane_b32 s0, v254, 58
	s_waitcnt lgkmcnt(0)
	s_barrier
	v_mov_b32_e32 v2, s0
	ds_read_b32 v2, v2
	v_readlane_b32 s1, v253, 4
	v_readfirstlane_b32 s14, v1
	s_waitcnt lgkmcnt(0)
	v_readfirstlane_b32 s22, v2
	s_lshl_b32 s0, s22, 3
	s_cmp_eq_u32 s101, 0
	s_cbranch_scc1 .Lno_help9
	s_cmpk_lt_i32 s1, 0xe0
	s_cbranch_scc1 .Lno_help9
	s_movk_i32 s100, 0x800
	s_movk_i32 s101, 0x1d00
	s_mov_b32 s0, 0
	v_writelane_b32 v251, s0, 30
	s_branch .Lhp_entry
.Lno_help9:
	s_cmp_ge_i32 s1, s0
	s_cbranch_scc1 .LBB0_954
	v_ashrrev_i32_e32 v3, 31, v1
	v_lshrrev_b32_e32 v3, 26, v3
	v_lshlrev_b32_e32 v2, 4, v1
	v_add_u32_e32 v3, v1, v3
	v_bfe_i32 v1, v1, 27, 1
	v_lshrrev_b32_e32 v1, 22, v1
	v_add_u32_e32 v1, v2, v1
	v_and_b32_e32 v1, 0xfffffc00, v1
	v_sub_u32_e32 v1, v2, v1
	v_ashrrev_i32_e32 v3, 6, v3
	v_lshrrev_b32_e32 v4, 4, v1
	v_bitop3_b32 v4, v4, v1, 32 bitop3:0x6c
	v_lshlrev_b32_e32 v1, 3, v3
	v_and_b32_e32 v5, -16, v1
	v_ashrrev_i32_e32 v1, 31, v4
	v_lshrrev_b32_e32 v1, 26, v1
	v_add_u32_e32 v1, v4, v1
	v_ashrrev_i32_e32 v1, 6, v1
	v_add_u32_e32 v2, 0x2000, v2
	s_add_u32 s23, s6, 0x900000
	v_add_u32_e32 v32, v1, v5
	v_ashrrev_i32_e32 v5, 31, v2
	v_readlane_b32 s1, v254, 4
	s_addc_u32 s24, s7, 0
	v_lshrrev_b32_e32 v5, 22, v5
	s_add_i32 s1, s22, s1
	v_readlane_b32 s2, v254, 3
	v_add_u32_e32 v5, v2, v5
	s_mul_i32 s1, s1, s2
	v_readlane_b32 s2, v253, 48
	v_ashrrev_i32_e32 v5, 10, v5
	s_add_i32 s1, s1, s2
	v_mul_i32_i24_e32 v6, 0x400, v5
	s_ashr_i32 s2, s1, 31
	v_sub_u32_e32 v2, v2, v6
	s_lshr_b32 s2, s2, 27
	v_lshrrev_b32_e32 v6, 4, v2
	s_add_i32 s2, s1, s2
	v_bitop3_b32 v6, v6, v2, 32 bitop3:0x6c
	v_lshlrev_b32_e32 v2, 3, v5
	s_ashr_i32 s3, s2, 5
	v_and_b32_e32 v7, -16, v2
	v_ashrrev_i32_e32 v2, 31, v6
	s_lshl_b32 s3, s3, 2
	v_lshrrev_b32_e32 v2, 26, v2
	s_sub_i32 s4, s22, s3
	v_add_u32_e32 v2, v6, v2
	s_min_i32 s4, s4, 4
	v_ashrrev_i32_e32 v2, 6, v2
	s_abs_i32 s9, s4
	v_add_u32_e32 v162, v2, v7
	v_cvt_f32_u32_e32 v7, s9
	s_sub_i32 s10, 0, s9
	s_andn2_b32 s2, s2, 31
	s_sub_i32 s1, s1, s2
	v_rcp_iflag_f32_e32 v7, v7
	s_abs_i32 s5, s1
	s_xor_b32 s2, s1, s4
	s_ashr_i32 s2, s2, 31
	v_mul_f32_e32 v7, 0x4f7ffffe, v7
	v_cvt_u32_f32_e32 v7, v7
	s_mov_b32 s8, 0
	v_readfirstlane_b32 s11, v7
	s_mul_i32 s10, s10, s11
	s_mul_hi_u32 s10, s11, s10
	s_add_i32 s11, s11, s10
	s_mul_hi_u32 s10, s5, s11
	s_mul_i32 s11, s10, s9
	s_sub_i32 s5, s5, s11
	s_add_i32 s11, s10, 1
	s_sub_i32 s12, s5, s9
	s_cmp_ge_u32 s5, s9
	s_cselect_b32 s10, s11, s10
	s_cselect_b32 s5, s12, s5
	s_add_i32 s11, s10, 1
	s_cmp_ge_u32 s5, s9
	s_cselect_b32 s5, s11, s10
	s_xor_b32 s5, s5, s2
	s_sub_i32 s27, s5, s2
	s_mul_i32 s2, s27, s4
	s_sub_i32 s1, s1, s2
	s_add_i32 s28, s3, s1
	v_readlane_b32 s1, v255, 23
	s_nop 1
	v_mov_b32_e32 v7, s1
	ds_read_b128 v[8:11], v7
	v_readlane_b32 s1, v255, 24
	s_waitcnt lgkmcnt(0)
	v_cmp_ge_i32_e32 vcc, s28, v8
	v_cmp_ge_i32_e64 s[4:5], s28, v9
	s_nop 0
	v_cndmask_b32_e32 v7, 0, v8, vcc
	v_cndmask_b32_e64 v8, 0, 1, s[4:5]
	v_addc_co_u32_e32 v8, vcc, 0, v8, vcc
	v_cndmask_b32_e64 v7, v7, v9, s[4:5]
	v_cmp_ge_i32_e32 vcc, s28, v10
	s_nop 1
	v_cndmask_b32_e64 v9, 0, 1, vcc
	v_cndmask_b32_e32 v7, v7, v10, vcc
	v_cmp_ge_i32_e32 vcc, s28, v11
	s_nop 1
	v_cndmask_b32_e32 v7, v7, v11, vcc
	v_addc_co_u32_e32 v12, vcc, v8, v9, vcc
	v_mov_b32_e32 v8, s1
	ds_read_b128 v[8:11], v8
	v_readlane_b32 s1, v255, 25
	s_waitcnt lgkmcnt(0)
	v_cmp_ge_i32_e32 vcc, s28, v8
	s_nop 1
	v_cndmask_b32_e64 v13, 0, 1, vcc
	v_cndmask_b32_e32 v7, v7, v8, vcc
	v_cmp_ge_i32_e32 vcc, s28, v9
	s_nop 1
	v_cndmask_b32_e32 v7, v7, v9, vcc
	v_addc_co_u32_e32 v8, vcc, v12, v13, vcc
	v_cmp_ge_i32_e32 vcc, s28, v10
	s_nop 1
	v_cndmask_b32_e64 v9, 0, 1, vcc
	v_cndmask_b32_e32 v7, v7, v10, vcc
	v_cmp_ge_i32_e32 vcc, s28, v11
	s_nop 1
	v_cndmask_b32_e32 v7, v7, v11, vcc
	v_addc_co_u32_e32 v12, vcc, v8, v9, vcc
	v_mov_b32_e32 v8, s1
	ds_read_b128 v[8:11], v8
	v_readlane_b32 s1, v255, 26
	s_waitcnt lgkmcnt(0)
	v_cmp_ge_i32_e32 vcc, s28, v8
	s_nop 1
	v_cndmask_b32_e64 v13, 0, 1, vcc
	v_cndmask_b32_e32 v7, v7, v8, vcc
	v_cmp_ge_i32_e32 vcc, s28, v9
	s_nop 1
	v_cndmask_b32_e32 v7, v7, v9, vcc
	v_addc_co_u32_e32 v8, vcc, v12, v13, vcc
	v_cmp_ge_i32_e32 vcc, s28, v10
	s_nop 1
	v_cndmask_b32_e64 v9, 0, 1, vcc
	v_cndmask_b32_e32 v7, v7, v10, vcc
	v_cmp_ge_i32_e32 vcc, s28, v11
	s_nop 1
	v_cndmask_b32_e32 v7, v7, v11, vcc
	v_addc_co_u32_e32 v12, vcc, v8, v9, vcc
	v_mov_b32_e32 v8, s1
	ds_read_b128 v[8:11], v8
	s_waitcnt lgkmcnt(0)
	v_cmp_ge_i32_e32 vcc, s28, v8
	s_nop 1
	v_cndmask_b32_e64 v13, 0, 1, vcc
	v_cndmask_b32_e32 v7, v7, v8, vcc
	v_cmp_ge_i32_e32 vcc, s28, v9
	s_nop 1
	v_cndmask_b32_e32 v7, v7, v9, vcc
	v_addc_co_u32_e32 v8, vcc, v12, v13, vcc
	v_cmp_ge_i32_e32 vcc, s28, v10
	s_nop 1
	v_cndmask_b32_e64 v9, 0, 1, vcc
	v_cndmask_b32_e32 v7, v7, v10, vcc
	v_cmp_ge_i32_e32 vcc, s28, v11
	s_nop 1
	v_cndmask_b32_e32 v7, v7, v11, vcc
	v_addc_co_u32_e32 v8, vcc, v8, v9, vcc
	s_nop 0
	v_readfirstlane_b32 s2, v8
	s_lshl_b32 s3, s2, 2
	v_readfirstlane_b32 s1, v7
	v_mov_b32_e32 v7, 0x7f7f7f7f
	s_add_i32 s3, s3, 0
	s_add_i32 s3, s3, 0x22040
	v_mov_b32_e32 v7, s3
	ds_read_b32 v12, v7
	s_sub_i32 s1, s28, s1
	s_lshl_b32 s1, s1, 8
	s_ashr_i32 s3, s2, 31
	v_add_u32_e32 v7, s1, v32
	s_lshl_b64 s[4:5], s[2:3], 16
	s_waitcnt lgkmcnt(0)
	v_cmp_lt_i32_e32 vcc, v7, v12
	s_add_u32 s4, s23, s4
	s_addc_u32 s5, s24, s5
	v_cndmask_b32_e32 v8, 0, v7, vcc
	v_ashrrev_i32_e32 v9, 31, v8
	v_lshl_add_u64 v[8:9], v[8:9], 2, s[4:5]
	global_load_dword v7, v[8:9], off
	v_add_u32_e32 v8, s1, v162
	v_cmp_lt_i32_e32 vcc, v8, v12
	s_bitset1_b32 s1, 7
	s_nop 0
	v_cndmask_b32_e32 v8, 0, v8, vcc
	v_ashrrev_i32_e32 v9, 31, v8
	v_lshl_add_u64 v[8:9], v[8:9], 2, s[4:5]
	global_load_dword v8, v[8:9], off
	v_add_u32_e32 v9, s1, v32
	v_cmp_lt_i32_e32 vcc, v9, v12
	s_nop 1
	v_cndmask_b32_e32 v10, 0, v9, vcc
	v_ashrrev_i32_e32 v11, 31, v10
	v_lshl_add_u64 v[10:11], v[10:11], 2, s[4:5]
	global_load_dword v9, v[10:11], off
	v_add_u32_e32 v10, s1, v162
	v_cmp_lt_i32_e32 vcc, v10, v12
	s_ashr_i32 s1, s0, 31
	v_mov_b64_e32 v[12:13], s[0:1]
	v_cndmask_b32_e32 v10, 0, v10, vcc
	v_ashrrev_i32_e32 v11, 31, v10
	v_lshl_add_u64 v[10:11], v[10:11], 2, s[4:5]
	global_load_dword v10, v[10:11], off
	v_readlane_b32 s4, v253, 35
	v_readlane_b32 s5, v253, 36
	s_sub_u32 s4, s4, s101
	s_subb_u32 s5, s5, 0
	s_nop 1
	v_cmp_ge_i64_e32 vcc, s[4:5], v[12:13]
	v_cmp_lt_i64_e64 s[18:19], s[4:5], v[12:13]
	s_cbranch_vccnz .LBB0_932
; #define LAS __attribute__((address_space(3)))
;     __device__ __forceinline__ bool next(int i, Unit& u) const { u.e = 0; u.ti = 0; return grid_order<WGM, ROT>(nM, nN, G, c, i, u.pm, u.pn); }
;     __device__ __forceinline__ bool next(int i, Unit& u) const { u.e = i & 1; u.ti = 0; return grid_order<WGM_MIX, ROT_MIX>(nM, nN, G, c, i >> 1, u.pm, u.pn); }
;     const int nwg = nM * nN; const long L = (long)i * G + c; if (L >= nwg) return false;
;     int wgid = (int)L; const int xcd = wgid % NXCD; { const int q = nwg / NXCD, r = nwg % NXCD, off = wgid / NXCD; wgid = (xcd < r ? xcd * (q + 1) : r * (q + 1) + (xcd - r) * q) + off; }
;     const int nig = WGM * nN, gid = wgid / nig, fm = gid * WGM, gsz = (nM - fm) < WGM ? (nM - fm) : WGM;
;     pm = fm + ((wgid % nig) % gsz); pn = (wgid % nig) / gsz;
;     __device__ __forceinline__ bool next(int i, Unit& u) const {
;         if (!grid_order<WGM_MOE>(NT, nN, G, c, i, u.pm, u.pn)) return false;
;         int e = 0, ts = 0;
; #pragma unroll
;         for (int q = 0; q < 4; ++q) { const i32x4 t = ((const LAS i32x4*)(lds + MOE_TAB_OFF))[q];
; #pragma unroll
;             for (int j = 0; j < 4; ++j) { const bool ge = u.pm >= t[j]; e += ge ? 1 : 0; ts = ge ? t[j] : ts; } }
;         u.e = __builtin_amdgcn_readfirstlane(e); u.ti = u.pm - __builtin_amdgcn_readfirstlane(ts); return true;
	v_readlane_b32 s3, v254, 2
	s_add_i32 s3, s22, s3
	v_readlane_b32 s4, v254, 1
	s_mul_i32 s3, s3, s4
	v_readlane_b32 s4, v253, 34
	s_lshr_b32 s5, s101, 3
	s_sub_i32 s4, s4, s5
	s_add_i32 s3, s3, s4
	s_ashr_i32 s4, s3, 31
	s_lshr_b32 s4, s4, 27
	s_add_i32 s4, s3, s4
	s_ashr_i32 s5, s4, 5
	s_lshl_b32 s5, s5, 2
	s_sub_i32 s8, s22, s5
	s_min_i32 s8, s8, 4
	s_abs_i32 s10, s8
	v_cvt_f32_u32_e32 v11, s10
	s_sub_i32 s11, 0, s10
	s_andn2_b32 s4, s4, 31
	s_sub_i32 s3, s3, s4
	v_rcp_iflag_f32_e32 v11, v11
	s_abs_i32 s9, s3
	s_xor_b32 s4, s3, s8
	s_ashr_i32 s4, s4, 31
	v_mul_f32_e32 v11, 0x4f7ffffe, v11
	v_cvt_u32_f32_e32 v11, v11
	s_nop 0
	v_readfirstlane_b32 s12, v11
	s_mul_i32 s11, s11, s12
	s_mul_hi_u32 s11, s12, s11
	s_add_i32 s12, s12, s11
	s_mul_hi_u32 s11, s9, s12
	s_mul_i32 s12, s11, s10
	s_sub_i32 s9, s9, s12
	s_add_i32 s12, s11, 1
	s_sub_i32 s13, s9, s10
	s_cmp_ge_u32 s9, s10
	s_cselect_b32 s11, s12, s11
	s_cselect_b32 s9, s13, s9
	s_add_i32 s12, s11, 1
	s_cmp_ge_u32 s9, s10
	s_cselect_b32 s9, s12, s11
	s_xor_b32 s9, s9, s4
	s_sub_i32 s25, s9, s4
	s_mul_i32 s4, s25, s8
	s_sub_i32 s3, s3, s4
	s_add_i32 s26, s3, s5
	v_readlane_b32 s3, v255, 23
	s_nop 1
	v_mov_b32_e32 v11, s3
	ds_read_b128 v[12:15], v11
	v_readlane_b32 s3, v255, 24
	s_waitcnt lgkmcnt(0)
	v_cmp_ge_i32_e32 vcc, s26, v12
	v_cmp_ge_i32_e64 s[4:5], s26, v13
	s_nop 0
	v_cndmask_b32_e32 v11, 0, v12, vcc
	v_cndmask_b32_e64 v12, 0, 1, s[4:5]
	v_addc_co_u32_e32 v12, vcc, 0, v12, vcc
	v_cndmask_b32_e64 v11, v11, v13, s[4:5]
	v_cmp_ge_i32_e32 vcc, s26, v14
	s_nop 1
	v_cndmask_b32_e64 v13, 0, 1, vcc
	v_cndmask_b32_e32 v11, v11, v14, vcc
	v_cmp_ge_i32_e32 vcc, s26, v15
	s_nop 1
	v_cndmask_b32_e32 v11, v11, v15, vcc
	v_addc_co_u32_e32 v16, vcc, v12, v13, vcc
	v_mov_b32_e32 v12, s3
	ds_read_b128 v[12:15], v12
	v_readlane_b32 s3, v255, 25
	s_waitcnt lgkmcnt(0)
	v_cmp_ge_i32_e32 vcc, s26, v12
	s_nop 1
	v_cndmask_b32_e64 v17, 0, 1, vcc
	v_cndmask_b32_e32 v11, v11, v12, vcc
	v_cmp_ge_i32_e32 vcc, s26, v13
	s_nop 1
	v_cndmask_b32_e32 v11, v11, v13, vcc
	v_addc_co_u32_e32 v12, vcc, v16, v17, vcc
	v_cmp_ge_i32_e32 vcc, s26, v14
	s_nop 1
	v_cndmask_b32_e64 v13, 0, 1, vcc
	v_cndmask_b32_e32 v11, v11, v14, vcc
	v_cmp_ge_i32_e32 vcc, s26, v15
	s_nop 1
	v_cndmask_b32_e32 v11, v11, v15, vcc
	v_addc_co_u32_e32 v16, vcc, v12, v13, vcc
	v_mov_b32_e32 v12, s3
	ds_read_b128 v[12:15], v12
	v_readlane_b32 s3, v255, 26
	s_waitcnt lgkmcnt(0)
	v_cmp_ge_i32_e32 vcc, s26, v12
	s_nop 1
	v_cndmask_b32_e64 v17, 0, 1, vcc
	v_cndmask_b32_e32 v11, v11, v12, vcc
	v_cmp_ge_i32_e32 vcc, s26, v13
	s_nop 1
	v_cndmask_b32_e32 v11, v11, v13, vcc
	v_addc_co_u32_e32 v12, vcc, v16, v17, vcc
	v_cmp_ge_i32_e32 vcc, s26, v14
	s_nop 1
	v_cndmask_b32_e64 v13, 0, 1, vcc
	v_cndmask_b32_e32 v11, v11, v14, vcc
	v_cmp_ge_i32_e32 vcc, s26, v15
	s_nop 1
	v_cndmask_b32_e32 v11, v11, v15, vcc
	v_addc_co_u32_e32 v16, vcc, v12, v13, vcc
	v_mov_b32_e32 v12, s3
	ds_read_b128 v[12:15], v12
	s_waitcnt lgkmcnt(0)
	v_cmp_ge_i32_e32 vcc, s26, v12
	s_nop 1
	v_cndmask_b32_e64 v17, 0, 1, vcc
	v_cndmask_b32_e32 v11, v11, v12, vcc
	v_cmp_ge_i32_e32 vcc, s26, v13
	s_nop 1
	v_cndmask_b32_e32 v11, v11, v13, vcc
	v_addc_co_u32_e32 v12, vcc, v16, v17, vcc
	v_cmp_ge_i32_e32 vcc, s26, v14
	s_nop 1
	v_cndmask_b32_e64 v13, 0, 1, vcc
	v_cndmask_b32_e32 v11, v11, v14, vcc
	v_cmp_ge_i32_e32 vcc, s26, v15
	s_nop 1
	v_cndmask_b32_e32 v11, v11, v15, vcc
	v_addc_co_u32_e32 v12, vcc, v12, v13, vcc
	v_readfirstlane_b32 s3, v11
	s_sub_i32 s3, s26, s3
	v_readfirstlane_b32 s20, v12
	s_lshl_b32 s8, s3, 8

; #define LAS __attribute__((address_space(3)))
;     __device__ __forceinline__ bool next(int i, Unit& u) const { u.e = 0; u.ti = 0; return grid_order<WGM, ROT>(nM, nN, G, c, i, u.pm, u.pn); }
;     __device__ __forceinline__ bool next(int i, Unit& u) const { u.e = i & 1; u.ti = 0; return grid_order<WGM_MIX, ROT_MIX>(nM, nN, G, c, i >> 1, u.pm, u.pn); }
;     const int nwg = nM * nN; const long L = (long)i * G + c; if (L >= nwg) return false;
;     int wgid = (int)L; const int xcd = wgid % NXCD; { const int q = nwg / NXCD, r = nwg % NXCD, off = wgid / NXCD; wgid = (xcd < r ? xcd * (q + 1) : r * (q + 1) + (xcd - r) * q) + off; }
;     const int nig = WGM * nN, gid = wgid / nig, fm = gid * WGM, gsz = (nM - fm) < WGM ? (nM - fm) : WGM;
;     pm = fm + ((wgid % nig) % gsz); pn = (wgid % nig) / gsz;
;     __device__ __forceinline__ bool next(int i, Unit& u) const {
;         if (!grid_order<WGM_MOE>(NT, nN, G, c, i, u.pm, u.pn)) return false;
;         int e = 0, ts = 0;
; #pragma unroll
;         for (int q = 0; q < 4; ++q) { const i32x4 t = ((const LAS i32x4*)(lds + MOE_TAB_OFF))[q];
; #pragma unroll
;             for (int j = 0; j < 4; ++j) { const bool ge = u.pm >= t[j]; e += ge ? 1 : 0; ts = ge ? t[j] : ts; } }
;         u.e = __builtin_amdgcn_readfirstlane(e); u.ti = u.pm - __builtin_amdgcn_readfirstlane(ts); return true;
.LBB0_941:
	s_and_b64 vcc, exec, s[4:5]
	s_mov_b64 s[16:17], 0
	s_cbranch_vccnz .LBB0_944
	s_add_i32 s7, s52, 2
	s_mul_i32 s10, s7, s75
	s_mul_hi_u32 s11, s7, s100
	s_add_i32 s11, s11, s10
	s_mul_i32 s7, s7, s100
	v_readlane_b32 s10, v253, 4
	s_add_u32 s10, s7, s10
	v_readlane_b32 s7, v253, 33
	s_addc_u32 s11, s11, s7
	v_mov_b64_e32 v[0:1], s[0:1]
	v_cmp_ge_i64_e32 vcc, s[10:11], v[0:1]
	s_cbranch_vccnz .LBB0_944
	s_ashr_i32 s6, s10, 31
	s_lshr_b32 s6, s6, 29
	s_add_i32 s6, s10, s6
	s_ashr_i32 s7, s6, 3
	s_and_b32 s6, s6, -8
	s_sub_i32 s6, s10, s6
	s_lshr_b32 s10, s6, 31
	s_add_i32 s10, s22, s10
	s_mul_i32 s6, s10, s6
	s_add_i32 s6, s6, s7
	s_ashr_i32 s7, s6, 31
	s_lshr_b32 s7, s7, 27
	s_add_i32 s7, s6, s7
	s_ashr_i32 s10, s7, 5
	s_lshl_b32 s10, s10, 2
	s_sub_i32 s11, s22, s10
	s_min_i32 s11, s11, 4
	s_abs_i32 s17, s11
	v_cvt_f32_u32_e32 v0, s17
	s_sub_i32 s25, 0, s17
	s_andn2_b32 s7, s7, 31
	s_sub_i32 s6, s6, s7
	v_rcp_iflag_f32_e32 v0, v0
	s_abs_i32 s16, s6
	s_xor_b32 s7, s6, s11
	s_ashr_i32 s7, s7, 31
	v_mul_f32_e32 v0, 0x4f7ffffe, v0
	v_cvt_u32_f32_e32 v0, v0
	s_nop 0
	v_readfirstlane_b32 s26, v0
	s_mul_i32 s25, s25, s26
	s_mul_hi_u32 s25, s26, s25
	s_add_i32 s26, s26, s25
	s_mul_hi_u32 s25, s16, s26
	s_mul_i32 s26, s25, s17
	s_sub_i32 s16, s16, s26
	s_add_i32 s26, s25, 1
	s_sub_i32 s55, s16, s17
	s_cmp_ge_u32 s16, s17
	s_cselect_b32 s25, s26, s25
	s_cselect_b32 s16, s55, s16
	s_add_i32 s26, s25, 1
	s_cmp_ge_u32 s16, s17
	s_cselect_b32 s16, s26, s25
	s_xor_b32 s16, s16, s7
	s_sub_i32 s25, s16, s7
	s_mul_i32 s7, s25, s11
	s_sub_i32 s6, s6, s7
	s_add_i32 s26, s6, s10
	v_readlane_b32 s6, v255, 23
	s_mov_b64 s[16:17], -1
	s_nop 0
	v_mov_b32_e32 v0, s6
	ds_read_b128 v[0:3], v0
	s_waitcnt lgkmcnt(0)
	v_cmp_ge_i32_e32 vcc, s26, v0
	v_cmp_ge_i32_e64 s[6:7], s26, v1
	s_nop 0
	v_cndmask_b32_e32 v0, 0, v0, vcc
	v_cndmask_b32_e64 v4, 0, 1, s[6:7]
	v_cndmask_b32_e64 v0, v0, v1, s[6:7]
	v_addc_co_u32_e32 v1, vcc, 0, v4, vcc
	v_cmp_ge_i32_e32 vcc, s26, v2
	v_readlane_b32 s6, v255, 24
	s_nop 0
	v_cndmask_b32_e64 v4, 0, 1, vcc
	v_cndmask_b32_e32 v0, v0, v2, vcc
	v_cmp_ge_i32_e32 vcc, s26, v3
	s_nop 1
	v_cndmask_b32_e32 v5, v0, v3, vcc
	v_mov_b32_e32 v0, s6
	v_addc_co_u32_e32 v4, vcc, v1, v4, vcc
	ds_read_b128 v[0:3], v0
	v_readlane_b32 s6, v255, 25
	s_waitcnt lgkmcnt(0)
	v_cmp_ge_i32_e32 vcc, s26, v0
	s_nop 1
	v_cndmask_b32_e64 v6, 0, 1, vcc
	v_cndmask_b32_e32 v0, v5, v0, vcc
	v_cmp_ge_i32_e32 vcc, s26, v1
	s_nop 1
	v_cndmask_b32_e32 v0, v0, v1, vcc
	v_addc_co_u32_e32 v1, vcc, v4, v6, vcc
	v_cmp_ge_i32_e32 vcc, s26, v2
	s_nop 1
	v_cndmask_b32_e64 v4, 0, 1, vcc
	v_cndmask_b32_e32 v0, v0, v2, vcc
	v_cmp_ge_i32_e32 vcc, s26, v3
	s_nop 1
	v_cndmask_b32_e32 v5, v0, v3, vcc
	v_mov_b32_e32 v0, s6
	v_addc_co_u32_e32 v4, vcc, v1, v4, vcc
	ds_read_b128 v[0:3], v0
	v_readlane_b32 s6, v255, 26
	s_waitcnt lgkmcnt(0)
	v_cmp_ge_i32_e32 vcc, s26, v0
	s_nop 1
	v_cndmask_b32_e64 v6, 0, 1, vcc
	v_cndmask_b32_e32 v0, v5, v0, vcc
	v_cmp_ge_i32_e32 vcc, s26, v1
	s_nop 1
	v_cndmask_b32_e32 v0, v0, v1, vcc
	v_addc_co_u32_e32 v1, vcc, v4, v6, vcc
	v_cmp_ge_i32_e32 vcc, s26, v2
	s_nop 1
	v_cndmask_b32_e64 v4, 0, 1, vcc
	v_cndmask_b32_e32 v0, v0, v2, vcc
	v_cmp_ge_i32_e32 vcc, s26, v3
	s_nop 1
	v_cndmask_b32_e32 v5, v0, v3, vcc
	v_mov_b32_e32 v0, s6
	v_addc_co_u32_e32 v4, vcc, v1, v4, vcc
	ds_read_b128 v[0:3], v0
	s_waitcnt lgkmcnt(0)
	v_cmp_ge_i32_e32 vcc, s26, v0
	s_nop 1
	v_cndmask_b32_e64 v6, 0, 1, vcc
	v_cndmask_b32_e32 v0, v5, v0, vcc
	v_cmp_ge_i32_e32 vcc, s26, v1
	s_nop 1
	v_cndmask_b32_e32 v0, v0, v1, vcc
	v_addc_co_u32_e32 v1, vcc, v4, v6, vcc
	v_cmp_ge_i32_e32 vcc, s26, v2
	s_nop 1
	v_cndmask_b32_e64 v4, 0, 1, vcc
	v_cndmask_b32_e32 v0, v0, v2, vcc
	v_cmp_ge_i32_e32 vcc, s26, v3
	s_nop 1
	v_cndmask_b32_e32 v0, v0, v3, vcc
	v_addc_co_u32_e32 v1, vcc, v1, v4, vcc
	v_readfirstlane_b32 s7, v0
	v_readfirstlane_b32 s6, v1
	s_sub_i32 s55, s26, s7

;     ...
;         const int gw = vcu * NWAVES + wave, NGW = G * NWAVES;
;         constexpr int C_IN = 32 * 188, C_OA = 8 * 32, C_OB = 16 * 32, C_O = 32 * 32, C_GU = 16 * 32 * 32, C_DN = 16 * 16 * 32, C_L = C_IN + C_OA + C_OB + C_O + C_GU + C_DN, NIT = DEPTH * C_L;
;         const int q4 = lane & 15, kk = lane >> 4;
;         auto decode = [&](int it) -> TrDesc {
;             TrDesc d; d.zero = 0; d.rope = 0; d.f8 = 0;
;             const int l = it / C_L; int r = it % C_L;
;             const float* W; unsigned char* WT; int ldw, K, k0, n0, scol, esz = 2;
;             if (r < C_IN) { const int kb = r / 188, nb = r % 188; n0 = 64 * nb; k0 = 64 * kb; ldw = NIN; K = D; W = a.w_in + (size_t)l * D * NIN;
;                 if (n0 < 3072) { d.rope = 1; scol = (n0 >> 7) * 128 + 32 * ((n0 >> 6) & 1) + 64 * (q4 >> 3) + 4 * (q4 & 7); }
;                 else if (n0 < 7680) scol = n0 + 4 * q4;
;                 else if (n0 < 11776) scol = n0 + 16 + 4 * q4;
;                 else if (n0 == 11776) { scol = (q4 < 4) ? 7680 + 4 * q4 : 0; d.zero = (q4 < 4) ? 0 : 1; }
;                 else { scol = 0; d.zero = 1; }
;     ...
;                 d.f8 = 1; esz = 1; WT = ws + WS_WIN + (size_t)l * NP * D;
;     ...
;                 WT = ws + WS_WIN + (size_t)l * NP * D * 2;
;     ...
;             } else if ((r -= C_IN) < C_OA) { const int kb = r / 32, nb = r % 32; n0 = 64 * nb; k0 = 64 * kb; ldw = D; K = 512; scol = n0 + 4 * q4; W = a.w_out_a + (size_t)l * 512 * D; WT = ws + WS_WOA + (size_t)l * D * 512 * (MIX_F8 ? 1 : 2); if (MIX_F8) { d.f8 = 1; esz = 1; }
;                 if (BR_FUSE) { K = 1536; WT = ws + WS_WOA + (size_t)l * D * 1536 + 1024; }
;             } else if ((r -= C_OA) < C_OB) { const int kb = r / 32, nb = r % 32; n0 = 64 * nb; k0 = 64 * kb; ldw = D; K = 1024; scol = n0 + 4 * q4; W = a.w_out_b + (size_t)l * 1024 * D; WT = ws + WS_WOB + (size_t)l * D * 1024 * (MIX_F8 ? 1 : 2); if (MIX_F8) { d.f8 = 1; esz = 1; }
;                 if (BR_FUSE) { K = 1536; WT = ws + WS_WOA + (size_t)l * D * 1536; }
;             } else if ((r -= C_OB) < C_O) { const int kb = r / 32, nb = r % 32; n0 = 64 * nb; k0 = 64 * kb; ldw = D; K = D; scol = n0 + 4 * q4; W = a.w_out + (size_t)l * D * D; WT = ws + WS_WO + (size_t)l * D * D * (MIX_F8 ? 1 : 2); if (MIX_F8) { d.f8 = 1; esz = 1; }
.LBB0_953:
	s_waitcnt vmcnt(0)
	s_barrier
	s_branch .LBB0_954
.Lhp_entry:
	v_writelane_b32 v251, s16, 0
	v_writelane_b32 v251, s17, 1
	v_writelane_b32 v251, s18, 2
	v_writelane_b32 v251, s19, 3
	v_writelane_b32 v251, s20, 4
	v_writelane_b32 v251, s21, 5
	v_writelane_b32 v251, s23, 6
	v_writelane_b32 v251, s25, 7
	v_writelane_b32 v251, s26, 8
	v_writelane_b32 v251, s33, 9
	v_writelane_b32 v251, s38, 10
	v_writelane_b32 v251, s39, 11
	v_writelane_b32 v251, s41, 12
	v_writelane_b32 v251, s42, 13
	v_writelane_b32 v251, s45, 14
	v_writelane_b32 v251, s48, 15
	v_writelane_b32 v251, s49, 16
	v_writelane_b32 v251, s50, 17
	v_writelane_b32 v251, s51, 18
	v_writelane_b32 v251, s74, 19
	v_writelane_b32 v251, s76, 20
	v_mov_b32_e32 v193, v3
	v_mov_b32_e32 v194, v33
	v_mov_b32_e32 v195, v59
	v_mov_b32_e32 v196, v63
	v_mov_b32_e32 v197, v110
	v_mov_b32_e32 v198, v111
	v_mov_b32_e32 v199, v114
	v_mov_b32_e32 v200, v115
	v_mov_b32_e32 v201, v149
	v_mov_b32_e32 v202, v153
	v_mov_b32_e32 v203, v157
	v_mov_b32_e32 v204, v161
	v_mov_b32_e32 v205, v165
	v_mov_b32_e32 v206, v169
	v_mov_b32_e32 v207, v173
	v_mov_b32_e32 v208, v177
	v_mov_b32_e32 v209, v178
	v_mov_b32_e32 v210, v179
	v_mov_b32_e32 v211, v180
	v_mov_b32_e32 v212, v181
	v_mov_b32_e32 v214, v182
	v_mov_b32_e32 v215, v183
	v_mov_b32_e32 v216, v184
	v_mov_b32_e32 v218, v185
	v_readlane_b32 s76, v253, 4
	v_readlane_b32 s8, v253, 0
	v_readlane_b32 s9, v253, 1
	s_nop 1
	s_and_b32 s0, s76, 7
	s_lshr_b32 s1, s76, 3
	s_sub_i32 s1, s1, 28
	s_lshl_b32 s0, s0, 1
	s_lshr_b32 s2, s1, 1
	s_add_i32 s0, s0, s2
	s_and_b32 s1, s1, 1
	s_lshr_b32 s2, s0, 2
	s_lshl_b32 s2, s2, 3
	s_lshl_b32 s1, s1, 2
	s_and_b32 s0, s0, 3
	s_or_b32 s2, s2, s1
	s_or_b32 s76, s2, s0
	s_lshr_b32 s33, s78, 6
	s_movk_i32 s74, 32
	s_load_dwordx2 s[10:11], s[8:9], 0xa0
	v_mbcnt_lo_u32_b32 v69, -1, 0
	v_mbcnt_hi_u32_b32 v69, -1, v69
	s_mov_b64 exec, -1
	v_lshlrev_b32_e32 v76, 3, v69
	s_waitcnt lgkmcnt(0)
	s_branch .Lhp_common
.Lhp_entry_all:
	v_writelane_b32 v251, s16, 0
	v_writelane_b32 v251, s17, 1
	v_writelane_b32 v251, s18, 2
	v_writelane_b32 v251, s19, 3
	v_writelane_b32 v251, s20, 4
	v_writelane_b32 v251, s21, 5
	v_writelane_b32 v251, s23, 6
	v_writelane_b32 v251, s25, 7
	v_writelane_b32 v251, s26, 8
	v_writelane_b32 v251, s33, 9
	v_writelane_b32 v251, s38, 10
	v_writelane_b32 v251, s39, 11
	v_writelane_b32 v251, s41, 12
	v_writelane_b32 v251, s42, 13
	v_writelane_b32 v251, s45, 14
	v_writelane_b32 v251, s48, 15
	v_writelane_b32 v251, s49, 16
	v_writelane_b32 v251, s50, 17
	v_writelane_b32 v251, s51, 18
	v_writelane_b32 v251, s74, 19
	v_writelane_b32 v251, s76, 20
	v_mov_b32_e32 v193, v3
	v_mov_b32_e32 v194, v33
	v_mov_b32_e32 v195, v59
	v_mov_b32_e32 v196, v63
	v_mov_b32_e32 v197, v110
	v_mov_b32_e32 v198, v111
	v_mov_b32_e32 v199, v114
	v_mov_b32_e32 v200, v115
	v_mov_b32_e32 v201, v149
	v_mov_b32_e32 v202, v153
	v_mov_b32_e32 v203, v157
	v_mov_b32_e32 v204, v161
	v_mov_b32_e32 v205, v165
	v_mov_b32_e32 v206, v169
	v_mov_b32_e32 v207, v173
	v_mov_b32_e32 v208, v177
	v_mov_b32_e32 v209, v178
	v_mov_b32_e32 v210, v179
	v_mov_b32_e32 v211, v180
	v_mov_b32_e32 v212, v181
	v_mov_b32_e32 v214, v182
	v_mov_b32_e32 v215, v183
	v_mov_b32_e32 v216, v184
	v_mov_b32_e32 v218, v185
	v_readlane_b32 s8, v253, 0
	v_readlane_b32 s9, v253, 1
	s_nop 1
	s_lshr_b32 s33, s78, 6
	s_movk_i32 s74, 0x100
	s_load_dwordx2 s[10:11], s[8:9], 0xa0
	v_mbcnt_lo_u32_b32 v69, -1, 0
	v_mbcnt_hi_u32_b32 v69, -1, v69
	s_mov_b64 exec, -1
	v_lshlrev_b32_e32 v76, 3, v69
	s_waitcnt lgkmcnt(0)
	s_branch .Lhp_common
.Lhp_common:
	s_lshl_b32 s47, s76, 3
	s_add_i32 s47, s47, s33
	s_add_i32 s47, s47, s100
	v_and_b32_e32 v2, 15, v69
	s_cmp_ge_i32 s47, s101
	v_ashrrev_i32_e32 v133, 4, v69
	s_cbranch_scc1 .LBB0_36_hp
	s_sub_i32 s1, 0xfcff, s47
	s_mul_hi_u32 s0, s1, 0x81848da9
	s_lshr_b32 s0, s0, 14
	s_mul_i32 s2, s0, 0x7e80
	s_sub_i32 s17, s1, s2
	s_cmpk_gt_u32 s17, 0x177f
	s_cbranch_scc0 .LBB0_37_hp
	s_cmpk_gt_u32 s17, 0x187f
	s_cbranch_scc0 .LBB0_39_hp
	s_cmpk_gt_u32 s17, 0x1a7f
	s_cbranch_scc0 .LBB0_40_hp
	s_cmpk_gt_u32 s17, 0x1e7f
	s_cbranch_scc0 .LBB0_41_hp
	s_lshl_b32 s1, s17, 6
	s_cmpk_gt_u32 s17, 0x5e7f
	s_cbranch_scc0 .LBB0_42_hp
	s_add_i32 s2, s17, 0xffffa180
	s_lshr_b32 s4, s2, 9
	s_lshl_b32 s2, s2, 1
	s_and_b32 s18, s2, 0x3c0
	s_load_dwordx2 s[2:3], s[8:9], 0x88
	s_lshl_b32 s5, s0, 4
	s_add_i32 s6, s4, s5
	s_mov_b32 s7, 0
	s_and_b32 s16, s1, 0x7c0
	s_lshl_b64 s[4:5], s[6:7], 23
	s_waitcnt lgkmcnt(0)
	s_add_u32 s4, s2, s4
	s_addc_u32 s5, s3, s5
	s_lshl_b64 s[2:3], s[6:7], 21
	s_add_u32 s2, s10, s2
	s_addc_u32 s3, s11, s3
	s_add_u32 s6, s2, 0x18600000
	v_lshl_or_b32 v0, v2, 2, s16
	s_addc_u32 s7, s3, 0
	s_mov_b64 s[2:3], 0
	s_branch .LBB0_43_hp

;     ...
;             const int l = it / C_L; int r = it % C_L;
;             const float* W; unsigned char* WT; int ldw, K, k0, n0, scol, esz = 2;
;             if (r < C_IN) { const int kb = r / 188, nb = r % 188; n0 = 64 * nb; k0 = 64 * kb; ldw = NIN; K = D; W = a.w_in + (size_t)l * D * NIN;
;                 if (n0 < 3072) { d.rope = 1; scol = (n0 >> 7) * 128 + 32 * ((n0 >> 6) & 1) + 64 * (q4 >> 3) + 4 * (q4 & 7); }
;                 else if (n0 < 7680) scol = n0 + 4 * q4;
;                 else if (n0 < 11776) scol = n0 + 16 + 4 * q4;
;                 else if (n0 == 11776) { scol = (q4 < 4) ? 7680 + 4 * q4 : 0; d.zero = (q4 < 4) ? 0 : 1; }
;                 else { scol = 0; d.zero = 1; }
;     ...
;                 d.f8 = 1; esz = 1; WT = ws + WS_WIN + (size_t)l * NP * D;
;     ...
;                 WT = ws + WS_WIN + (size_t)l * NP * D * 2;
;     ...
;             } else if ((r -= C_IN) < C_OA) { const int kb = r / 32, nb = r % 32; n0 = 64 * nb; k0 = 64 * kb; ldw = D; K = 512; scol = n0 + 4 * q4; W = a.w_out_a + (size_t)l * 512 * D; WT = ws + WS_WOA + (size_t)l * D * 512 * (MIX_F8 ? 1 : 2); if (MIX_F8) { d.f8 = 1; esz = 1; }
;                 if (BR_FUSE) { K = 1536; WT = ws + WS_WOA + (size_t)l * D * 1536 + 1024; }
;             } else if ((r -= C_OA) < C_OB) { const int kb = r / 32, nb = r % 32; n0 = 64 * nb; k0 = 64 * kb; ldw = D; K = 1024; scol = n0 + 4 * q4; W = a.w_out_b + (size_t)l * 1024 * D; WT = ws + WS_WOB + (size_t)l * D * 1024 * (MIX_F8 ? 1 : 2); if (MIX_F8) { d.f8 = 1; esz = 1; }
;                 if (BR_FUSE) { K = 1536; WT = ws + WS_WOA + (size_t)l * D * 1536; }
;             } else if ((r -= C_OB) < C_O) { const int kb = r / 32, nb = r % 32; n0 = 64 * nb; k0 = 64 * kb; ldw = D; K = D; scol = n0 + 4 * q4; W = a.w_out + (size_t)l * D * D; WT = ws + WS_WO + (size_t)l * D * D * (MIX_F8 ? 1 : 2); if (MIX_F8) { d.f8 = 1; esz = 1; }
;     ...
;         while (it < NIT) {
;             const int itB = it + NGW;
;             if (itB < NIT) { dB = decode(NIT - 1 - itB); tr_load(dB, vB); }
;             tr_finish(dA, vA, scr, lane);
;             if (itB >= NIT) break;
;             const int itA = itB + NGW;
;             if (itA < NIT) { dA = decode(NIT - 1 - itA); tr_load(dA, vA); }
;             tr_finish(dB, vB, scr, lane);
;             it = itA;
.LBB0_72_hp:
	s_cmp_ge_i32 s42, s101
	s_cbranch_scc1 .LBB0_70_hp
	s_add_i32 s44, s42, s48
	s_cmp_lt_i32 s44, s101
	s_cselect_b64 s[20:21], -1, 0
	s_cmp_ge_i32 s44, s101
	s_cselect_b64 s[12:13], -1, 0
	s_and_b64 vcc, exec, s[12:13]
	s_cbranch_vccnz .LBB0_106_hp
	s_sub_i32 s3, 0xfcff, s44
	s_mul_hi_u32 s0, s3, 0x81848da9
	s_lshr_b32 s0, s0, 14
	s_mul_i32 s14, s0, 0x7e80
	s_sub_i32 s45, s3, s14
	s_cmpk_gt_u32 s45, 0x177f
	s_cbranch_scc0 .LBB0_81_hp
	s_cmpk_gt_u32 s45, 0x187f
	s_cbranch_scc0 .LBB0_83_hp
	s_cmpk_gt_u32 s45, 0x1a7f
	s_cbranch_scc0 .LBB0_84_hp
	s_cmpk_gt_u32 s45, 0x1e7f
	s_cbranch_scc0 .LBB0_85_hp
	s_lshl_b32 s24, s45, 6
	s_cmpk_gt_u32 s45, 0x5e7f
	s_cbranch_scc0 .LBB0_121_hp
	s_add_i32 s14, s45, 0xffffa180
	s_lshr_b32 s18, s14, 9
	s_lshl_b32 s14, s14, 1
	s_and_b32 s49, s14, 0x3c0
	s_load_dwordx2 s[14:15], s[8:9], 0x88
	s_lshl_b32 s19, s0, 4
	s_add_i32 s22, s18, s19
	s_mov_b32 s23, s1
	s_and_b32 s3, s24, 0x7c0
	s_lshl_b64 s[18:19], s[22:23], 23
	s_waitcnt lgkmcnt(0)
	s_add_u32 s18, s14, s18
	s_addc_u32 s19, s15, s19
	s_lshl_b64 s[14:15], s[22:23], 21
	s_add_u32 s22, s28, s14
	v_or_b32_e32 v0, s3, v136
	s_addc_u32 s23, s29, s15
	s_cbranch_execz .LBB0_122_hp
	s_movk_i32 s14, 0x400
	s_mov_b64 s[24:25], 0x800
	s_cbranch_execz .LBB0_86_hp
	s_branch .LBB0_87_hp

; #define LAS __attribute__((address_space(3)))
; #define GAS __attribute__((address_space(1)))
; #define LDS_WAIT() asm volatile("s_waitcnt lgkmcnt(0)" ::: "memory")
; __device__ __forceinline__ unsigned pk_fp8x4(float a, float b, float c, float d) { int p = __builtin_amdgcn_cvt_pk_fp8_f32(sat8(a), sat8(b), 0, false); p = __builtin_amdgcn_cvt_pk_fp8_f32(sat8(c), sat8(d), p, true); return (unsigned)p; }
; __device__ __forceinline__ void tr_finish(const TrDesc& d, f32x4 (&v)[16], LAS float* scr, int lane) {
;     ...
;     { LAS float* rp = scr + kk * 65 + d0;
; #pragma unroll
;         for (int i = 0; i < 16; ++i) { rp[4 * i * 65] = v[i][0]; rp[4 * i * 65 + ds] = v[i][1]; rp[4 * i * 65 + 2 * ds] = v[i][2]; rp[4 * i * 65 + 3 * ds] = v[i][3]; } }
;     LDS_WAIT(); asm volatile("" ::: "memory");
;     if (d.f8) {
;         const int c = lane & 3, nl = lane >> 2; const LAS float* sp = scr + (16 * c) * 65 + nl; unsigned char* dp = d.dst + (size_t)nl * d.K + 16 * c;
; #pragma unroll
;         for (int j = 0; j < 4; ++j) { u32x4 o;
;             o.x = pk_fp8x4(sp[0 * 65 + 16 * j] * 32.0f, sp[1 * 65 + 16 * j] * 32.0f, sp[2 * 65 + 16 * j] * 32.0f, sp[3 * 65 + 16 * j] * 32.0f);
;             o.y = pk_fp8x4(sp[4 * 65 + 16 * j] * 32.0f, sp[5 * 65 + 16 * j] * 32.0f, sp[6 * 65 + 16 * j] * 32.0f, sp[7 * 65 + 16 * j] * 32.0f);
;             o.z = pk_fp8x4(sp[8 * 65 + 16 * j] * 32.0f, sp[9 * 65 + 16 * j] * 32.0f, sp[10 * 65 + 16 * j] * 32.0f, sp[11 * 65 + 16 * j] * 32.0f);
;             o.w = pk_fp8x4(sp[12 * 65 + 16 * j] * 32.0f, sp[13 * 65 + 16 * j] * 32.0f, sp[14 * 65 + 16 * j] * 32.0f, sp[15 * 65 + 16 * j] * 32.0f);
;             *(GAS u32x4*)(dp + (size_t)(16 * j) * d.K) = o; }
.LBB0_108_hp:
	s_or_b64 exec, exec, s[22:23]
	s_cmp_eq_u32 s43, 0
	s_cselect_b64 vcc, -1, 0
	s_cmp_lg_u32 s43, 0
	s_cselect_b64 s[22:23], -1, 0
	v_cndmask_b32_e64 v2, 0, 1, s[22:23]
	s_and_b64 s[22:23], s[22:23], exec
	v_cndmask_b32_e32 v0, v140, v136, vcc
	s_cselect_b32 s0, 2, 1
	v_lshl_add_u32 v0, v0, 2, v141
	s_lshl_b32 s3, s0, 2
	v_add_u32_e32 v3, s3, v0
	v_lshlrev_b32_e64 v2, v2, 3
	s_waitcnt vmcnt(15)
	ds_write_b32 v3, v5
	v_lshl_add_u32 v3, s0, 3, v0
	v_lshl_add_u32 v2, v2, 2, v0
	v_subrev_u32_e32 v146, s3, v3
	ds_write_b32 v0, v4
	ds_write_b32 v3, v6
	ds_write_b32 v2, v7
	s_waitcnt vmcnt(14)
	ds_write_b32 v0, v8 offset:1040
	ds_write_b32 v146, v9 offset:1040
	ds_write_b32 v3, v10 offset:1040
	ds_write_b32 v2, v11 offset:1040
	s_waitcnt vmcnt(13)
	ds_write_b32 v0, v12 offset:2080
	ds_write_b32 v146, v13 offset:2080
	ds_write_b32 v3, v14 offset:2080
	ds_write_b32 v2, v15 offset:2080
	s_waitcnt vmcnt(12)
	ds_write_b32 v0, v16 offset:3120
	ds_write_b32 v146, v17 offset:3120
	ds_write_b32 v3, v18 offset:3120
	ds_write_b32 v2, v19 offset:3120
	s_waitcnt vmcnt(11)
	ds_write_b32 v0, v20 offset:4160
	ds_write_b32 v146, v21 offset:4160
	ds_write_b32 v3, v22 offset:4160
	ds_write_b32 v2, v23 offset:4160
	s_waitcnt vmcnt(10)
	ds_write_b32 v0, v24 offset:5200
	ds_write_b32 v146, v25 offset:5200
	ds_write_b32 v3, v26 offset:5200
	ds_write_b32 v2, v27 offset:5200
	s_waitcnt vmcnt(9)
	ds_write_b32 v0, v28 offset:6240
	ds_write_b32 v146, v29 offset:6240
	ds_write_b32 v3, v30 offset:6240
	ds_write_b32 v2, v31 offset:6240
	s_waitcnt vmcnt(8)
	ds_write_b32 v0, v32 offset:7280
	ds_write_b32 v146, v33 offset:7280
	ds_write_b32 v3, v34 offset:7280
	ds_write_b32 v2, v35 offset:7280
	s_waitcnt vmcnt(7)
	ds_write_b32 v0, v36 offset:8320
	ds_write_b32 v146, v37 offset:8320
	ds_write_b32 v3, v38 offset:8320
	ds_write_b32 v2, v39 offset:8320
	s_waitcnt vmcnt(6)
	ds_write_b32 v0, v40 offset:9360
	ds_write_b32 v146, v41 offset:9360
	ds_write_b32 v3, v42 offset:9360
	ds_write_b32 v2, v43 offset:9360
	s_waitcnt vmcnt(5)
	ds_write_b32 v0, v44 offset:10400
	ds_write_b32 v146, v45 offset:10400
	ds_write_b32 v3, v46 offset:10400
	ds_write_b32 v2, v47 offset:10400
	s_waitcnt vmcnt(4)
	ds_write_b32 v0, v48 offset:11440
	ds_write_b32 v146, v49 offset:11440
	ds_write_b32 v3, v50 offset:11440
	ds_write_b32 v2, v51 offset:11440
	s_waitcnt vmcnt(3)
	ds_write_b32 v0, v52 offset:12480
	ds_write_b32 v146, v53 offset:12480
	ds_write_b32 v3, v54 offset:12480
	ds_write_b32 v2, v55 offset:12480
	s_waitcnt vmcnt(2)
	ds_write_b32 v0, v56 offset:13520
	ds_write_b32 v146, v57 offset:13520
	ds_write_b32 v3, v58 offset:13520
	ds_write_b32 v2, v59 offset:13520
	s_waitcnt vmcnt(1)
	ds_write_b32 v0, v60 offset:14560
	ds_write_b32 v146, v61 offset:14560
	ds_write_b32 v3, v62 offset:14560
	ds_write_b32 v2, v63 offset:14560
	s_waitcnt vmcnt(0)
	ds_write_b32 v0, v64 offset:15600
	ds_write_b32 v146, v65 offset:15600
	ds_write_b32 v3, v66 offset:15600
	ds_write_b32 v2, v67 offset:15600
	s_waitcnt lgkmcnt(0)
	ds_read2_b32 v[2:3], v142 offset1:16
	ds_read2_b32 v[148:149], v142 offset0:65 offset1:81
	ds_read2_b32 v[154:155], v142 offset0:130 offset1:146
	ds_read2_b32 v[156:157], v142 offset0:195 offset1:211
	v_mov_b32_e32 v150, 0
	s_waitcnt lgkmcnt(3)
	v_mul_f32_e32 v0, 0x42000000, v2
	s_waitcnt lgkmcnt(2)
	v_mul_f32_e32 v2, 0x42000000, v148
	v_med3_f32 v0, v0, s41, v143
	s_waitcnt lgkmcnt(0)
	v_mul_f32_e32 v147, 0x42000000, v156
	v_med3_f32 v2, v2, s41, v143
	v_cvt_pk_fp8_f32 v150, v0, v2
	v_med3_f32 v2, v147, s41, v143
	v_add_u32_e32 v147, 0x400, v142
	ds_read2_b32 v[160:161], v147 offset0:4 offset1:20
	ds_read2_b32 v[162:163], v147 offset0:69 offset1:85
	ds_read2_b32 v[164:165], v147 offset0:134 offset1:150
	ds_read2_b32 v[166:167], v147 offset0:199 offset1:215
	v_mul_f32_e32 v146, 0x42000000, v154
	v_med3_f32 v0, v146, s41, v143
	v_cvt_pk_fp8_f32 v150, v0, v2 op_sel:[0,0,1]
	s_waitcnt lgkmcnt(3)
	v_mul_f32_e32 v0, 0x42000000, v160
	s_waitcnt lgkmcnt(2)
	v_mul_f32_e32 v2, 0x42000000, v162
	s_waitcnt lgkmcnt(0)
	v_mul_f32_e32 v148, 0x42000000, v166
	v_med3_f32 v0, v0, s41, v143
	v_med3_f32 v2, v2, s41, v143
	v_mov_b32_e32 v151, 0
	v_cvt_pk_fp8_f32 v151, v0, v2
	v_med3_f32 v2, v148, s41, v143
	v_add_u32_e32 v148, 0x800, v142
	ds_read2_b32 v[168:169], v148 offset0:8 offset1:24
	ds_read2_b32 v[170:171], v148 offset0:73 offset1:89
	ds_read2_b32 v[172:173], v148 offset0:138 offset1:154
	ds_read2_b32 v[174:175], v148 offset0:203 offset1:219
	v_mul_f32_e32 v146, 0x42000000, v164
	v_med3_f32 v0, v146, s41, v143
	v_cvt_pk_fp8_f32 v151, v0, v2 op_sel:[0,0,1]
	s_waitcnt lgkmcnt(3)
	v_mul_f32_e32 v0, 0x42000000, v168
	s_waitcnt lgkmcnt(2)
	v_mul_f32_e32 v2, 0x42000000, v170
	s_waitcnt lgkmcnt(1)
	v_mul_f32_e32 v146, 0x42000000, v172
	v_med3_f32 v0, v0, s41, v143
	v_med3_f32 v2, v2, s41, v143
	v_mov_b32_e32 v152, 0
	v_cvt_pk_fp8_f32 v152, v0, v2
	v_med3_f32 v0, v146, s41, v143
	v_add_u32_e32 v146, 0xc00, v142
	ds_read2_b32 v[176:177], v146 offset0:12 offset1:28
	ds_read2_b32 v[178:179], v146 offset0:77 offset1:93
	ds_read2_b32 v[180:181], v146 offset0:142 offset1:158
	s_waitcnt lgkmcnt(3)
	v_mul_f32_e32 v153, 0x42000000, v174
	v_med3_f32 v2, v153, s41, v143
	ds_read2_b32 v[182:183], v146 offset0:207 offset1:223
	v_cvt_pk_fp8_f32 v152, v0, v2 op_sel:[0,0,1]
	s_waitcnt lgkmcnt(3)
	v_mul_f32_e32 v0, 0x42000000, v176
	s_waitcnt lgkmcnt(2)
	v_mul_f32_e32 v2, 0x42000000, v178
	v_med3_f32 v0, v0, s41, v143
	v_med3_f32 v2, v2, s41, v143
	v_mov_b32_e32 v153, 0
	v_cvt_pk_fp8_f32 v153, v0, v2
	s_waitcnt lgkmcnt(1)
	v_mul_f32_e32 v154, 0x42000000, v180
	s_waitcnt lgkmcnt(0)
; #define GAS __attribute__((address_space(1)))
; __device__ __forceinline__ unsigned pk_fp8x4(float a, float b, float c, float d) { int p = __builtin_amdgcn_cvt_pk_fp8_f32(sat8(a), sat8(b), 0, false); p = __builtin_amdgcn_cvt_pk_fp8_f32(sat8(c), sat8(d), p, true); return (unsigned)p; }
; __device__ __forceinline__ void tr_finish(const TrDesc& d, f32x4 (&v)[16], LAS float* scr, int lane) {
;     ...
;         for (int j = 0; j < 4; ++j) { u32x4 o;
;             o.x = pk_fp8x4(sp[0 * 65 + 16 * j] * 32.0f, sp[1 * 65 + 16 * j] * 32.0f, sp[2 * 65 + 16 * j] * 32.0f, sp[3 * 65 + 16 * j] * 32.0f);
;             o.y = pk_fp8x4(sp[4 * 65 + 16 * j] * 32.0f, sp[5 * 65 + 16 * j] * 32.0f, sp[6 * 65 + 16 * j] * 32.0f, sp[7 * 65 + 16 * j] * 32.0f);
;             o.z = pk_fp8x4(sp[8 * 65 + 16 * j] * 32.0f, sp[9 * 65 + 16 * j] * 32.0f, sp[10 * 65 + 16 * j] * 32.0f, sp[11 * 65 + 16 * j] * 32.0f);
;             o.w = pk_fp8x4(sp[12 * 65 + 16 * j] * 32.0f, sp[13 * 65 + 16 * j] * 32.0f, sp[14 * 65 + 16 * j] * 32.0f, sp[15 * 65 + 16 * j] * 32.0f);
;             *(GAS u32x4*)(dp + (size_t)(16 * j) * d.K) = o; }
;     ...
;             if (itB >= NIT) break;
;             const int itA = itB + NGW;
;             if (itA < NIT) { dA = decode(NIT - 1 - itA); tr_load(dA, vA); }
	v_mul_f32_e32 v0, 0x42000000, v182
	v_med3_f32 v2, v154, s41, v143
	v_med3_f32 v0, v0, s41, v143
	v_cvt_pk_fp8_f32 v153, v2, v0 op_sel:[0,0,1]
	v_mov_b64_e32 v[158:159], s[16:17]
	v_mad_i64_i32 v[158:159], s[22:23], s2, v132, v[158:159]
	v_lshl_add_u64 v[158:159], v[158:159], 0, v[134:135]
	v_mul_f32_e32 v0, 0x42000000, v3
	v_mul_f32_e32 v2, 0x42000000, v149
	global_store_dwordx4 v[158:159], v[150:153], off
	v_med3_f32 v0, v0, s41, v143
	v_med3_f32 v2, v2, s41, v143
	v_mov_b32_e32 v150, 0
	v_cvt_pk_fp8_f32 v150, v0, v2
	v_mul_f32_e32 v3, 0x42000000, v155
	v_mul_f32_e32 v0, 0x42000000, v157
	v_med3_f32 v2, v3, s41, v143
	v_med3_f32 v0, v0, s41, v143
	v_cvt_pk_fp8_f32 v150, v2, v0 op_sel:[0,0,1]
	v_mul_f32_e32 v0, 0x42000000, v161
	v_mul_f32_e32 v2, 0x42000000, v163
	v_med3_f32 v0, v0, s41, v143
	v_med3_f32 v2, v2, s41, v143
	v_mov_b32_e32 v151, 0
	v_cvt_pk_fp8_f32 v151, v0, v2
	v_mul_f32_e32 v3, 0x42000000, v165
	v_mul_f32_e32 v0, 0x42000000, v167
	v_med3_f32 v2, v3, s41, v143
	v_med3_f32 v0, v0, s41, v143
	v_cvt_pk_fp8_f32 v151, v2, v0 op_sel:[0,0,1]
	v_mul_f32_e32 v0, 0x42000000, v169
	v_mul_f32_e32 v2, 0x42000000, v171
	v_med3_f32 v0, v0, s41, v143
	v_med3_f32 v2, v2, s41, v143
	v_mov_b32_e32 v152, 0
	v_cvt_pk_fp8_f32 v152, v0, v2
	v_mul_f32_e32 v3, 0x42000000, v173
	v_mul_f32_e32 v0, 0x42000000, v175
	v_med3_f32 v2, v3, s41, v143
	v_med3_f32 v0, v0, s41, v143
	v_cvt_pk_fp8_f32 v152, v2, v0 op_sel:[0,0,1]
	v_mul_f32_e32 v0, 0x42000000, v177
	v_mul_f32_e32 v2, 0x42000000, v179
	v_med3_f32 v0, v0, s41, v143
	v_med3_f32 v2, v2, s41, v143
	v_mov_b32_e32 v153, 0
	v_cvt_pk_fp8_f32 v153, v0, v2
	s_ashr_i32 s3, s2, 31
	v_mul_f32_e32 v3, 0x42000000, v181
	v_mul_f32_e32 v0, 0x42000000, v183
	v_med3_f32 v2, v3, s41, v143
	v_med3_f32 v0, v0, s41, v143
	s_lshl_b64 s[22:23], s[2:3], 4
	v_cvt_pk_fp8_f32 v153, v2, v0 op_sel:[0,0,1]
	v_lshl_add_u64 v[2:3], v[158:159], 0, s[22:23]
	ds_read2_b32 v[154:155], v142 offset0:32 offset1:48
	ds_read2_b32 v[156:157], v142 offset0:97 offset1:113
	ds_read2_b32 v[158:159], v142 offset0:162 offset1:178
	ds_read2_b32 v[160:161], v142 offset0:227 offset1:243
	s_andn2_b64 vcc, exec, s[20:21]
	s_waitcnt lgkmcnt(3)
	v_mul_f32_e32 v0, 0x42000000, v154
	s_waitcnt lgkmcnt(2)
	v_mul_f32_e32 v149, 0x42000000, v156
	global_store_dwordx4 v[2:3], v[150:153], off
	v_med3_f32 v0, v0, s41, v143
	v_med3_f32 v149, v149, s41, v143
	v_mov_b32_e32 v150, 0
	v_cvt_pk_fp8_f32 v150, v0, v149
	ds_read2_b32 v[162:163], v147 offset0:36 offset1:52
	ds_read2_b32 v[164:165], v147 offset0:101 offset1:117
	ds_read2_b32 v[166:167], v147 offset0:166 offset1:182
	ds_read2_b32 v[168:169], v147 offset0:231 offset1:247
	s_waitcnt lgkmcnt(5)
	v_mul_f32_e32 v151, 0x42000000, v158
	s_waitcnt lgkmcnt(4)
	v_mul_f32_e32 v152, 0x42000000, v160
	v_med3_f32 v0, v151, s41, v143
	v_med3_f32 v149, v152, s41, v143
	v_cvt_pk_fp8_f32 v150, v0, v149 op_sel:[0,0,1]
	s_waitcnt lgkmcnt(3)
	v_mul_f32_e32 v0, 0x42000000, v162
	s_waitcnt lgkmcnt(2)
	v_mul_f32_e32 v149, 0x42000000, v164
	v_med3_f32 v0, v0, s41, v143
	v_med3_f32 v149, v149, s41, v143
	v_mov_b32_e32 v151, 0
	v_cvt_pk_fp8_f32 v151, v0, v149
	ds_read2_b32 v[170:171], v148 offset0:40 offset1:56
	ds_read2_b32 v[172:173], v148 offset0:105 offset1:121
	ds_read2_b32 v[174:175], v148 offset0:170 offset1:186
	ds_read2_b32 v[176:177], v148 offset0:235 offset1:251
	s_waitcnt lgkmcnt(5)
	v_mul_f32_e32 v152, 0x42000000, v166
	s_waitcnt lgkmcnt(4)
	v_mul_f32_e32 v153, 0x42000000, v168
	v_med3_f32 v0, v152, s41, v143
	v_med3_f32 v149, v153, s41, v143
	v_cvt_pk_fp8_f32 v151, v0, v149 op_sel:[0,0,1]
	s_waitcnt lgkmcnt(3)
	v_mul_f32_e32 v0, 0x42000000, v170
	s_waitcnt lgkmcnt(2)
	v_mul_f32_e32 v149, 0x42000000, v172
	v_med3_f32 v0, v0, s41, v143
	v_med3_f32 v149, v149, s41, v143
	v_mov_b32_e32 v152, 0
	v_cvt_pk_fp8_f32 v152, v0, v149
	ds_read2_b32 v[178:179], v146 offset0:44 offset1:60
	ds_read2_b32 v[180:181], v146 offset0:109 offset1:125
	ds_read2_b32 v[182:183], v146 offset0:174 offset1:190
	s_waitcnt lgkmcnt(4)
	v_mul_f32_e32 v153, 0x42000000, v174
	s_waitcnt lgkmcnt(3)
	v_mul_f32_e32 v154, 0x42000000, v176
	v_med3_f32 v0, v153, s41, v143
	v_med3_f32 v149, v154, s41, v143
	ds_read2_b32 v[184:185], v146 offset0:239 offset1:255
	v_cvt_pk_fp8_f32 v152, v0, v149 op_sel:[0,0,1]
	s_waitcnt lgkmcnt(3)
	v_mul_f32_e32 v0, 0x42000000, v178
	s_waitcnt lgkmcnt(2)
	v_mul_f32_e32 v149, 0x42000000, v180
	v_med3_f32 v0, v0, s41, v143
	v_med3_f32 v149, v149, s41, v143
	v_mov_b32_e32 v153, 0
	v_cvt_pk_fp8_f32 v153, v0, v149
	s_waitcnt lgkmcnt(1)
	v_mul_f32_e32 v154, 0x42000000, v182
	s_waitcnt lgkmcnt(0)
	v_mul_f32_e32 v0, 0x42000000, v184
	v_med3_f32 v149, v154, s41, v143
	v_med3_f32 v0, v0, s41, v143
	v_cvt_pk_fp8_f32 v153, v149, v0 op_sel:[0,0,1]
	v_mul_f32_e32 v0, 0x42000000, v155
	v_mul_f32_e32 v149, 0x42000000, v157
	v_med3_f32 v0, v0, s41, v143
	v_med3_f32 v149, v149, s41, v143
	v_mov_b32_e32 v154, 0
	v_cvt_pk_fp8_f32 v154, v0, v149
	v_mul_f32_e32 v155, 0x42000000, v159
	v_mul_f32_e32 v0, 0x42000000, v161
	v_med3_f32 v149, v155, s41, v143
	v_med3_f32 v0, v0, s41, v143
	v_cvt_pk_fp8_f32 v154, v149, v0 op_sel:[0,0,1]
	v_mul_f32_e32 v0, 0x42000000, v163
	v_mul_f32_e32 v149, 0x42000000, v165
	v_med3_f32 v0, v0, s41, v143
	v_med3_f32 v149, v149, s41, v143
	v_mov_b32_e32 v155, 0
	v_cvt_pk_fp8_f32 v155, v0, v149
	v_mul_f32_e32 v156, 0x42000000, v167
	v_mul_f32_e32 v0, 0x42000000, v169
	v_med3_f32 v149, v156, s41, v143
	v_med3_f32 v0, v0, s41, v143
	v_cvt_pk_fp8_f32 v155, v149, v0 op_sel:[0,0,1]
	v_mul_f32_e32 v0, 0x42000000, v171
	v_mul_f32_e32 v149, 0x42000000, v173
	v_med3_f32 v0, v0, s41, v143
	v_med3_f32 v149, v149, s41, v143
	v_mov_b32_e32 v156, 0
	v_cvt_pk_fp8_f32 v156, v0, v149
	v_mul_f32_e32 v157, 0x42000000, v175
	v_mul_f32_e32 v0, 0x42000000, v177
	v_med3_f32 v149, v157, s41, v143
	v_med3_f32 v0, v0, s41, v143
	v_cvt_pk_fp8_f32 v156, v149, v0 op_sel:[0,0,1]
	v_mul_f32_e32 v0, 0x42000000, v179
	v_mul_f32_e32 v149, 0x42000000, v181
	v_med3_f32 v0, v0, s41, v143
	v_med3_f32 v149, v149, s41, v143
	v_mov_b32_e32 v157, 0
	v_cvt_pk_fp8_f32 v157, v0, v149
	v_mul_f32_e32 v158, 0x42000000, v183
	v_mul_f32_e32 v0, 0x42000000, v185
	v_med3_f32 v149, v158, s41, v143
	v_med3_f32 v0, v0, s41, v143
	v_cvt_pk_fp8_f32 v157, v149, v0 op_sel:[0,0,1]
	v_lshl_add_u64 v[2:3], v[2:3], 0, s[22:23]
	global_store_dwordx4 v[2:3], v[150:153], off
	v_lshl_add_u64 v[2:3], v[2:3], 0, s[22:23]
	global_store_dwordx4 v[2:3], v[154:157], off
	s_waitcnt lgkmcnt(0)
	s_cbranch_vccnz .LBB0_71_hp
;     ...
;             const int l = it / C_L; int r = it % C_L;
;             const float* W; unsigned char* WT; int ldw, K, k0, n0, scol, esz = 2;
;             if (r < C_IN) { const int kb = r / 188, nb = r % 188; n0 = 64 * nb; k0 = 64 * kb; ldw = NIN; K = D; W = a.w_in + (size_t)l * D * NIN;
;                 if (n0 < 3072) { d.rope = 1; scol = (n0 >> 7) * 128 + 32 * ((n0 >> 6) & 1) + 64 * (q4 >> 3) + 4 * (q4 & 7); }
;                 else if (n0 < 7680) scol = n0 + 4 * q4;
;                 else if (n0 < 11776) scol = n0 + 16 + 4 * q4;
;                 else if (n0 == 11776) { scol = (q4 < 4) ? 7680 + 4 * q4 : 0; d.zero = (q4 < 4) ? 0 : 1; }
;                 else { scol = 0; d.zero = 1; }
;     ...
;                 d.f8 = 1; esz = 1; WT = ws + WS_WIN + (size_t)l * NP * D;
;     ...
;                 WT = ws + WS_WIN + (size_t)l * NP * D * 2;
;     ...
;             } else if ((r -= C_IN) < C_OA) { const int kb = r / 32, nb = r % 32; n0 = 64 * nb; k0 = 64 * kb; ldw = D; K = 512; scol = n0 + 4 * q4; W = a.w_out_a + (size_t)l * 512 * D; WT = ws + WS_WOA + (size_t)l * D * 512 * (MIX_F8 ? 1 : 2); if (MIX_F8) { d.f8 = 1; esz = 1; }
;                 if (BR_FUSE) { K = 1536; WT = ws + WS_WOA + (size_t)l * D * 1536 + 1024; }
;             } else if ((r -= C_OA) < C_OB) { const int kb = r / 32, nb = r % 32; n0 = 64 * nb; k0 = 64 * kb; ldw = D; K = 1024; scol = n0 + 4 * q4; W = a.w_out_b + (size_t)l * 1024 * D; WT = ws + WS_WOB + (size_t)l * D * 1024 * (MIX_F8 ? 1 : 2); if (MIX_F8) { d.f8 = 1; esz = 1; }
;                 if (BR_FUSE) { K = 1536; WT = ws + WS_WOA + (size_t)l * D * 1536; }
;             } else if ((r -= C_OB) < C_O) { const int kb = r / 32, nb = r % 32; n0 = 64 * nb; k0 = 64 * kb; ldw = D; K = D; scol = n0 + 4 * q4; W = a.w_out + (size_t)l * D * D; WT = ws + WS_WO + (size_t)l * D * D * (MIX_F8 ? 1 : 2); if (MIX_F8) { d.f8 = 1; esz = 1; }
;             } else if ((r -= C_O) < C_GU) { const int e = r / 1024, r2 = r % 1024, kb = r2 / 32, nb = r2 % 32, pn = nb >> 2, sgu = (nb >> 1) & 1, c0 = 64 * (nb & 1);
;                 n0 = 64 * nb; k0 = 64 * kb; ldw = FF; K = D; scol = 128 * pn + c0 + 4 * q4; W = (sgu ? a.w_up_e : a.w_gate_e) + (size_t)(l * NE + e) * D * FF; WT = ws + WS_WGU + (size_t)(l * NE + e) * 2048 * D; d.f8 = 1; esz = 1;
;             } else { r -= C_GU; const int e = r / 512, r2 = r % 512, kb = r2 / 32, nb = r2 % 32;
	s_add_i32 s42, s44, s48
	s_cmp_ge_i32 s42, s101
	s_cbranch_scc1 .LBB0_144_hp
	s_sub_i32 s2, 0xfcff, s42
	s_mul_hi_u32 s0, s2, 0x81848da9
	s_lshr_b32 s0, s0, 14
	s_mul_i32 s3, s0, 0x7e80
	s_sub_i32 s27, s2, s3
	s_cmpk_gt_u32 s27, 0x177f
	s_cbranch_scc0 .LBB0_117_hp
	s_cmpk_gt_u32 s27, 0x187f
	s_cbranch_scc0 .LBB0_119_hp
	s_cmpk_gt_u32 s27, 0x1a7f
	s_cbranch_scc0 .LBB0_120_hp
	s_cmpk_gt_u32 s27, 0x1e7f
	s_cbranch_scc0 .LBB0_123_hp
	s_lshl_b32 s22, s27, 6
	s_cmpk_gt_u32 s27, 0x5e7f
	s_cbranch_scc0 .LBB0_147_hp
	s_add_i32 s2, s27, 0xffffa180
	s_lshr_b32 s16, s2, 9
	s_lshl_b32 s2, s2, 1
	s_and_b32 s44, s2, 0x3c0
	s_load_dwordx2 s[2:3], s[8:9], 0x88
	s_lshl_b32 s17, s0, 4
	s_add_i32 s20, s16, s17
	s_mov_b32 s21, s1
	s_and_b32 s15, s22, 0x7c0
	s_lshl_b64 s[16:17], s[20:21], 23
	s_waitcnt lgkmcnt(0)
	s_add_u32 s16, s2, s16
	s_addc_u32 s17, s3, s17
	s_lshl_b64 s[2:3], s[20:21], 21
	s_add_u32 s20, s28, s2
	v_or_b32_e32 v0, s15, v136
	s_addc_u32 s21, s29, s3
	s_cbranch_execz .LBB0_148_hp
	s_movk_i32 s2, 0x400
	s_mov_b64 s[22:23], 0x800
	s_cbranch_execz .LBB0_124_hp
	s_branch .LBB0_125_hp

;     ...
;         int it = gw; TrDesc dA, dB; f32x4 vA[16], vB[16];
;         if (it < NIT) { dA = decode(NIT - 1 - it); tr_load(dA, vA); }
;         while (it < NIT) {
;             const int itB = it + NGW;
;             if (itB < NIT) { dB = decode(NIT - 1 - itB); tr_load(dB, vB); }
;             tr_finish(dA, vA, scr, lane);
;             if (itB >= NIT) break;
;             const int itA = itB + NGW;
;             if (itA < NIT) { dA = decode(NIT - 1 - itA); tr_load(dA, vA); }
;             tr_finish(dB, vB, scr, lane);
;             it = itA;
;         }
;     }
.Lhp_done:
	s_mov_b64 exec, -1
	s_waitcnt vmcnt(0) lgkmcnt(0)
	v_mov_b32_e32 v3, v193
	v_mov_b32_e32 v33, v194
	v_mov_b32_e32 v59, v195
	v_mov_b32_e32 v63, v196
	v_mov_b32_e32 v110, v197
	v_mov_b32_e32 v111, v198
	v_mov_b32_e32 v114, v199
	v_mov_b32_e32 v115, v200
	v_mov_b32_e32 v149, v201
	v_mov_b32_e32 v153, v202
	v_mov_b32_e32 v157, v203
	v_mov_b32_e32 v161, v204
	v_mov_b32_e32 v165, v205
	v_mov_b32_e32 v169, v206
	v_mov_b32_e32 v173, v207
	v_mov_b32_e32 v177, v208
	v_mov_b32_e32 v178, v209
	v_mov_b32_e32 v179, v210
	v_mov_b32_e32 v180, v211
	v_mov_b32_e32 v181, v212
	v_mov_b32_e32 v182, v214
	v_mov_b32_e32 v183, v215
	v_mov_b32_e32 v184, v216
	v_mov_b32_e32 v185, v218
	v_readlane_b32 s16, v251, 0
	v_readlane_b32 s17, v251, 1
	v_readlane_b32 s18, v251, 2
	v_readlane_b32 s19, v251, 3
	v_readlane_b32 s20, v251, 4
	v_readlane_b32 s21, v251, 5
	v_readlane_b32 s23, v251, 6
	v_readlane_b32 s25, v251, 7
	v_readlane_b32 s26, v251, 8
	v_readlane_b32 s33, v251, 9
	v_readlane_b32 s38, v251, 10
	v_readlane_b32 s39, v251, 11
	v_readlane_b32 s41, v251, 12
	v_readlane_b32 s42, v251, 13
	v_readlane_b32 s45, v251, 14
	v_readlane_b32 s48, v251, 15
	v_readlane_b32 s49, v251, 16
	v_readlane_b32 s50, v251, 17
	v_readlane_b32 s51, v251, 18
	v_readlane_b32 s74, v251, 19
	v_readlane_b32 s76, v251, 20
	v_readlane_b32 s0, v251, 30
	s_nop 4
	s_cmp_eq_u32 s0, 0
	s_cbranch_scc1 .LBB0_954
	s_branch .LBB0_1026

; #define PG8_STAGE(bufoff, soffB, voff) do { _Pragma("unroll") for (int _i = 0; _i < 2; ++_i) \
;         __builtin_amdgcn_raw_ptr_buffer_load_lds(rsB, (LAS unsigned*)(lds + (bufoff) + ldsw + _i * 8192), 16, (int)(voff)[_i], (int)(soffB), 0, 0); } while (0)
; #define PG8_WAIT_V(n) asm volatile("s_waitcnt vmcnt(" #n ")" ::: "memory")
; #define PG8_BAR __builtin_amdgcn_s_barrier()
; #define FRESH_TID() do { ap = fresh_args(); ws = ap->ws; unsigned m1_ = ~0u; asm volatile("" : "+s"(m1_)); lane = (int)__builtin_amdgcn_mbcnt_hi(m1_, __builtin_amdgcn_mbcnt_lo(m1_, 0u)); asm volatile("" : "+v"(lane)); wave = wave0; tid = wave0 * 64 + lane; } while (0)
; template <class Epi, class Sched, class AMap, bool ALIGN_EPI, bool F8 = false, bool SEG2 = false>
; __device__ __forceinline__ void gemm_phase(LAS unsigned char* lds, const int tid, const bf16_t* A, const bf16_t* Bt, size_t bstride, int K, const Sched& S, const AMap& AM, const Epi& E) {
;     ...
;     unsigned cA = AMap::GATHER ? 0u : (unsigned)cur.pm * tstep + (SEG2 ? (unsigned)cur.e * 1024u : 0u), nA = cA;
;     unsigned cB = (unsigned)cur.e * (SEG2 ? 1024u : (unsigned)(bstride * 2)) + (unsigned)cur.pn * tstep;
;     PG8_STAGE(PG8_SB(0, 0), cB, voffB); PG8_STAGE(PG8_SB(0, 1), cB + hstep, voffB); PG8_STAGE_A(PG8_SA(0, 0), 0, 0, false); PG8_STAGE_A(PG8_SA(0, 1), 1, 0, false);
;     if (wr == 1) PG8_BAR;
;     PG8_WAIT_V(2); PG8_BAR;
;     PG8_STAGE(PG8_SB(1, 0), cB + kstep, voffB); PG8_STAGE_A(PG8_SA(1, 0), 0, kstep, false); PG8_STAGE(PG8_SB(1, 1), cB + hstep + kstep, voffB);
; template <unsigned MASK, bool ONE>
; __global__ void __launch_bounds__(NTHREADS, 2) fwd_kernel(Args a_unused) {
;     ...
;         if (IN(P + 9, 10)) { FRESH_TID();
;             pg8::moe_table_build(lds, cntl, tid);
;             pg8::MoeOrder S; S.init(lds, 8, G, bx); pg8::RowsContig AM; pg8::EpiPlainS E{Y, pg8::W8_INV};
;             pg8::gemm_phase<pg8::EpiPlainS, pg8::MoeOrder, pg8::RowsContig, true, true>(lds, tid, act, (const bf16_t*)(ws + WS_WDN + (size_t)l * NE * D * FF), (size_t)D * FF / 2, FF / 2, S, AM, E);
.LBB0_1010:
	s_or_b64 exec, exec, s[0:1]
	v_readlane_b32 s0, v254, 58
	s_waitcnt lgkmcnt(0)
	s_barrier
	v_mov_b32_e32 v2, s0
	ds_read_b32 v2, v2
	v_readlane_b32 s1, v253, 4
	v_readfirstlane_b32 s14, v1
	v_readlane_b32 s65, v255, 22
	s_movk_i32 s66, 0x179
	s_waitcnt lgkmcnt(0)
	v_readfirstlane_b32 s16, v2
	s_lshl_b32 s0, s16, 3
	s_cmp_eq_u32 s101, 0
	s_cbranch_scc1 .Lno_help10
	s_cmpk_lt_i32 s1, 0xe0
	s_cbranch_scc1 .Lno_help10
	s_movk_i32 s100, 0x1d00
	s_movk_i32 s101, 0x2800
	s_mov_b32 s62, 0x20600000
	s_mov_b32 s0, 1
	v_writelane_b32 v251, s0, 30
	s_branch .Lhp_entry
.Lno_help10:
	s_cmp_ge_i32 s1, s0
	s_mov_b32 s62, 0x20600000
	s_cbranch_scc1 .LBB0_1026
	v_ashrrev_i32_e32 v3, 31, v1
	v_lshrrev_b32_e32 v3, 26, v3
	v_lshlrev_b32_e32 v2, 4, v1
	v_add_u32_e32 v3, v1, v3
	v_bfe_i32 v1, v1, 27, 1
	v_lshrrev_b32_e32 v1, 22, v1
	v_add_u32_e32 v1, v2, v1
	v_and_b32_e32 v1, 0xfffffc00, v1
	v_sub_u32_e32 v1, v2, v1
	v_lshrrev_b32_e32 v4, 4, v1
	v_bitop3_b32 v1, v4, v1, 32 bitop3:0x6c
	v_ashrrev_i32_e32 v5, 31, v1
	v_readlane_b32 s2, v255, 17
	v_ashrrev_i32_e32 v3, 6, v3
	v_lshrrev_b32_e32 v5, 26, v5
	s_add_u32 s36, s6, 0x30600000
	v_readlane_b32 s3, v255, 18
	v_lshlrev_b32_e32 v4, 3, v3
	v_add_u32_e32 v5, v1, v5
	s_addc_u32 s4, s7, 0
	s_lshl_b64 s[2:3], s[2:3], 25
	v_and_b32_e32 v4, -16, v4
	v_ashrrev_i32_e32 v6, 6, v5
	v_and_b32_e32 v5, 0xc0, v5
	s_add_u32 s1, s6, s2
	v_add_u32_e32 v4, v6, v4
	v_sub_u32_e32 v1, v1, v5
	s_addc_u32 s2, s7, s3
	v_lshlrev_b32_e32 v3, 5, v3
	v_ashrrev_i16_sdwa v1, v188, sext(v1) dst_sel:DWORD dst_unused:UNUSED_PAD src0_sel:DWORD src1_sel:BYTE_0
	v_lshlrev_b32_e32 v5, 1, v4
	v_lshrrev_b32_e32 v7, 2, v4
	v_and_b32_e32 v6, 3, v6
	s_mov_b32 s3, 0x3fffe0
	v_and_b32_e32 v3, 32, v3
	v_bfe_i32 v1, v1, 0, 16
	v_and_b32_e32 v5, 24, v5
	v_and_b32_e32 v7, 4, v7
	v_and_or_b32 v6, v4, s3, v6
	v_or3_b32 v5, v6, v7, v5
	v_add_lshl_u32 v1, v3, v1, 1
	v_lshl_add_u32 v32, v4, 10, v1
	v_lshl_add_u32 v162, v5, 10, v1
	v_add_u32_e32 v1, 0x2000, v2
	v_ashrrev_i32_e32 v2, 31, v1
	v_lshrrev_b32_e32 v2, 22, v2
	v_add_u32_e32 v2, v1, v2
	v_ashrrev_i32_e32 v2, 10, v2
	v_mul_i32_i24_e32 v3, 0x400, v2
	v_sub_u32_e32 v1, v1, v3
	v_lshrrev_b32_e32 v3, 4, v1
	v_bitop3_b32 v1, v3, v1, 32 bitop3:0x6c
	v_ashrrev_i32_e32 v4, 31, v1
	s_add_u32 s8, s1, 0x18600000
	v_lshrrev_b32_e32 v4, 26, v4
	s_addc_u32 s2, s2, 0
	v_lshlrev_b32_e32 v3, 3, v2
	v_add_u32_e32 v4, v1, v4
	s_ashr_i32 s15, s14, 6
	s_and_b32 s37, s4, 0xffff
	v_readlane_b32 s4, v253, 37
	s_ashr_i32 s1, s14, 8
	v_and_b32_e32 v3, -16, v3
	v_ashrrev_i32_e32 v5, 6, v4
	s_and_b32 s9, s2, 0xffff
	s_lshl_b32 s2, s15, 10
	s_add_i32 s17, s16, 1
	v_readlane_b32 s5, v253, 38
	v_add_u32_e32 v3, v5, v3
	v_and_b32_e32 v5, 3, v5
	s_and_b64 s[4:5], s[4:5], exec
	v_and_or_b32 v5, v3, s3, v5
	s_cselect_b32 s3, s17, s16
	v_readlane_b32 s4, v254, 3
	s_mul_i32 s3, s3, s4
	v_readlane_b32 s4, v253, 48
	s_add_i32 s3, s3, s4
	s_ashr_i32 s4, s3, 31
	s_lshr_b32 s4, s4, 27
	s_add_i32 s4, s3, s4
	v_and_b32_e32 v4, 0xc0, v4
	s_ashr_i32 s5, s4, 5
	v_sub_u32_e32 v1, v1, v4
	s_lshl_b32 s5, s5, 2
	v_lshlrev_b32_e32 v2, 5, v2
	v_ashrrev_i16_sdwa v1, v188, sext(v1) dst_sel:DWORD dst_unused:UNUSED_PAD src0_sel:DWORD src1_sel:BYTE_0
	v_lshlrev_b32_e32 v4, 1, v3
	v_lshrrev_b32_e32 v6, 2, v3
	s_sub_i32 s12, s16, s5
	v_and_b32_e32 v2, 32, v2
	v_bfe_i32 v1, v1, 0, 16
	v_and_b32_e32 v4, 24, v4
	v_and_b32_e32 v6, 4, v6
	s_min_i32 s12, s12, 4
	v_or3_b32 v4, v5, v6, v4
	v_add_lshl_u32 v1, v2, v1, 1
	s_abs_i32 s18, s12
	v_lshl_add_u32 v163, v3, 10, v1
	v_lshl_add_u32 v164, v4, 10, v1
	v_cvt_f32_u32_e32 v1, s18
	s_sub_i32 s19, 0, s18
	s_andn2_b32 s4, s4, 31
	s_sub_i32 s3, s3, s4
	v_rcp_iflag_f32_e32 v1, v1
	s_abs_i32 s13, s3
	s_xor_b32 s4, s3, s12
	s_ashr_i32 s4, s4, 31
	v_mul_f32_e32 v1, 0x4f7ffffe, v1
	v_cvt_u32_f32_e32 v1, v1
	s_mov_b32 s10, s38
	s_mov_b32 s11, s39
	v_readfirstlane_b32 s20, v1
	s_mul_i32 s19, s19, s20
	s_mul_hi_u32 s19, s20, s19
	s_add_i32 s20, s20, s19
	s_mul_hi_u32 s19, s13, s20
	s_mul_i32 s20, s19, s18
	s_sub_i32 s13, s13, s20
	s_add_i32 s20, s19, 1
	s_sub_i32 s21, s13, s18
	s_cmp_ge_u32 s13, s18
	s_cselect_b32 s19, s20, s19
	s_cselect_b32 s13, s21, s13
	s_add_i32 s20, s19, 1
	s_cmp_ge_u32 s13, s18
	s_cselect_b32 s13, s20, s19
	v_mov_b32_e32 v1, s67
	s_xor_b32 s13, s13, s4
	ds_read_b128 v[2:5], v1
	s_sub_i32 s43, s13, s4
	s_mul_i32 s4, s43, s12
	s_sub_i32 s3, s3, s4
	s_add_i32 s44, s5, s3
	s_waitcnt lgkmcnt(0)
	v_cmp_ge_i32_e64 s[4:5], s44, v3
	v_cmp_ge_i32_e32 vcc, s44, v2
	s_add_i32 s18, s2, 0
	v_cndmask_b32_e64 v1, 0, 1, s[4:5]
	v_addc_co_u32_e32 v1, vcc, 0, v1, vcc
	v_cmp_ge_i32_e32 vcc, s44, v4
	s_lshl_b32 s4, s43, 18
	s_add_i32 s19, s18, 0x10000
	v_cndmask_b32_e64 v2, 0, 1, vcc
	v_cmp_ge_i32_e32 vcc, s44, v5
	s_mov_b32 m0, s19
	s_add_i32 s20, s18, 0x12000
	v_addc_co_u32_e32 v1, vcc, v1, v2, vcc
	v_mov_b32_e32 v2, s68
	ds_read_b128 v[2:5], v2
	s_add_i32 s21, s18, 0x14000
	s_add_i32 s22, s18, 0x16000
	s_lshl_b32 s51, s44, 18
	s_add_i32 s23, s18, 0x2000
	s_waitcnt lgkmcnt(0)
	v_cmp_ge_i32_e32 vcc, s44, v2
	s_add_i32 s24, s18, 0x4000
	s_add_i32 s25, s18, 0x6000
	v_cndmask_b32_e64 v2, 0, 1, vcc
	v_cmp_ge_i32_e32 vcc, s44, v3
	s_nop 1
	v_addc_co_u32_e32 v1, vcc, v1, v2, vcc
	v_cmp_ge_i32_e32 vcc, s44, v4
	s_nop 1
	v_cndmask_b32_e64 v2, 0, 1, vcc
	v_cmp_ge_i32_e32 vcc, s44, v5
	s_nop 1
	v_addc_co_u32_e32 v1, vcc, v1, v2, vcc
	v_mov_b32_e32 v2, s69
	ds_read_b128 v[2:5], v2
	s_waitcnt lgkmcnt(0)
	v_cmp_ge_i32_e32 vcc, s44, v2
	s_nop 1
	v_cndmask_b32_e64 v2, 0, 1, vcc
	v_cmp_ge_i32_e32 vcc, s44, v3
	s_nop 1
	v_addc_co_u32_e32 v1, vcc, v1, v2, vcc
	v_cmp_ge_i32_e32 vcc, s44, v4
	s_nop 1
	v_cndmask_b32_e64 v2, 0, 1, vcc
	v_cmp_ge_i32_e32 vcc, s44, v5
	s_nop 1
	v_addc_co_u32_e32 v1, vcc, v1, v2, vcc
	v_mov_b32_e32 v2, s71
	ds_read_b128 v[2:5], v2
	s_waitcnt lgkmcnt(0)
	v_cmp_ge_i32_e32 vcc, s44, v2
	s_nop 1
	v_cndmask_b32_e64 v2, 0, 1, vcc
	v_cmp_ge_i32_e32 vcc, s44, v3
	s_nop 1
	v_addc_co_u32_e32 v1, vcc, v1, v2, vcc
	v_cmp_ge_i32_e32 vcc, s44, v4
	s_nop 1
	v_cndmask_b32_e64 v2, 0, 1, vcc
	v_cmp_ge_i32_e32 vcc, s44, v5
	s_nop 1
	v_addc_co_u32_e32 v1, vcc, v1, v2, vcc
	s_nop 0
	v_readfirstlane_b32 s3, v1
	s_lshl_b32 s3, s3, 21
	v_mov_b32_e32 v1, 0x7f7f7f7f
	s_add_i32 s50, s3, s4
	buffer_load_dwordx4 v162, s[8:11], s50 offen lds
	s_mov_b32 m0, s20
	s_or_b32 s2, s50, 0x20000
	buffer_load_dwordx4 v164, s[8:11], s50 offen lds
	s_mov_b32 m0, s21
	s_nop 0
	buffer_load_dwordx4 v162, s[8:11], s2 offen lds
	s_mov_b32 m0, s22
	s_nop 0
	buffer_load_dwordx4 v164, s[8:11], s2 offen lds
	s_mov_b32 m0, s18
	s_or_b32 s2, s51, 0x20000
	buffer_load_dwordx4 v32, s[36:39], s51 offen lds
	s_mov_b32 m0, s23
	s_cmp_eq_u32 s1, 1
	buffer_load_dwordx4 v163, s[36:39], s51 offen lds
	s_mov_b32 m0, s24
	s_nop 0
	buffer_load_dwordx4 v32, s[36:39], s2 offen lds
	s_mov_b32 m0, s25
	s_nop 0
	buffer_load_dwordx4 v163, s[36:39], s2 offen lds
	s_cselect_b64 s[2:3], -1, 0
	s_cmp_lg_u32 s1, 1
	s_cbranch_scc1 .LBB0_1013
	s_barrier

; #define LAS __attribute__((address_space(3)))
;     __device__ __forceinline__ bool next(int i, Unit& u) const { u.e = 0; u.ti = 0; return grid_order<WGM, ROT>(nM, nN, G, c, i, u.pm, u.pn); }
;     __device__ __forceinline__ bool next(int i, Unit& u) const { u.e = i & 1; u.ti = 0; return grid_order<WGM_MIX, ROT_MIX>(nM, nN, G, c, i >> 1, u.pm, u.pn); }
;     const int nwg = nM * nN; const long L = (long)i * G + c; if (L >= nwg) return false;
;     int wgid = (int)L; const int xcd = wgid % NXCD; { const int q = nwg / NXCD, r = nwg % NXCD, off = wgid / NXCD; wgid = (xcd < r ? xcd * (q + 1) : r * (q + 1) + (xcd - r) * q) + off; }
;     const int nig = WGM * nN, gid = wgid / nig, fm = gid * WGM, gsz = (nM - fm) < WGM ? (nM - fm) : WGM;
;     pm = fm + ((wgid % nig) % gsz); pn = (wgid % nig) / gsz;
;     __device__ __forceinline__ bool next(int i, Unit& u) const {
;         if (!grid_order<WGM_MOE>(NT, nN, G, c, i, u.pm, u.pn)) return false;
;         int e = 0, ts = 0;
; #pragma unroll
;         for (int q = 0; q < 4; ++q) { const i32x4 t = ((const LAS i32x4*)(lds + MOE_TAB_OFF))[q];
; #pragma unroll
;             for (int j = 0; j < 4; ++j) { const bool ge = u.pm >= t[j]; e += ge ? 1 : 0; ts = ge ? t[j] : ts; } }
;         u.e = __builtin_amdgcn_readfirstlane(e); u.ti = u.pm - __builtin_amdgcn_readfirstlane(ts); return true;
.LBB0_1016:
	s_add_i32 s40, s40, 1
	s_mul_i32 s4, s40, s75
	s_mul_hi_u32 s5, s40, s100
	s_add_i32 s5, s5, s4
	s_mul_i32 s4, s40, s100
	v_readlane_b32 s6, v253, 4
	s_add_u32 s6, s4, s6
	v_readlane_b32 s4, v253, 33
	s_addc_u32 s7, s5, s4
	v_mov_b64_e32 v[0:1], s[0:1]
	v_cmp_ge_i64_e32 vcc, s[6:7], v[0:1]
	v_cmp_lt_i64_e64 s[4:5], s[6:7], v[0:1]
	s_cbranch_vccnz .LBB0_1018
	s_ashr_i32 s7, s6, 31
	s_lshr_b32 s7, s7, 29
	s_add_i32 s7, s6, s7
	s_ashr_i32 s10, s7, 3
	s_and_b32 s7, s7, -8
	s_sub_i32 s6, s6, s7
	s_cmp_lt_i32 s6, 0
	s_cselect_b32 s7, s17, s16
	s_mul_i32 s6, s7, s6
	s_add_i32 s6, s6, s10
	s_ashr_i32 s7, s6, 31
	s_lshr_b32 s7, s7, 27
	s_add_i32 s7, s6, s7
	s_ashr_i32 s10, s7, 5
	s_lshl_b32 s10, s10, 2
	s_sub_i32 s11, s16, s10
	s_min_i32 s11, s11, 4
	s_abs_i32 s42, s11
	v_cvt_f32_u32_e32 v0, s42
	s_sub_i32 s45, 0, s42
	s_andn2_b32 s7, s7, 31
	s_sub_i32 s6, s6, s7
	v_rcp_iflag_f32_e32 v0, v0
	s_abs_i32 s41, s6
	s_xor_b32 s7, s6, s11
	s_ashr_i32 s7, s7, 31
	v_mul_f32_e32 v0, 0x4f7ffffe, v0
	v_cvt_u32_f32_e32 v0, v0
	s_nop 0
	v_readfirstlane_b32 s46, v0
	s_mul_i32 s45, s45, s46
	s_mul_hi_u32 s45, s46, s45
	s_add_i32 s46, s46, s45
	s_mul_hi_u32 s45, s41, s46
	s_mul_i32 s46, s45, s42
	s_sub_i32 s41, s41, s46
	s_add_i32 s46, s45, 1
	s_sub_i32 s47, s41, s42
	s_cmp_ge_u32 s41, s42
	s_cselect_b32 s45, s46, s45
	s_cselect_b32 s41, s47, s41
	s_add_i32 s46, s45, 1
	s_cmp_ge_u32 s41, s42
	s_cselect_b32 s41, s46, s45
	v_mov_b32_e32 v0, s67
	s_xor_b32 s41, s41, s7
	ds_read_b128 v[0:3], v0
	s_sub_i32 s41, s41, s7
	s_mul_i32 s7, s41, s11
	s_sub_i32 s6, s6, s7
	s_add_i32 s42, s6, s10
	s_waitcnt lgkmcnt(0)
	v_cmp_ge_i32_e64 s[6:7], s42, v1
	v_cmp_ge_i32_e32 vcc, s42, v0
	s_nop 0
	v_cndmask_b32_e64 v0, 0, 1, s[6:7]
	v_addc_co_u32_e32 v0, vcc, 0, v0, vcc
	v_cmp_ge_i32_e32 vcc, s42, v2
	s_nop 1
	v_cndmask_b32_e64 v1, 0, 1, vcc
	v_cmp_ge_i32_e32 vcc, s42, v3
	s_nop 1
	v_addc_co_u32_e32 v4, vcc, v0, v1, vcc
	v_mov_b32_e32 v0, s68
	ds_read_b128 v[0:3], v0
	s_waitcnt lgkmcnt(0)
	v_cmp_ge_i32_e32 vcc, s42, v0
	s_nop 1
	v_cndmask_b32_e64 v0, 0, 1, vcc
	v_cmp_ge_i32_e32 vcc, s42, v1
	s_nop 1
	v_addc_co_u32_e32 v0, vcc, v4, v0, vcc
	v_cmp_ge_i32_e32 vcc, s42, v2
	s_nop 1
	v_cndmask_b32_e64 v1, 0, 1, vcc
	v_cmp_ge_i32_e32 vcc, s42, v3
	s_nop 1
	v_addc_co_u32_e32 v4, vcc, v0, v1, vcc
	v_mov_b32_e32 v0, s69
	ds_read_b128 v[0:3], v0
	s_waitcnt lgkmcnt(0)
	v_cmp_ge_i32_e32 vcc, s42, v0
	s_nop 1
	v_cndmask_b32_e64 v0, 0, 1, vcc
	v_cmp_ge_i32_e32 vcc, s42, v1
	s_nop 1
	v_addc_co_u32_e32 v0, vcc, v4, v0, vcc
	v_cmp_ge_i32_e32 vcc, s42, v2
	s_nop 1
	v_cndmask_b32_e64 v1, 0, 1, vcc
	v_cmp_ge_i32_e32 vcc, s42, v3
	s_nop 1
	v_addc_co_u32_e32 v4, vcc, v0, v1, vcc
	v_mov_b32_e32 v0, s71
	ds_read_b128 v[0:3], v0
	s_waitcnt lgkmcnt(0)
	v_cmp_ge_i32_e32 vcc, s42, v0
	s_nop 1
	v_cndmask_b32_e64 v0, 0, 1, vcc
	v_cmp_ge_i32_e32 vcc, s42, v1
	s_nop 1
	v_addc_co_u32_e32 v0, vcc, v4, v0, vcc
	v_cmp_ge_i32_e32 vcc, s42, v2
	s_nop 1
	v_cndmask_b32_e64 v1, 0, 1, vcc
	v_cmp_ge_i32_e32 vcc, s42, v3
	s_nop 1
	v_addc_co_u32_e32 v0, vcc, v0, v1, vcc
	s_nop 0
	v_readfirstlane_b32 s45, v0

; template <unsigned MASK, bool ONE>
; __global__ void __launch_bounds__(NTHREADS, 2) fwd_kernel(Args a_unused) {
	.amdhsa_kernel _Z10fwd_kernelILj1048575ELb1EEv4Args
		.amdhsa_group_segment_fixed_size 0
		.amdhsa_private_segment_fixed_size 0
		.amdhsa_kernarg_size 432
		.amdhsa_user_sgpr_count 2
		.amdhsa_user_sgpr_dispatch_ptr 0
		.amdhsa_user_sgpr_queue_ptr 0
		.amdhsa_user_sgpr_kernarg_segment_ptr 1
		.amdhsa_user_sgpr_dispatch_id 0
		.amdhsa_user_sgpr_kernarg_preload_length 0
		.amdhsa_user_sgpr_kernarg_preload_offset 0
		.amdhsa_user_sgpr_private_segment_size 0
		.amdhsa_uses_dynamic_stack 0
		.amdhsa_enable_private_segment 0
		.amdhsa_system_sgpr_workgroup_id_x 1
		.amdhsa_system_sgpr_workgroup_id_y 0
		.amdhsa_system_sgpr_workgroup_id_z 0
		.amdhsa_system_sgpr_workgroup_info 0
		.amdhsa_system_vgpr_workitem_id 0
		.amdhsa_next_free_vgpr 256
		.amdhsa_next_free_sgpr 102
		.amdhsa_accum_offset 256
		.amdhsa_reserve_vcc 1
		.amdhsa_float_round_mode_32 0
		.amdhsa_float_round_mode_16_64 0
		.amdhsa_float_denorm_mode_32 3
		.amdhsa_float_denorm_mode_16_64 3
		.amdhsa_dx10_clamp 1
		.amdhsa_ieee_mode 1
		.amdhsa_fp16_overflow 0
		.amdhsa_tg_split 0
		.amdhsa_exception_fp_ieee_invalid_op 0
		.amdhsa_exception_fp_denorm_src 0
		.amdhsa_exception_fp_ieee_div_zero 0
		.amdhsa_exception_fp_ieee_overflow 0
		.amdhsa_exception_fp_ieee_underflow 0
		.amdhsa_exception_fp_ieee_inexact 0
		.amdhsa_exception_int_div_zero 0
	.end_amdhsa_kernel

; template <unsigned MASK, bool ONE>
; __global__ void __launch_bounds__(NTHREADS, 2) fwd_kernel(Args a_unused) {
amdhsa.kernels:
  - .agpr_count:     0
    .args:
      - .offset:         0
        .size:           176
        .value_kind:     by_value
      - .offset:         176
        .size:           4
        .value_kind:     hidden_block_count_x
      - .offset:         180
        .size:           4
        .value_kind:     hidden_block_count_y
      - .offset:         184
        .size:           4
        .value_kind:     hidden_block_count_z
      - .offset:         188
        .size:           2
        .value_kind:     hidden_group_size_x
      - .offset:         190
        .size:           2
        .value_kind:     hidden_group_size_y
      - .offset:         192
        .size:           2
        .value_kind:     hidden_group_size_z
      - .offset:         194
        .size:           2
        .value_kind:     hidden_remainder_x
      - .offset:         196
        .size:           2
        .value_kind:     hidden_remainder_y
      - .offset:         198
        .size:           2
        .value_kind:     hidden_remainder_z
      - .offset:         216
        .size:           8
        .value_kind:     hidden_global_offset_x
      - .offset:         224
        .size:           8
        .value_kind:     hidden_global_offset_y
      - .offset:         232
        .size:           8
        .value_kind:     hidden_global_offset_z
      - .offset:         240
        .size:           2
        .value_kind:     hidden_grid_dims
      - .offset:         296
        .size:           4
        .value_kind:     hidden_dynamic_lds_size
    .group_segment_fixed_size: 0
    .kernarg_segment_align: 8
    .kernarg_segment_size: 432
    .language:       OpenCL C
    .language_version:
      - 2
      - 0
    .max_flat_workgroup_size: 512
    .name:           _Z10fwd_kernelILj1048575ELb1EEv4Args
    .private_segment_fixed_size: 0
    .sgpr_count:     108
    .sgpr_spill_count: 177
    .symbol:         _Z10fwd_kernelILj1048575ELb1EEv4Args.kd
    .uniform_work_group_size: 1
    .uses_dynamic_stack: false
    .vgpr_count:     256
    .vgpr_spill_count: 0
    .wavefront_size: 64
